# P6 pool-merge epilogue loads pipelined in a VGPR ring; P3 KV row scales hoisted; paired accumulator zeroing
# speedup vs baseline: 1.0058x; 1.0058x over previous
; template <bool FP8 = false, class Epi, class Sched>
; __device__ __forceinline__ void gemm_phase(LAS unsigned char* lds, const int K, const int lda, const int ldb, const Sched& S, const Epi& E, const int wid) {
;     ...
; #pragma unroll
;         for (int a = 0; a < 2; ++a)
; #pragma unroll
;             for (int b = 0; b < 2; ++b)
; #pragma unroll
;                 for (int m = 0; m < 4; ++m)
; #pragma unroll
;                     for (int n = 0; n < 2; ++n) acc[a][b][m][n] = (f32x4){0.f, 0.f, 0.f, 0.f};
.LBB0_117:
	s_add_u32 s25, s50, 0x100
	v_mov_b32_e32 v0, 0
	s_addc_u32 s71, s51, 0
	s_mov_b32 s72, -2
	v_mov_b32_e32 v1, v0
	v_mov_b64_e32 v[2:3], 0
	v_mov_b64_e32 v[4:5], 0
	v_mov_b64_e32 v[6:7], 0
	v_mov_b64_e32 v[16:17], 0
	v_mov_b64_e32 v[18:19], 0
	v_mov_b64_e32 v[20:21], 0
	v_mov_b64_e32 v[22:23], 0
	v_mov_b64_e32 v[32:33], 0
	v_mov_b64_e32 v[34:35], 0
	v_mov_b64_e32 v[36:37], 0
	v_mov_b64_e32 v[38:39], 0
	v_mov_b64_e32 v[48:49], 0
	v_mov_b64_e32 v[50:51], 0
	v_mov_b64_e32 v[52:53], 0
	v_mov_b64_e32 v[54:55], 0
	v_mov_b64_e32 v[8:9], 0
	v_mov_b64_e32 v[10:11], 0
	v_mov_b64_e32 v[12:13], 0
	v_mov_b64_e32 v[14:15], 0
	v_mov_b64_e32 v[24:25], 0
	v_mov_b64_e32 v[26:27], 0
	v_mov_b64_e32 v[28:29], 0
	v_mov_b64_e32 v[30:31], 0
	v_mov_b64_e32 v[40:41], 0
	v_mov_b64_e32 v[42:43], 0
	v_mov_b64_e32 v[44:45], 0
	v_mov_b64_e32 v[46:47], 0
	v_mov_b64_e32 v[56:57], 0
	v_mov_b64_e32 v[58:59], 0
	v_mov_b64_e32 v[60:61], 0
	v_mov_b64_e32 v[62:63], 0
	v_mov_b64_e32 v[64:65], 0
	v_mov_b64_e32 v[66:67], 0
	v_mov_b64_e32 v[68:69], 0
	v_mov_b64_e32 v[70:71], 0
	v_mov_b64_e32 v[80:81], 0
	v_mov_b64_e32 v[82:83], 0
	v_mov_b64_e32 v[84:85], 0
	v_mov_b64_e32 v[86:87], 0
	v_mov_b64_e32 v[96:97], 0
	v_mov_b64_e32 v[98:99], 0
	v_mov_b64_e32 v[100:101], 0
	v_mov_b64_e32 v[102:103], 0
	v_mov_b64_e32 v[112:113], 0
	v_mov_b64_e32 v[114:115], 0
	v_mov_b64_e32 v[116:117], 0
	v_mov_b64_e32 v[118:119], 0
	v_mov_b64_e32 v[72:73], 0
	v_mov_b32_e32 v74, v0
	v_mov_b32_e32 v75, v0
	v_mov_b32_e32 v76, v0
	v_mov_b32_e32 v77, v0
	v_mov_b32_e32 v78, v0
	v_mov_b32_e32 v79, v0
	v_mov_b32_e32 v88, v0
	v_mov_b32_e32 v89, v0
	v_mov_b32_e32 v90, v0
	v_mov_b32_e32 v91, v0
	v_mov_b32_e32 v92, v0
	v_mov_b32_e32 v93, v0
	v_mov_b32_e32 v94, v0
	v_mov_b32_e32 v95, v0
	v_mov_b32_e32 v104, v0
	v_mov_b32_e32 v105, v0
	v_mov_b32_e32 v106, v0
	v_mov_b32_e32 v107, v0
	v_mov_b32_e32 v108, v0
	v_mov_b32_e32 v109, v0
	v_mov_b32_e32 v110, v0
	v_mov_b32_e32 v111, v0
	v_mov_b32_e32 v120, v0
	v_mov_b32_e32 v121, v0
	v_mov_b32_e32 v122, v0
	v_mov_b32_e32 v123, v0
	v_mov_b32_e32 v124, v0
	v_mov_b32_e32 v125, v0
	v_mov_b32_e32 v126, v0
	v_mov_b32_e32 v127, v0

; template <bool FP8 = false, class Epi, class Sched>
; __device__ __forceinline__ void gemm_phase(LAS unsigned char* lds, const int K, const int lda, const int ldb, const Sched& S, const Epi& E, const int wid) {
;     ...
; #pragma unroll
;         for (int a = 0; a < 2; ++a)
; #pragma unroll
;             for (int b = 0; b < 2; ++b)
; #pragma unroll
;                 for (int m = 0; m < 4; ++m)
; #pragma unroll
;                     for (int n = 0; n < 2; ++n) acc[a][b][m][n] = (f32x4){0.f, 0.f, 0.f, 0.f};
.LBB0_141:
	s_add_u32 s47, s56, 0x100
	v_mov_b32_e32 v0, 0
	s_addc_u32 s76, s57, 0
	s_mov_b32 s77, -2
	v_mov_b32_e32 v1, v0
	v_mov_b64_e32 v[2:3], 0
	v_mov_b64_e32 v[4:5], 0
	v_mov_b64_e32 v[6:7], 0
	v_mov_b64_e32 v[12:13], 0
	v_mov_b64_e32 v[14:15], 0
	v_mov_b64_e32 v[20:21], 0
	v_mov_b64_e32 v[22:23], 0
	v_mov_b64_e32 v[28:29], 0
	v_mov_b64_e32 v[30:31], 0
	v_mov_b64_e32 v[36:37], 0
	v_mov_b64_e32 v[38:39], 0
	v_mov_b64_e32 v[44:45], 0
	v_mov_b64_e32 v[46:47], 0
	v_mov_b64_e32 v[52:53], 0
	v_mov_b64_e32 v[54:55], 0
	v_mov_b64_e32 v[8:9], 0
	v_mov_b64_e32 v[10:11], 0
	v_mov_b64_e32 v[16:17], 0
	v_mov_b64_e32 v[18:19], 0
	v_mov_b64_e32 v[24:25], 0
	v_mov_b64_e32 v[26:27], 0
	v_mov_b64_e32 v[32:33], 0
	v_mov_b64_e32 v[34:35], 0
	v_mov_b64_e32 v[40:41], 0
	v_mov_b64_e32 v[42:43], 0
	v_mov_b64_e32 v[48:49], 0
	v_mov_b64_e32 v[50:51], 0
	v_mov_b64_e32 v[56:57], 0
	v_mov_b64_e32 v[58:59], 0
	v_mov_b64_e32 v[60:61], 0
	v_mov_b64_e32 v[62:63], 0
	v_mov_b64_e32 v[64:65], 0
	v_mov_b64_e32 v[66:67], 0
	v_mov_b64_e32 v[68:69], 0
	v_mov_b64_e32 v[70:71], 0
	v_mov_b64_e32 v[80:81], 0
	v_mov_b64_e32 v[82:83], 0
	v_mov_b64_e32 v[84:85], 0
	v_mov_b64_e32 v[86:87], 0
	v_mov_b64_e32 v[96:97], 0
	v_mov_b64_e32 v[98:99], 0
	v_mov_b64_e32 v[100:101], 0
	v_mov_b64_e32 v[102:103], 0
	v_mov_b64_e32 v[112:113], 0
	v_mov_b64_e32 v[114:115], 0
	v_mov_b64_e32 v[116:117], 0
	v_mov_b64_e32 v[118:119], 0
	v_mov_b64_e32 v[72:73], 0
	v_mov_b32_e32 v74, v0
	v_mov_b32_e32 v75, v0
	v_mov_b32_e32 v76, v0
	v_mov_b32_e32 v77, v0
	v_mov_b32_e32 v78, v0
	v_mov_b32_e32 v79, v0
	v_mov_b32_e32 v88, v0
	v_mov_b32_e32 v89, v0
	v_mov_b32_e32 v90, v0
	v_mov_b32_e32 v91, v0
	v_mov_b32_e32 v92, v0
	v_mov_b32_e32 v93, v0
	v_mov_b32_e32 v94, v0
	v_mov_b32_e32 v95, v0
	v_mov_b32_e32 v104, v0
	v_mov_b32_e32 v105, v0
	v_mov_b32_e32 v106, v0
	v_mov_b32_e32 v107, v0
	v_mov_b32_e32 v108, v0
	v_mov_b32_e32 v109, v0
	v_mov_b32_e32 v110, v0
	v_mov_b32_e32 v111, v0
	v_mov_b32_e32 v120, v0
	v_mov_b32_e32 v121, v0
	v_mov_b32_e32 v122, v0
	v_mov_b32_e32 v123, v0
	v_mov_b32_e32 v124, v0
	v_mov_b32_e32 v125, v0
	v_mov_b32_e32 v126, v0
	v_mov_b32_e32 v127, v0

; template <bool FP8 = false, class Epi, class Sched>
; __device__ __forceinline__ void gemm_phase(LAS unsigned char* lds, const int K, const int lda, const int ldb, const Sched& S, const Epi& E, const int wid) {
;     ...
; #pragma unroll
;         for (int a = 0; a < 2; ++a)
; #pragma unroll
;             for (int b = 0; b < 2; ++b)
; #pragma unroll
;                 for (int m = 0; m < 4; ++m)
; #pragma unroll
;                     for (int n = 0; n < 2; ++n) acc[a][b][m][n] = (f32x4){0.f, 0.f, 0.f, 0.f};
.LBB0_165:
	s_add_u32 s13, s46, 0x100
	v_mov_b32_e32 v0, 0
	s_addc_u32 s64, s47, 0
	s_mov_b32 s65, -2
	v_mov_b32_e32 v1, v0
	v_mov_b64_e32 v[2:3], 0
	v_mov_b64_e32 v[4:5], 0
	v_mov_b64_e32 v[6:7], 0
	v_mov_b64_e32 v[8:9], 0
	v_mov_b64_e32 v[10:11], 0
	v_mov_b64_e32 v[16:17], 0
	v_mov_b64_e32 v[18:19], 0
	v_mov_b64_e32 v[24:25], 0
	v_mov_b64_e32 v[26:27], 0
	v_mov_b64_e32 v[32:33], 0
	v_mov_b64_e32 v[34:35], 0
	v_mov_b64_e32 v[40:41], 0
	v_mov_b64_e32 v[42:43], 0
	v_mov_b64_e32 v[48:49], 0
	v_mov_b64_e32 v[50:51], 0
	v_mov_b64_e32 v[12:13], 0
	v_mov_b64_e32 v[14:15], 0
	v_mov_b64_e32 v[20:21], 0
	v_mov_b64_e32 v[22:23], 0
	v_mov_b64_e32 v[28:29], 0
	v_mov_b64_e32 v[30:31], 0
	v_mov_b64_e32 v[36:37], 0
	v_mov_b64_e32 v[38:39], 0
	v_mov_b64_e32 v[44:45], 0
	v_mov_b64_e32 v[46:47], 0
	v_mov_b64_e32 v[52:53], 0
	v_mov_b64_e32 v[54:55], 0
	v_mov_b64_e32 v[56:57], 0
	v_mov_b64_e32 v[58:59], 0
	v_mov_b64_e32 v[60:61], 0
	v_mov_b64_e32 v[62:63], 0
	v_mov_b64_e32 v[64:65], 0
	v_mov_b64_e32 v[66:67], 0
	v_mov_b64_e32 v[68:69], 0
	v_mov_b64_e32 v[70:71], 0
	v_mov_b64_e32 v[72:73], 0
	v_mov_b64_e32 v[74:75], 0
	v_mov_b64_e32 v[80:81], 0
	v_mov_b64_e32 v[82:83], 0
	v_mov_b64_e32 v[88:89], 0
	v_mov_b64_e32 v[90:91], 0
	v_mov_b64_e32 v[96:97], 0
	v_mov_b64_e32 v[98:99], 0
	v_mov_b64_e32 v[104:105], 0
	v_mov_b64_e32 v[106:107], 0
	v_mov_b64_e32 v[112:113], 0
	v_mov_b64_e32 v[114:115], 0
	v_mov_b64_e32 v[76:77], 0
	v_mov_b32_e32 v78, v0
	v_mov_b32_e32 v79, v0
	v_mov_b32_e32 v84, v0
	v_mov_b32_e32 v85, v0
	v_mov_b32_e32 v86, v0
	v_mov_b32_e32 v87, v0
	v_mov_b32_e32 v92, v0
	v_mov_b32_e32 v93, v0
	v_mov_b32_e32 v94, v0
	v_mov_b32_e32 v95, v0
	v_mov_b32_e32 v100, v0
	v_mov_b32_e32 v101, v0
	v_mov_b32_e32 v102, v0
	v_mov_b32_e32 v103, v0
	v_mov_b32_e32 v108, v0
	v_mov_b32_e32 v109, v0
	v_mov_b32_e32 v110, v0
	v_mov_b32_e32 v111, v0
	v_mov_b32_e32 v116, v0
	v_mov_b32_e32 v117, v0
	v_mov_b32_e32 v118, v0
	v_mov_b32_e32 v119, v0
	v_mov_b32_e32 v120, v0
	v_mov_b32_e32 v121, v0
	v_mov_b32_e32 v122, v0
	v_mov_b32_e32 v123, v0
	v_mov_b32_e32 v124, v0
	v_mov_b32_e32 v125, v0
	v_mov_b32_e32 v126, v0
	v_mov_b32_e32 v127, v0

; template <bool FP8 = false, class Epi, class Sched>
; __device__ __forceinline__ void gemm_phase(LAS unsigned char* lds, const int K, const int lda, const int ldb, const Sched& S, const Epi& E, const int wid) {
;     ...
; #pragma unroll
;         for (int a = 0; a < 2; ++a)
; #pragma unroll
;             for (int b = 0; b < 2; ++b)
; #pragma unroll
;                 for (int m = 0; m < 4; ++m)
; #pragma unroll
;                     for (int n = 0; n < 2; ++n) acc[a][b][m][n] = (f32x4){0.f, 0.f, 0.f, 0.f};
.LBB0_370:
	v_mov_b32_e32 v0, 0
	s_mov_b64 s[58:59], 0
	s_mov_b64 s[56:57], -1
	s_mov_b64 s[60:61], 0
	v_mov_b32_e32 v1, v0
	v_mov_b64_e32 v[2:3], 0
	v_mov_b64_e32 v[4:5], 0
	v_mov_b64_e32 v[6:7], 0
	v_mov_b64_e32 v[16:17], 0
	v_mov_b64_e32 v[18:19], 0
	v_mov_b64_e32 v[20:21], 0
	v_mov_b64_e32 v[22:23], 0
	v_mov_b64_e32 v[32:33], 0
	v_mov_b64_e32 v[34:35], 0
	v_mov_b64_e32 v[36:37], 0
	v_mov_b64_e32 v[38:39], 0
	v_mov_b64_e32 v[48:49], 0
	v_mov_b64_e32 v[50:51], 0
	v_mov_b64_e32 v[52:53], 0
	v_mov_b64_e32 v[54:55], 0
	v_mov_b64_e32 v[8:9], 0
	v_mov_b64_e32 v[10:11], 0
	v_mov_b64_e32 v[12:13], 0
	v_mov_b64_e32 v[14:15], 0
	v_mov_b64_e32 v[24:25], 0
	v_mov_b64_e32 v[26:27], 0
	v_mov_b64_e32 v[28:29], 0
	v_mov_b64_e32 v[30:31], 0
	v_mov_b64_e32 v[40:41], 0
	v_mov_b64_e32 v[42:43], 0
	v_mov_b64_e32 v[44:45], 0
	v_mov_b64_e32 v[46:47], 0
	v_mov_b64_e32 v[56:57], 0
	v_mov_b64_e32 v[58:59], 0
	v_mov_b64_e32 v[60:61], 0
	v_mov_b64_e32 v[62:63], 0
	v_mov_b64_e32 v[64:65], 0
	v_mov_b64_e32 v[66:67], 0
	v_mov_b64_e32 v[68:69], 0
	v_mov_b64_e32 v[70:71], 0
	v_mov_b64_e32 v[80:81], 0
	v_mov_b64_e32 v[82:83], 0
	v_mov_b64_e32 v[84:85], 0
	v_mov_b64_e32 v[86:87], 0
	v_mov_b64_e32 v[96:97], 0
	v_mov_b64_e32 v[98:99], 0
	v_mov_b64_e32 v[100:101], 0
	v_mov_b64_e32 v[102:103], 0
	v_mov_b64_e32 v[112:113], 0
	v_mov_b64_e32 v[114:115], 0
	v_mov_b64_e32 v[116:117], 0
	v_mov_b64_e32 v[118:119], 0
	v_mov_b64_e32 v[72:73], 0
	v_mov_b32_e32 v74, v0
	v_mov_b32_e32 v75, v0
	v_mov_b32_e32 v76, v0
	v_mov_b32_e32 v77, v0
	v_mov_b32_e32 v78, v0
	v_mov_b32_e32 v79, v0
	v_mov_b32_e32 v88, v0
	v_mov_b32_e32 v89, v0
	v_mov_b32_e32 v90, v0
	v_mov_b32_e32 v91, v0
	v_mov_b32_e32 v92, v0
	v_mov_b32_e32 v93, v0
	v_mov_b32_e32 v94, v0
	v_mov_b32_e32 v95, v0
	v_mov_b32_e32 v104, v0
	v_mov_b32_e32 v105, v0
	v_mov_b32_e32 v106, v0
	v_mov_b32_e32 v107, v0
	v_mov_b32_e32 v108, v0
	v_mov_b32_e32 v109, v0
	v_mov_b32_e32 v110, v0
	v_mov_b32_e32 v111, v0
	v_mov_b32_e32 v120, v0
	v_mov_b32_e32 v121, v0
	v_mov_b32_e32 v122, v0
	v_mov_b32_e32 v123, v0
	v_mov_b32_e32 v124, v0
	v_mov_b32_e32 v125, v0
	v_mov_b32_e32 v126, v0
	v_mov_b32_e32 v127, v0

; template <bool FP8 = false, class Epi, class Sched>
; __device__ __forceinline__ void gemm_phase(LAS unsigned char* lds, const int K, const int lda, const int ldb, const Sched& S, const Epi& E, const int wid) {
;     ...
; #pragma unroll
;         for (int a = 0; a < 2; ++a)
; #pragma unroll
;             for (int b = 0; b < 2; ++b)
; #pragma unroll
;                 for (int m = 0; m < 4; ++m)
; #pragma unroll
;                     for (int n = 0; n < 2; ++n) acc[a][b][m][n] = (f32x4){0.f, 0.f, 0.f, 0.f};
.LBB0_397:
	v_mov_b32_e32 v0, 0
	s_mov_b64 s[62:63], 0
	s_mov_b64 s[4:5], -1
	s_mov_b64 s[64:65], 0
	v_mov_b32_e32 v1, v0
	v_mov_b64_e32 v[2:3], 0
	v_mov_b64_e32 v[16:17], 0
	v_mov_b64_e32 v[18:19], 0
	v_mov_b64_e32 v[4:5], 0
	v_mov_b64_e32 v[6:7], 0
	v_mov_b64_e32 v[20:21], 0
	v_mov_b64_e32 v[22:23], 0
	v_mov_b64_e32 v[8:9], 0
	v_mov_b64_e32 v[10:11], 0
	v_mov_b64_e32 v[24:25], 0
	v_mov_b64_e32 v[26:27], 0
	v_mov_b64_e32 v[12:13], 0
	v_mov_b64_e32 v[14:15], 0
	v_mov_b64_e32 v[28:29], 0
	v_mov_b64_e32 v[30:31], 0
	v_mov_b64_e32 v[64:65], 0
	v_mov_b64_e32 v[66:67], 0
	v_mov_b64_e32 v[68:69], 0
	v_mov_b64_e32 v[70:71], 0
	v_mov_b64_e32 v[72:73], 0
	v_mov_b64_e32 v[74:75], 0
	v_mov_b64_e32 v[76:77], 0
	v_mov_b64_e32 v[78:79], 0
	v_mov_b64_e32 v[80:81], 0
	v_mov_b64_e32 v[82:83], 0
	v_mov_b64_e32 v[84:85], 0
	v_mov_b64_e32 v[86:87], 0
	v_mov_b64_e32 v[88:89], 0
	v_mov_b64_e32 v[90:91], 0
	v_mov_b64_e32 v[92:93], 0
	v_mov_b64_e32 v[94:95], 0
	v_mov_b64_e32 v[32:33], 0
	v_mov_b64_e32 v[34:35], 0
	v_mov_b64_e32 v[48:49], 0
	v_mov_b64_e32 v[50:51], 0
	v_mov_b64_e32 v[36:37], 0
	v_mov_b64_e32 v[38:39], 0
	v_mov_b64_e32 v[52:53], 0
	v_mov_b64_e32 v[54:55], 0
	v_mov_b64_e32 v[40:41], 0
	v_mov_b64_e32 v[42:43], 0
	v_mov_b64_e32 v[56:57], 0
	v_mov_b64_e32 v[58:59], 0
	v_mov_b64_e32 v[44:45], 0
	v_mov_b64_e32 v[46:47], 0
	v_mov_b64_e32 v[60:61], 0
	v_mov_b64_e32 v[62:63], 0
	v_mov_b64_e32 v[96:97], 0
	v_mov_b32_e32 v98, v0
	v_mov_b32_e32 v99, v0
	v_mov_b32_e32 v100, v0
	v_mov_b32_e32 v101, v0
	v_mov_b32_e32 v102, v0
	v_mov_b32_e32 v103, v0
	v_mov_b32_e32 v104, v0
	v_mov_b32_e32 v105, v0
	v_mov_b32_e32 v106, v0
	v_mov_b32_e32 v107, v0
	v_mov_b32_e32 v108, v0
	v_mov_b32_e32 v109, v0
	v_mov_b32_e32 v110, v0
	v_mov_b32_e32 v111, v0
	v_mov_b32_e32 v112, v0
	v_mov_b32_e32 v113, v0
	v_mov_b32_e32 v114, v0
	v_mov_b32_e32 v115, v0
	v_mov_b32_e32 v116, v0
	v_mov_b32_e32 v117, v0
	v_mov_b32_e32 v118, v0
	v_mov_b32_e32 v119, v0
	v_mov_b32_e32 v120, v0
	v_mov_b32_e32 v121, v0
	v_mov_b32_e32 v122, v0
	v_mov_b32_e32 v123, v0
	v_mov_b32_e32 v124, v0
	v_mov_b32_e32 v125, v0
	v_mov_b32_e32 v126, v0
	v_mov_b32_e32 v127, v0

;     __device__ __forceinline__ void operator()(const f32x4 (&acc)[2][2][4][2], const Unit& u, int wr, int wc, int fr, int fq) const {
;     ...
;             for (int m = 0; m < 4; ++m) { const int rl = rl0 + ai * HALF + m; const float c = rs[u.pm * BM + rl] * (1.0f / W8_SCALE);
;                 const f32x4 a = acc[ai][0][m][0] * c, b = acc[ai][0][m][1] * c;
;                 float q = (a[0] * a[0] + a[1] * a[1]) + (a[2] * a[2] + a[3] * a[3]) + (b[0] * b[0] + b[1] * b[1]) + (b[2] * b[2] + b[3] * b[3]);
;                 q += __shfl_xor(q, 16); q += __shfl_xor(q, 32);
;                 if (fq == 0) xch[rl * 4 + wc] = q; }
.LBB0_401:
	v_mbcnt_lo_u32_b32 v128, -1, 0
	v_mbcnt_hi_u32_b32 v128, -1, v128
	s_lshl_b32 s58, s56, 8
	v_and_b32_e32 v184, 15, v128
	v_lshl_or_b32 v185, v184, 2, s34
	v_add_u32_e32 v152, s58, v185
	v_ashrrev_i32_e32 v153, 31, v152
	v_lshl_add_u64 v[170:171], v[152:153], 2, s[12:13]
	global_load_dword v131, v[170:171], off
	global_load_dword v240, v[170:171], off
	global_load_dword v241, v[170:171], off offset:4
	global_load_dword v242, v[170:171], off offset:8
	global_load_dword v243, v[170:171], off offset:12
	global_load_dword v244, v[170:171], off offset:512
	global_load_dword v245, v[170:171], off offset:516
	global_load_dword v246, v[170:171], off offset:520
	global_load_dword v247, v[170:171], off offset:524
	v_and_b32_e32 v132, 64, v183
	v_add_u32_e32 v140, 64, v132
	v_xor_b32_e32 v130, 16, v183
	v_cmp_lt_i32_e32 vcc, v130, v140
	s_waitcnt vmcnt(0)
	v_mul_f32_e32 v132, 0x3c800000, v131
	v_pk_mul_f32 v[134:135], v[126:127], v[132:133] op_sel_hi:[1,0]
	v_pk_mul_f32 v[136:137], v[124:125], v[132:133] op_sel_hi:[1,0]
	v_pk_mul_f32 v[138:139], v[122:123], v[132:133] op_sel_hi:[1,0]
	v_pk_mul_f32 v[132:133], v[120:121], v[132:133] op_sel_hi:[1,0]
	v_mul_f32_e32 v131, v137, v137
	v_mul_f32_e32 v135, v135, v135
	v_mul_f32_e32 v133, v133, v133
	v_fmac_f32_e32 v131, v136, v136
	v_fmac_f32_e32 v135, v134, v134
	v_mul_f32_e32 v137, v139, v139
	v_fmac_f32_e32 v133, v132, v132
	v_add_f32_e32 v131, v131, v135
	v_cndmask_b32_e32 v130, v183, v130, vcc
	v_add_f32_e32 v131, v133, v131
	v_fmac_f32_e32 v137, v138, v138
	v_lshlrev_b32_e32 v130, 2, v130
	v_add_f32_e32 v132, v137, v131
	ds_bpermute_b32 v133, v130, v132
	v_xor_b32_e32 v131, 32, v183
	v_cmp_lt_i32_e32 vcc, v131, v140
	s_waitcnt lgkmcnt(0)
	v_add_f32_e32 v132, v132, v133
	v_cndmask_b32_e32 v131, v183, v131, vcc
	v_lshlrev_b32_e32 v131, 2, v131
	ds_bpermute_b32 v133, v131, v132
	v_cmp_gt_u32_e32 vcc, 16, v128
	s_and_saveexec_b64 s[4:5], vcc
	s_cbranch_execz .LBB0_403
	s_waitcnt lgkmcnt(0)
	v_add_f32_e32 v132, v132, v133
	v_lshl_add_u32 v133, v185, 4, s85
	ds_write_b32 v133, v132
.LBB0_403:
	s_or_b64 exec, exec, s[4:5]
	v_or_b32_e32 v172, 1, v185
	v_add_u32_e32 v166, s58, v172
	v_ashrrev_i32_e32 v167, 31, v166
	v_lshl_add_u64 v[168:169], v[166:167], 2, s[12:13]
	v_mov_b32_e32 v132, v241
	v_mul_f32_e32 v132, 0x3c800000, v132
	s_waitcnt lgkmcnt(0)
	v_pk_mul_f32 v[134:135], v[118:119], v[132:133] op_sel_hi:[1,0]
	v_pk_mul_f32 v[136:137], v[116:117], v[132:133] op_sel_hi:[1,0]
	v_pk_mul_f32 v[138:139], v[114:115], v[132:133] op_sel_hi:[1,0]
	v_pk_mul_f32 v[132:133], v[112:113], v[132:133] op_sel_hi:[1,0]
	v_mul_f32_e32 v137, v137, v137
	v_mul_f32_e32 v135, v135, v135
	v_mul_f32_e32 v133, v133, v133
	v_fmac_f32_e32 v137, v136, v136
	v_fmac_f32_e32 v135, v134, v134
	v_mul_f32_e32 v139, v139, v139
	v_fmac_f32_e32 v133, v132, v132
	v_add_f32_e32 v132, v137, v135
	v_add_f32_e32 v132, v133, v132
	v_fmac_f32_e32 v139, v138, v138
	v_add_f32_e32 v132, v139, v132
	ds_bpermute_b32 v133, v130, v132
	s_waitcnt lgkmcnt(0)
	v_add_f32_e32 v132, v132, v133
	ds_bpermute_b32 v133, v131, v132
	s_and_saveexec_b64 s[4:5], vcc
	s_cbranch_execz .LBB0_405
	s_waitcnt lgkmcnt(0)
	v_add_f32_e32 v132, v132, v133
	v_lshl_add_u32 v133, v172, 4, s85
	ds_write_b32 v133, v132
.LBB0_405:
	s_or_b64 exec, exec, s[4:5]
	v_or_b32_e32 v191, 2, v185
	v_add_u32_e32 v162, s58, v191
	v_ashrrev_i32_e32 v163, 31, v162
	v_lshl_add_u64 v[164:165], v[162:163], 2, s[12:13]
	v_mov_b32_e32 v132, v242
	v_mul_f32_e32 v132, 0x3c800000, v132
	s_waitcnt lgkmcnt(0)
	v_pk_mul_f32 v[134:135], v[110:111], v[132:133] op_sel_hi:[1,0]
	v_pk_mul_f32 v[136:137], v[108:109], v[132:133] op_sel_hi:[1,0]
	v_pk_mul_f32 v[138:139], v[106:107], v[132:133] op_sel_hi:[1,0]
	v_pk_mul_f32 v[132:133], v[104:105], v[132:133] op_sel_hi:[1,0]
	v_mul_f32_e32 v137, v137, v137
	v_mul_f32_e32 v135, v135, v135
	v_mul_f32_e32 v133, v133, v133
	v_fmac_f32_e32 v137, v136, v136
	v_fmac_f32_e32 v135, v134, v134
	v_mul_f32_e32 v139, v139, v139
	v_fmac_f32_e32 v133, v132, v132
	v_add_f32_e32 v132, v137, v135
	v_add_f32_e32 v132, v133, v132
	v_fmac_f32_e32 v139, v138, v138
	v_add_f32_e32 v132, v139, v132
	ds_bpermute_b32 v133, v130, v132
	s_waitcnt lgkmcnt(0)
	v_add_f32_e32 v132, v132, v133
	ds_bpermute_b32 v133, v131, v132
	s_and_saveexec_b64 s[4:5], vcc
	s_cbranch_execz .LBB0_407
	s_waitcnt lgkmcnt(0)
	v_add_f32_e32 v132, v132, v133
	v_lshl_add_u32 v133, v191, 4, s85
	ds_write_b32 v133, v132
.LBB0_407:
	s_or_b64 exec, exec, s[4:5]
	v_or_b32_e32 v192, 3, v185
	v_add_u32_e32 v158, s58, v192
	v_ashrrev_i32_e32 v159, 31, v158
	v_lshl_add_u64 v[160:161], v[158:159], 2, s[12:13]
	v_mov_b32_e32 v132, v243
	v_mul_f32_e32 v132, 0x3c800000, v132
	s_waitcnt lgkmcnt(0)
	v_pk_mul_f32 v[134:135], v[102:103], v[132:133] op_sel_hi:[1,0]
	v_pk_mul_f32 v[136:137], v[100:101], v[132:133] op_sel_hi:[1,0]
	v_pk_mul_f32 v[138:139], v[98:99], v[132:133] op_sel_hi:[1,0]
	v_pk_mul_f32 v[132:133], v[96:97], v[132:133] op_sel_hi:[1,0]
	v_mul_f32_e32 v137, v137, v137
	v_mul_f32_e32 v135, v135, v135
	v_mul_f32_e32 v133, v133, v133
	v_fmac_f32_e32 v137, v136, v136
	v_fmac_f32_e32 v135, v134, v134
	v_mul_f32_e32 v139, v139, v139
	v_fmac_f32_e32 v133, v132, v132
	v_add_f32_e32 v132, v137, v135
	v_add_f32_e32 v132, v133, v132
	v_fmac_f32_e32 v139, v138, v138
	v_add_f32_e32 v132, v139, v132
	ds_bpermute_b32 v133, v130, v132
	s_waitcnt lgkmcnt(0)
	v_add_f32_e32 v132, v132, v133
	ds_bpermute_b32 v133, v131, v132
	s_and_saveexec_b64 s[4:5], vcc
	s_cbranch_execz .LBB0_409
	s_waitcnt lgkmcnt(0)
	v_add_f32_e32 v132, v132, v133
	v_lshl_add_u32 v133, v192, 4, s85
	ds_write_b32 v133, v132
;     __device__ __forceinline__ void operator()(const f32x4 (&acc)[2][2][4][2], const Unit& u, int wr, int wc, int fr, int fq) const {
;     ...
;             for (int m = 0; m < 4; ++m) { const int rl = rl0 + ai * HALF + m; const float c = rs[u.pm * BM + rl] * (1.0f / W8_SCALE);
;                 const f32x4 a = acc[ai][0][m][0] * c, b = acc[ai][0][m][1] * c;
;                 float q = (a[0] * a[0] + a[1] * a[1]) + (a[2] * a[2] + a[3] * a[3]) + (b[0] * b[0] + b[1] * b[1]) + (b[2] * b[2] + b[3] * b[3]);
;                 q += __shfl_xor(q, 16); q += __shfl_xor(q, 32);
;                 if (fq == 0) xch[rl * 4 + wc] = q; }
.LBB0_409:
	s_or_b64 exec, exec, s[4:5]
	v_add_u32_e32 v189, 0x80, v185
	v_add_u32_e32 v154, s58, v189
	v_ashrrev_i32_e32 v155, 31, v154
	v_lshl_add_u64 v[156:157], v[154:155], 2, s[12:13]
	v_mov_b32_e32 v132, v244
	v_mul_f32_e32 v132, 0x3c800000, v132
	s_waitcnt lgkmcnt(0)
	v_pk_mul_f32 v[134:135], v[94:95], v[132:133] op_sel_hi:[1,0]
	v_pk_mul_f32 v[136:137], v[92:93], v[132:133] op_sel_hi:[1,0]
	v_pk_mul_f32 v[138:139], v[90:91], v[132:133] op_sel_hi:[1,0]
	v_pk_mul_f32 v[132:133], v[88:89], v[132:133] op_sel_hi:[1,0]
	v_mul_f32_e32 v137, v137, v137
	v_mul_f32_e32 v135, v135, v135
	v_mul_f32_e32 v133, v133, v133
	v_fmac_f32_e32 v137, v136, v136
	v_fmac_f32_e32 v135, v134, v134
	v_mul_f32_e32 v139, v139, v139
	v_fmac_f32_e32 v133, v132, v132
	v_add_f32_e32 v132, v137, v135
	v_add_f32_e32 v132, v133, v132
	v_fmac_f32_e32 v139, v138, v138
	v_add_f32_e32 v132, v139, v132
	ds_bpermute_b32 v133, v130, v132
	s_waitcnt lgkmcnt(0)
	v_add_f32_e32 v132, v132, v133
	ds_bpermute_b32 v133, v131, v132
	s_and_saveexec_b64 s[4:5], vcc
	s_cbranch_execz .LBB0_411
	s_waitcnt lgkmcnt(0)
	v_add_f32_e32 v132, v132, v133
	v_lshl_add_u32 v133, v189, 4, s85
	ds_write_b32 v133, v132
.LBB0_411:
	s_or_b64 exec, exec, s[4:5]
	v_add_u32_e32 v190, 0x81, v185
	v_add_u32_e32 v148, s58, v190
	v_ashrrev_i32_e32 v149, 31, v148
	v_lshl_add_u64 v[150:151], v[148:149], 2, s[12:13]
	v_mov_b32_e32 v132, v245
	v_mul_f32_e32 v132, 0x3c800000, v132
	s_waitcnt lgkmcnt(0)
	v_pk_mul_f32 v[134:135], v[86:87], v[132:133] op_sel_hi:[1,0]
	v_pk_mul_f32 v[136:137], v[84:85], v[132:133] op_sel_hi:[1,0]
	v_pk_mul_f32 v[138:139], v[82:83], v[132:133] op_sel_hi:[1,0]
	v_pk_mul_f32 v[132:133], v[80:81], v[132:133] op_sel_hi:[1,0]
	v_mul_f32_e32 v137, v137, v137
	v_mul_f32_e32 v135, v135, v135
	v_mul_f32_e32 v133, v133, v133
	v_fmac_f32_e32 v137, v136, v136
	v_fmac_f32_e32 v135, v134, v134
	v_mul_f32_e32 v139, v139, v139
	v_fmac_f32_e32 v133, v132, v132
	v_add_f32_e32 v132, v137, v135
	v_add_f32_e32 v132, v133, v132
	v_fmac_f32_e32 v139, v138, v138
	v_add_f32_e32 v132, v139, v132
	ds_bpermute_b32 v133, v130, v132
	s_waitcnt lgkmcnt(0)
	v_add_f32_e32 v132, v132, v133
	ds_bpermute_b32 v133, v131, v132
	s_and_saveexec_b64 s[4:5], vcc
	s_cbranch_execz .LBB0_413
	s_waitcnt lgkmcnt(0)
	v_add_f32_e32 v132, v132, v133
	v_lshl_add_u32 v133, v190, 4, s85
	ds_write_b32 v133, v132
.LBB0_413:
	s_or_b64 exec, exec, s[4:5]
	v_add_u32_e32 v187, 0x82, v185
	v_add_u32_e32 v144, s58, v187
	v_ashrrev_i32_e32 v145, 31, v144
	v_lshl_add_u64 v[146:147], v[144:145], 2, s[12:13]
	v_mov_b32_e32 v132, v246
	v_mul_f32_e32 v132, 0x3c800000, v132
	s_waitcnt lgkmcnt(0)
	v_pk_mul_f32 v[134:135], v[78:79], v[132:133] op_sel_hi:[1,0]
	v_pk_mul_f32 v[136:137], v[76:77], v[132:133] op_sel_hi:[1,0]
	v_pk_mul_f32 v[138:139], v[74:75], v[132:133] op_sel_hi:[1,0]
	v_pk_mul_f32 v[132:133], v[72:73], v[132:133] op_sel_hi:[1,0]
	v_mul_f32_e32 v137, v137, v137
	v_mul_f32_e32 v135, v135, v135
	v_mul_f32_e32 v133, v133, v133
	v_fmac_f32_e32 v137, v136, v136
	v_fmac_f32_e32 v135, v134, v134
	v_mul_f32_e32 v139, v139, v139
	v_fmac_f32_e32 v133, v132, v132
	v_add_f32_e32 v132, v137, v135
	v_add_f32_e32 v132, v133, v132
	v_fmac_f32_e32 v139, v138, v138
	v_add_f32_e32 v132, v139, v132
	ds_bpermute_b32 v133, v130, v132
	s_waitcnt lgkmcnt(0)
	v_add_f32_e32 v132, v132, v133
	ds_bpermute_b32 v133, v131, v132
	s_and_saveexec_b64 s[4:5], vcc
	s_cbranch_execz .LBB0_415
	s_waitcnt lgkmcnt(0)
	v_add_f32_e32 v132, v132, v133
	v_lshl_add_u32 v133, v187, 4, s85
	ds_write_b32 v133, v132
.LBB0_415:
	s_or_b64 exec, exec, s[4:5]
	v_add_u32_e32 v173, 0x83, v185
	v_add_u32_e32 v132, s58, v173
	s_waitcnt lgkmcnt(0)
	v_ashrrev_i32_e32 v133, 31, v132
	v_lshl_add_u64 v[134:135], v[132:133], 2, s[12:13]
	v_mov_b32_e32 v136, v247
	v_lshlrev_b32_e32 v188, 4, v173
	v_mul_f32_e32 v136, 0x3c800000, v136
	v_pk_mul_f32 v[138:139], v[70:71], v[136:137] op_sel_hi:[1,0]
	v_pk_mul_f32 v[140:141], v[68:69], v[136:137] op_sel_hi:[1,0]
	v_pk_mul_f32 v[142:143], v[66:67], v[136:137] op_sel_hi:[1,0]
	v_pk_mul_f32 v[136:137], v[64:65], v[136:137] op_sel_hi:[1,0]
	v_mul_f32_e32 v141, v141, v141
	v_mul_f32_e32 v139, v139, v139
	v_mul_f32_e32 v137, v137, v137
	v_fmac_f32_e32 v141, v140, v140
	v_fmac_f32_e32 v139, v138, v138
	v_mul_f32_e32 v143, v143, v143
	v_fmac_f32_e32 v137, v136, v136
	v_add_f32_e32 v136, v141, v139
	v_add_f32_e32 v136, v137, v136
	v_fmac_f32_e32 v143, v142, v142
	v_add_f32_e32 v136, v143, v136
	ds_bpermute_b32 v130, v130, v136
	s_waitcnt lgkmcnt(0)
	v_add_f32_e32 v130, v136, v130
	ds_bpermute_b32 v131, v131, v130
	s_and_saveexec_b64 s[4:5], vcc
	s_cbranch_execz .LBB0_417
	s_waitcnt lgkmcnt(0)
	v_add_f32_e32 v130, v130, v131
	v_add_u32_e32 v131, s85, v188
	ds_write_b32 v131, v130
; #define LAS __attribute__((address_space(3)))
; __device__ __forceinline__ unsigned cvt_pk4_fp8(float a, float b, float c, float d) { int w; asm("" : "=v"(w));     w = __builtin_amdgcn_cvt_pk_fp8_f32(a, b, w, false); w = __builtin_amdgcn_cvt_pk_fp8_f32(c, d, w, true); return (unsigned)w; }
;     __device__ __forceinline__ void operator()(const f32x4 (&acc)[2][2][4][2], const Unit& u, int wr, int wc, int fr, int fq) const {
;     ...
;         asm volatile("s_waitcnt lgkmcnt(0)" ::: "memory"); __builtin_amdgcn_s_barrier(); asm volatile("" ::: "memory");
;         const f32x4 g0 = *(const f32x4*)(gk + dl0) * *(const f32x4*)(gq + dl0), g1 = *(const f32x4*)(gk + dl0 + 4) * *(const f32x4*)(gq + dl0 + 4);
;         const int kpos = 64 * (wc >> 1) + 32 * (fq & 1) + 8 * ((2 * wc + (fq >> 1)) & 3);
; #pragma unroll
;         for (int ai = 0; ai < 2; ++ai)
; #pragma unroll
;             for (int m = 0; m < 4; ++m) { const int rl = rl0 + ai * HALF + m; const float c = rs[u.pm * BM + rl] * (1.0f / W8_SCALE);
;                 const f32x4 pq = *(const LAS f32x4*)(xch + rl * 4); const float rstd = rsqrtf(((pq[0] + pq[1]) + (pq[2] + pq[3])) * (1.0f / 128.0f) + RMS_EPS) * c;
;                 const f32x4 v0 = acc[ai][0][m][0] * (rstd * KSC_) * g0, v1 = acc[ai][0][m][1] * (rstd * KSC_) * g1;
;                 u32x2 w; w.x = cvt_pk4_fp8(v0[0], v0[1], v0[2], v0[3]); w.y = cvt_pk4_fp8(v1[0], v1[1], v1[2], v1[3]);
;                 *(u32x2*)(K8 + (size_t)(u.pm * BM + rl) * 2048 + u.pn * 128 + kpos) = w; }
.LBB0_417:
	s_or_b64 exec, exec, s[4:5]
	s_waitcnt lgkmcnt(0)
	s_barrier
	s_load_dwordx2 s[4:5], s[88:89], 0x50
	v_ashrrev_i32_e32 v128, 4, v128
	v_lshl_add_u32 v130, v128, 3, s41
	s_waitcnt lgkmcnt(0)
	v_ashrrev_i32_e32 v131, 31, v130
	v_lshlrev_b64 v[140:141], 2, v[130:131]
	v_lshl_add_u64 v[136:137], s[4:5], 0, v[140:141]
	global_load_dwordx4 v[194:197], v[136:137], off offset:16
	s_nop 0
	global_load_dwordx4 v[136:139], v[136:137], off
	s_load_dwordx2 s[4:5], s[88:89], 0x40
	v_lshlrev_b32_e32 v186, 5, v128
	v_lshl_add_u32 v128, v128, 2, s83
	v_and_b32_e32 v131, 32, v186
	v_and_b32_e32 v128, 24, v128
	s_waitcnt lgkmcnt(0)
	v_lshl_add_u64 v[140:141], s[4:5], 0, v[140:141]
	global_load_dwordx4 v[198:201], v[140:141], off offset:16
	global_load_dwordx4 v[202:205], v[140:141], off
	v_or3_b32 v128, v131, s82, v128
	v_mov_b32_e32 v131, v240
	s_lshl_b32 s60, s0, 7
	s_add_i32 s0, 0, 0x20000
	v_lshlrev_b64 v[152:153], 11, v[152:153]
	s_ashr_i32 s61, s60, 31
	v_lshl_add_u64 v[152:153], s[48:49], 0, v[152:153]
	v_lshl_add_u64 v[152:153], v[152:153], 0, s[60:61]
	s_mov_b32 s4, 0x358637bd
	s_ashr_i32 s59, s58, 31
	s_lshr_b32 s1, s59, 19
	s_add_i32 s1, s58, s1
	s_and_b32 s1, s1, 0xffffe000
	s_sub_i32 s1, s58, s1
	s_ashr_i32 s1, s1, 6
	s_waitcnt vmcnt(0)
	v_pk_mul_f32 v[140:141], v[138:139], v[204:205]
	v_pk_mul_f32 v[142:143], v[136:137], v[202:203]
	v_mul_f32_e32 v193, 0x3c800000, v131
	v_lshl_add_u32 v131, v185, 4, s0
	v_pk_mul_f32 v[136:137], v[196:197], v[200:201]
	v_pk_mul_f32 v[138:139], v[194:195], v[198:199]
	ds_read_b128 v[194:197], v131
	s_waitcnt lgkmcnt(0)
	v_mov_b32_e32 v170, v195
	v_mov_b32_e32 v171, v196
	v_mov_b32_e32 v195, v197
	v_pk_add_f32 v[198:199], v[170:171], v[194:195]
	v_lshl_add_u64 v[170:171], v[152:153], 0, v[128:129]
	v_lshl_add_u32 v152, v172, 4, s0
	ds_read_b128 v[194:197], v152
	v_mov_b32_e32 v173, v198
	s_waitcnt lgkmcnt(0)
	v_mov_b32_e32 v152, v195
	v_mov_b32_e32 v153, v196
	v_mov_b32_e32 v195, v197
	v_pk_add_f32 v[152:153], v[152:153], v[194:195]
	s_nop 0
	v_mov_b32_e32 v172, v152
	v_mov_b32_e32 v198, v153
	v_pk_add_f32 v[172:173], v[172:173], v[198:199]
	v_mov_b64_e32 v[152:153], s[4:5]
	v_pk_fma_f32 v[172:173], v[172:173], s[22:23], v[152:153] op_sel_hi:[1,0,0]
	s_nop 0
	v_mul_f32_e32 v194, 0x4b800000, v173
	v_cmp_gt_f32_e64 s[4:5], s86, v173
	v_cmp_gt_f32_e32 vcc, s86, v172
	s_nop 0
	v_cndmask_b32_e64 v173, v173, v194, s[4:5]
	v_rsq_f32_e32 v173, v173
	s_nop 0
	v_mul_f32_e32 v194, 0x45800000, v173
	v_cndmask_b32_e64 v173, v173, v194, s[4:5]
	v_mul_f32_e32 v173, v193, v173
	v_mul_f32_e32 v194, 0x3ed53b94, v173
	v_pk_mul_f32 v[124:125], v[124:125], v[194:195] op_sel_hi:[1,0]
	v_pk_mul_f32 v[196:197], v[120:121], v[194:195] op_sel_hi:[1,0]
	v_pk_mul_f32 v[126:127], v[126:127], v[194:195] op_sel_hi:[1,0]
	v_pk_mul_f32 v[124:125], v[142:143], v[124:125]
	v_pk_mul_f32 v[120:121], v[122:123], v[194:195] op_sel_hi:[1,0]
	v_pk_mul_f32 v[122:123], v[138:139], v[196:197]
	v_mov_b32_e32 v194, v131
	v_mov_b32_e32 v195, v131
	v_cvt_pk_fp8_f32 v194, v124, v125
	v_cvt_pk_fp8_f32 v195, v122, v123
	v_pk_mul_f32 v[126:127], v[140:141], v[126:127]
	v_pk_mul_f32 v[120:121], v[136:137], v[120:121]
	v_cvt_pk_fp8_f32 v194, v126, v127 op_sel:[0,0,1]
	v_cvt_pk_fp8_f32 v195, v120, v121 op_sel:[0,0,1]
	v_mul_f32_e32 v121, 0x4b800000, v172
	v_cndmask_b32_e32 v121, v172, v121, vcc
	v_rsq_f32_e32 v121, v121
	global_store_dwordx2 v[170:171], v[194:195], off
	v_mov_b32_e32 v120, v241
	v_mul_f32_e32 v122, 0x45800000, v121
	v_cndmask_b32_e32 v121, v121, v122, vcc
	v_mul_f32_e32 v120, 0x3c800000, v120
	v_mul_f32_e32 v120, v120, v121
	v_mul_f32_e32 v120, 0x3ed53b94, v120
	v_pk_mul_f32 v[116:117], v[116:117], v[120:121] op_sel_hi:[1,0]
	v_pk_mul_f32 v[112:113], v[112:113], v[120:121] op_sel_hi:[1,0]
	v_pk_mul_f32 v[118:119], v[118:119], v[120:121] op_sel_hi:[1,0]
	v_pk_mul_f32 v[116:117], v[142:143], v[116:117]
	v_pk_mul_f32 v[114:115], v[114:115], v[120:121] op_sel_hi:[1,0]
	v_pk_mul_f32 v[112:113], v[138:139], v[112:113]
	v_mov_b32_e32 v120, v131
	v_mov_b32_e32 v121, v131
	v_cvt_pk_fp8_f32 v120, v116, v117
	v_cvt_pk_fp8_f32 v121, v112, v113
	v_pk_mul_f32 v[118:119], v[140:141], v[118:119]
	v_pk_mul_f32 v[114:115], v[136:137], v[114:115]
	v_cvt_pk_fp8_f32 v120, v118, v119 op_sel:[0,0,1]
	v_cvt_pk_fp8_f32 v121, v114, v115 op_sel:[0,0,1]
	v_lshlrev_b64 v[112:113], 11, v[166:167]
	v_lshl_add_u64 v[112:113], s[48:49], 0, v[112:113]
	v_lshl_add_u64 v[112:113], v[112:113], 0, s[60:61]
	v_lshl_add_u64 v[112:113], v[112:113], 0, v[128:129]
	global_store_dwordx2 v[112:113], v[120:121], off
	v_mov_b32_e32 v112, v242
	v_mul_f32_e32 v122, 0x3c800000, v112
	v_lshl_add_u32 v112, v191, 4, s0
	ds_read_b128 v[112:115], v112
	s_waitcnt lgkmcnt(0)
	v_mov_b32_e32 v116, v113
	v_mov_b32_e32 v117, v114
	v_mov_b32_e32 v113, v115
	v_pk_add_f32 v[116:117], v[116:117], v[112:113]
	v_lshlrev_b64 v[112:113], 11, v[162:163]
	v_lshl_add_u64 v[112:113], s[48:49], 0, v[112:113]
	v_lshl_add_u64 v[112:113], v[112:113], 0, s[60:61]
	v_lshl_add_u64 v[118:119], v[112:113], 0, v[128:129]
	v_lshl_add_u32 v112, v192, 4, s0
	ds_read_b128 v[112:115], v112
	s_waitcnt lgkmcnt(0)
; #define LAS __attribute__((address_space(3)))
; __device__ __forceinline__ unsigned cvt_pk4_fp8(float a, float b, float c, float d) { int w; asm("" : "=v"(w));     w = __builtin_amdgcn_cvt_pk_fp8_f32(a, b, w, false); w = __builtin_amdgcn_cvt_pk_fp8_f32(c, d, w, true); return (unsigned)w; }
;     __device__ __forceinline__ void operator()(const f32x4 (&acc)[2][2][4][2], const Unit& u, int wr, int wc, int fr, int fq) const {
;     ...
;             for (int m = 0; m < 4; ++m) { const int rl = rl0 + ai * HALF + m; const float c = rs[u.pm * BM + rl] * (1.0f / W8_SCALE);
;                 const f32x4 pq = *(const LAS f32x4*)(xch + rl * 4); const float rstd = rsqrtf(((pq[0] + pq[1]) + (pq[2] + pq[3])) * (1.0f / 128.0f) + RMS_EPS) * c;
;                 const f32x4 v0 = acc[ai][0][m][0] * (rstd * KSC_) * g0, v1 = acc[ai][0][m][1] * (rstd * KSC_) * g1;
;                 u32x2 w; w.x = cvt_pk4_fp8(v0[0], v0[1], v0[2], v0[3]); w.y = cvt_pk4_fp8(v1[0], v1[1], v1[2], v1[3]);
;                 *(u32x2*)(K8 + (size_t)(u.pm * BM + rl) * 2048 + u.pn * 128 + kpos) = w; }
	v_mov_b32_e32 v120, v113
	v_mov_b32_e32 v121, v114
	v_mov_b32_e32 v113, v115
	v_pk_add_f32 v[112:113], v[120:121], v[112:113]
	v_mov_b32_e32 v115, v116
	v_mov_b32_e32 v114, v112
	v_mov_b32_e32 v116, v113
	v_pk_add_f32 v[112:113], v[114:115], v[116:117]
	s_nop 0
	v_pk_fma_f32 v[112:113], v[112:113], s[22:23], v[152:153] op_sel_hi:[1,0,0]
	s_nop 0
	v_mul_f32_e32 v114, 0x4b800000, v113
	v_cmp_gt_f32_e64 s[4:5], s86, v113
	v_cmp_gt_f32_e32 vcc, s86, v112
	s_nop 0
	v_cndmask_b32_e64 v113, v113, v114, s[4:5]
	v_rsq_f32_e32 v113, v113
	s_nop 0
	v_mul_f32_e32 v114, 0x45800000, v113
	v_cndmask_b32_e64 v113, v113, v114, s[4:5]
	v_mul_f32_e32 v113, v122, v113
	v_mul_f32_e32 v114, 0x3ed53b94, v113
	v_pk_mul_f32 v[108:109], v[108:109], v[114:115] op_sel_hi:[1,0]
	v_pk_mul_f32 v[104:105], v[104:105], v[114:115] op_sel_hi:[1,0]
	v_pk_mul_f32 v[110:111], v[110:111], v[114:115] op_sel_hi:[1,0]
	v_pk_mul_f32 v[108:109], v[142:143], v[108:109]
	v_pk_mul_f32 v[106:107], v[106:107], v[114:115] op_sel_hi:[1,0]
	v_pk_mul_f32 v[104:105], v[138:139], v[104:105]
	v_mov_b32_e32 v114, v131
	v_mov_b32_e32 v115, v131
	v_cvt_pk_fp8_f32 v114, v108, v109
	v_cvt_pk_fp8_f32 v115, v104, v105
	v_pk_mul_f32 v[110:111], v[140:141], v[110:111]
	v_pk_mul_f32 v[106:107], v[136:137], v[106:107]
	v_cvt_pk_fp8_f32 v114, v110, v111 op_sel:[0,0,1]
	v_cvt_pk_fp8_f32 v115, v106, v107 op_sel:[0,0,1]
	v_mul_f32_e32 v105, 0x4b800000, v112
	v_cndmask_b32_e32 v105, v112, v105, vcc
	v_rsq_f32_e32 v105, v105
	global_store_dwordx2 v[118:119], v[114:115], off
	v_mov_b32_e32 v104, v243
	v_mul_f32_e32 v106, 0x45800000, v105
	v_cndmask_b32_e32 v105, v105, v106, vcc
	v_mul_f32_e32 v104, 0x3c800000, v104
	v_mul_f32_e32 v104, v104, v105
	v_mul_f32_e32 v104, 0x3ed53b94, v104
	v_pk_mul_f32 v[100:101], v[100:101], v[104:105] op_sel_hi:[1,0]
	v_pk_mul_f32 v[96:97], v[96:97], v[104:105] op_sel_hi:[1,0]
	v_pk_mul_f32 v[102:103], v[102:103], v[104:105] op_sel_hi:[1,0]
	v_pk_mul_f32 v[100:101], v[142:143], v[100:101]
	v_pk_mul_f32 v[98:99], v[98:99], v[104:105] op_sel_hi:[1,0]
	v_pk_mul_f32 v[96:97], v[138:139], v[96:97]
	v_mov_b32_e32 v104, v131
	v_mov_b32_e32 v105, v131
	v_cvt_pk_fp8_f32 v104, v100, v101
	v_cvt_pk_fp8_f32 v105, v96, v97
	v_pk_mul_f32 v[102:103], v[140:141], v[102:103]
	v_pk_mul_f32 v[98:99], v[136:137], v[98:99]
	v_cvt_pk_fp8_f32 v104, v102, v103 op_sel:[0,0,1]
	v_cvt_pk_fp8_f32 v105, v98, v99 op_sel:[0,0,1]
	v_lshlrev_b64 v[96:97], 11, v[158:159]
	v_lshl_add_u64 v[96:97], s[48:49], 0, v[96:97]
	v_lshl_add_u64 v[96:97], v[96:97], 0, s[60:61]
	v_lshl_add_u64 v[96:97], v[96:97], 0, v[128:129]
	global_store_dwordx2 v[96:97], v[104:105], off
	v_mov_b32_e32 v96, v244
	v_mul_f32_e32 v106, 0x3c800000, v96
	v_lshl_add_u32 v96, v189, 4, s0
	ds_read_b128 v[96:99], v96
	s_waitcnt lgkmcnt(0)
	v_mov_b32_e32 v100, v97
	v_mov_b32_e32 v101, v98
	v_mov_b32_e32 v97, v99
	v_pk_add_f32 v[100:101], v[100:101], v[96:97]
	v_lshlrev_b64 v[96:97], 11, v[154:155]
	v_lshl_add_u64 v[96:97], s[48:49], 0, v[96:97]
	v_lshl_add_u64 v[96:97], v[96:97], 0, s[60:61]
	v_lshl_add_u64 v[102:103], v[96:97], 0, v[128:129]
	v_lshl_add_u32 v96, v190, 4, s0
	ds_read_b128 v[96:99], v96
	s_waitcnt lgkmcnt(0)
	v_mov_b32_e32 v104, v97
	v_mov_b32_e32 v105, v98
	v_mov_b32_e32 v97, v99
	v_pk_add_f32 v[96:97], v[104:105], v[96:97]
	v_mov_b32_e32 v99, v100
	v_mov_b32_e32 v98, v96
	v_mov_b32_e32 v100, v97
	v_pk_add_f32 v[96:97], v[98:99], v[100:101]
	s_nop 0
	v_pk_fma_f32 v[96:97], v[96:97], s[22:23], v[152:153] op_sel_hi:[1,0,0]
	s_nop 0
	v_mul_f32_e32 v98, 0x4b800000, v97
	v_cmp_gt_f32_e64 s[4:5], s86, v97
	v_cmp_gt_f32_e32 vcc, s86, v96
	s_nop 0
	v_cndmask_b32_e64 v97, v97, v98, s[4:5]
	v_rsq_f32_e32 v97, v97
	s_nop 0
	v_mul_f32_e32 v98, 0x45800000, v97
	v_cndmask_b32_e64 v97, v97, v98, s[4:5]
	v_mul_f32_e32 v97, v106, v97
	v_mul_f32_e32 v98, 0x3ed53b94, v97
	v_pk_mul_f32 v[92:93], v[92:93], v[98:99] op_sel_hi:[1,0]
	v_pk_mul_f32 v[88:89], v[88:89], v[98:99] op_sel_hi:[1,0]
	v_pk_mul_f32 v[94:95], v[94:95], v[98:99] op_sel_hi:[1,0]
	v_pk_mul_f32 v[92:93], v[142:143], v[92:93]
	v_pk_mul_f32 v[90:91], v[90:91], v[98:99] op_sel_hi:[1,0]
	v_pk_mul_f32 v[88:89], v[138:139], v[88:89]
	v_mov_b32_e32 v98, v131
	v_mov_b32_e32 v99, v131
	v_cvt_pk_fp8_f32 v98, v92, v93
	v_cvt_pk_fp8_f32 v99, v88, v89
	v_pk_mul_f32 v[94:95], v[140:141], v[94:95]
	v_pk_mul_f32 v[90:91], v[136:137], v[90:91]
	v_cvt_pk_fp8_f32 v98, v94, v95 op_sel:[0,0,1]
	v_cvt_pk_fp8_f32 v99, v90, v91 op_sel:[0,0,1]
	v_mul_f32_e32 v89, 0x4b800000, v96
	v_cndmask_b32_e32 v89, v96, v89, vcc
	v_rsq_f32_e32 v89, v89
	global_store_dwordx2 v[102:103], v[98:99], off
	v_mov_b32_e32 v88, v245
	v_mul_f32_e32 v90, 0x45800000, v89
	v_cndmask_b32_e32 v89, v89, v90, vcc
	v_mul_f32_e32 v88, 0x3c800000, v88
	v_mul_f32_e32 v88, v88, v89
	v_mul_f32_e32 v88, 0x3ed53b94, v88
	v_pk_mul_f32 v[84:85], v[84:85], v[88:89] op_sel_hi:[1,0]
	v_pk_mul_f32 v[80:81], v[80:81], v[88:89] op_sel_hi:[1,0]
	v_pk_mul_f32 v[86:87], v[86:87], v[88:89] op_sel_hi:[1,0]
	v_pk_mul_f32 v[84:85], v[142:143], v[84:85]
	v_pk_mul_f32 v[82:83], v[82:83], v[88:89] op_sel_hi:[1,0]
	v_pk_mul_f32 v[80:81], v[138:139], v[80:81]
	v_mov_b32_e32 v88, v131
	v_mov_b32_e32 v89, v131
	v_cvt_pk_fp8_f32 v88, v84, v85
	v_cvt_pk_fp8_f32 v89, v80, v81
	v_pk_mul_f32 v[86:87], v[140:141], v[86:87]
	v_pk_mul_f32 v[82:83], v[136:137], v[82:83]
	v_cvt_pk_fp8_f32 v88, v86, v87 op_sel:[0,0,1]
	v_cvt_pk_fp8_f32 v89, v82, v83 op_sel:[0,0,1]
	v_lshlrev_b64 v[80:81], 11, v[148:149]
	v_lshl_add_u64 v[80:81], s[48:49], 0, v[80:81]
	v_lshl_add_u64 v[80:81], v[80:81], 0, s[60:61]
	v_lshl_add_u64 v[80:81], v[80:81], 0, v[128:129]
	global_store_dwordx2 v[80:81], v[88:89], off
	v_mov_b32_e32 v80, v246
	v_mul_f32_e32 v90, 0x3c800000, v80
	v_lshl_add_u32 v80, v187, 4, s0
	ds_read_b128 v[80:83], v80
	s_waitcnt lgkmcnt(0)
; #define LAS __attribute__((address_space(3)))
; __device__ __forceinline__ unsigned cvt_pk4_fp8(float a, float b, float c, float d) { int w; asm("" : "=v"(w));     w = __builtin_amdgcn_cvt_pk_fp8_f32(a, b, w, false); w = __builtin_amdgcn_cvt_pk_fp8_f32(c, d, w, true); return (unsigned)w; }
;     __device__ __forceinline__ void operator()(const f32x4 (&acc)[2][2][4][2], const Unit& u, int wr, int wc, int fr, int fq) const {
;     ...
;             for (int m = 0; m < 4; ++m) { const int rl = rl0 + ai * HALF + m; const float c = rs[u.pm * BM + rl] * (1.0f / W8_SCALE);
;                 const f32x4 pq = *(const LAS f32x4*)(xch + rl * 4); const float rstd = rsqrtf(((pq[0] + pq[1]) + (pq[2] + pq[3])) * (1.0f / 128.0f) + RMS_EPS) * c;
;                 const f32x4 v0 = acc[ai][0][m][0] * (rstd * KSC_) * g0, v1 = acc[ai][0][m][1] * (rstd * KSC_) * g1;
;                 u32x2 w; w.x = cvt_pk4_fp8(v0[0], v0[1], v0[2], v0[3]); w.y = cvt_pk4_fp8(v1[0], v1[1], v1[2], v1[3]);
;                 *(u32x2*)(K8 + (size_t)(u.pm * BM + rl) * 2048 + u.pn * 128 + kpos) = w; }
;         const int t0 = u.pm * BM, bb = t0 / SEQ, tile0 = (t0 % SEQ) / 64 + wr;
; #pragma unroll
;         for (int ai = 0; ai < 2; ++ai) { unsigned char* tb = V8T + ((size_t)((bb * NH + u.pn) * (SEQ / 64) + tile0 + 2 * ai)) * 8192 + 4 * ((fr >> 1) & 3);
;             const f32x4 c4 = *(const f32x4*)(rs + u.pm * BM + rl0 + ai * HALF) * (1.0f / W8_SCALE);
; #pragma unroll
;             for (int e = 0; e < 8; ++e) { const int D = dl0 + e, ch = 2 * (fr & 1) + (fr >> 3);
;                 const unsigned w = cvt_pk4_fp8(acc[ai][1][0][e >> 2][e & 3] * c4[0], acc[ai][1][1][e >> 2][e & 3] * c4[1], acc[ai][1][2][e >> 2][e & 3] * c4[2], acc[ai][1][3][e >> 2][e & 3] * c4[3]);
;                 *(unsigned*)(tb + D * 64 + (((ch ^ (D >> 2)) & 3) << 4)) = w; } }
	v_mov_b32_e32 v84, v81
	v_mov_b32_e32 v85, v82
	v_mov_b32_e32 v81, v83
	v_pk_add_f32 v[84:85], v[84:85], v[80:81]
	v_lshlrev_b64 v[80:81], 11, v[144:145]
	v_lshl_add_u64 v[80:81], s[48:49], 0, v[80:81]
	v_lshl_add_u64 v[80:81], v[80:81], 0, s[60:61]
	v_lshl_add_u64 v[86:87], v[80:81], 0, v[128:129]
	v_add_u32_e32 v80, s0, v188
	ds_read_b128 v[80:83], v80
	s_ashr_i32 s0, s56, 31
	s_lshr_b32 s0, s0, 27
	s_add_i32 s0, s56, s0
	s_lshl_b32 s0, s0, 6
	s_waitcnt lgkmcnt(0)
	v_mov_b32_e32 v88, v81
	v_mov_b32_e32 v89, v82
	v_mov_b32_e32 v81, v83
	v_pk_add_f32 v[80:81], v[88:89], v[80:81]
	v_mov_b32_e32 v83, v84
	v_mov_b32_e32 v82, v80
	v_mov_b32_e32 v84, v81
	v_pk_add_f32 v[80:81], v[82:83], v[84:85]
	s_and_b32 s0, s0, 0xfffff800
	v_pk_fma_f32 v[80:81], v[80:81], s[22:23], v[152:153] op_sel_hi:[1,0,0]
	s_nop 0
	v_mul_f32_e32 v82, 0x4b800000, v81
	v_cmp_gt_f32_e64 s[4:5], s86, v81
	v_cmp_gt_f32_e32 vcc, s86, v80
	s_nop 0
	v_cndmask_b32_e64 v81, v81, v82, s[4:5]
	v_rsq_f32_e32 v81, v81
	s_nop 0
	v_mul_f32_e32 v82, 0x45800000, v81
	v_cndmask_b32_e64 v81, v81, v82, s[4:5]
	v_mul_f32_e32 v81, v90, v81
	v_mul_f32_e32 v82, 0x3ed53b94, v81
	v_pk_mul_f32 v[76:77], v[76:77], v[82:83] op_sel_hi:[1,0]
	v_pk_mul_f32 v[72:73], v[72:73], v[82:83] op_sel_hi:[1,0]
	v_pk_mul_f32 v[78:79], v[78:79], v[82:83] op_sel_hi:[1,0]
	v_pk_mul_f32 v[76:77], v[142:143], v[76:77]
	v_pk_mul_f32 v[74:75], v[74:75], v[82:83] op_sel_hi:[1,0]
	v_pk_mul_f32 v[72:73], v[138:139], v[72:73]
	v_mov_b32_e32 v82, v131
	v_mov_b32_e32 v83, v131
	v_cvt_pk_fp8_f32 v82, v76, v77
	v_cvt_pk_fp8_f32 v83, v72, v73
	v_pk_mul_f32 v[78:79], v[140:141], v[78:79]
	v_pk_mul_f32 v[74:75], v[136:137], v[74:75]
	v_cvt_pk_fp8_f32 v82, v78, v79 op_sel:[0,0,1]
	v_cvt_pk_fp8_f32 v83, v74, v75 op_sel:[0,0,1]
	v_mul_f32_e32 v73, 0x4b800000, v80
	v_cndmask_b32_e32 v73, v80, v73, vcc
	v_rsq_f32_e32 v73, v73
	global_store_dwordx2 v[86:87], v[82:83], off
	v_mov_b32_e32 v72, v247
	s_add_i32 s4, s60, s36
	v_mul_f32_e32 v74, 0x45800000, v73
	v_cndmask_b32_e32 v73, v73, v74, vcc
	s_add_i32 s0, s4, s0
	s_add_i32 s0, s0, s1
	s_lshl_b64 s[4:5], s[58:59], 2
	s_add_u32 s4, s12, s4
	s_addc_u32 s5, s13, s5
	v_mov_b32_e32 v78, v131
	v_lshrrev_b32_e32 v74, 3, v184
	s_ashr_i32 s1, s0, 31
	s_lshl_b64 s[0:1], s[0:1], 13
	s_andn2_b64 vcc, exec, s[26:27]
	v_mul_f32_e32 v72, 0x3c800000, v72
	v_mul_f32_e32 v72, v72, v73
	v_mul_f32_e32 v72, 0x3ed53b94, v72
	v_pk_mul_f32 v[68:69], v[68:69], v[72:73] op_sel_hi:[1,0]
	v_pk_mul_f32 v[64:65], v[64:65], v[72:73] op_sel_hi:[1,0]
	v_pk_mul_f32 v[70:71], v[70:71], v[72:73] op_sel_hi:[1,0]
	v_pk_mul_f32 v[68:69], v[142:143], v[68:69]
	v_pk_mul_f32 v[66:67], v[66:67], v[72:73] op_sel_hi:[1,0]
	v_pk_mul_f32 v[64:65], v[138:139], v[64:65]
	v_mov_b32_e32 v72, v131
	v_mov_b32_e32 v73, v131
	v_cvt_pk_fp8_f32 v72, v68, v69
	v_cvt_pk_fp8_f32 v73, v64, v65
	v_pk_mul_f32 v[70:71], v[140:141], v[70:71]
	v_pk_mul_f32 v[66:67], v[136:137], v[66:67]
	v_cvt_pk_fp8_f32 v72, v70, v71 op_sel:[0,0,1]
	v_cvt_pk_fp8_f32 v73, v66, v67 op_sel:[0,0,1]
	v_lshlrev_b64 v[64:65], 11, v[132:133]
	v_lshl_add_u64 v[64:65], s[48:49], 0, v[64:65]
	v_lshl_add_u64 v[64:65], v[64:65], 0, s[60:61]
	v_lshl_add_u64 v[64:65], v[64:65], 0, v[128:129]
	global_store_dwordx2 v[64:65], v[72:73], off
	v_lshlrev_b32_e32 v72, 2, v185
	v_mov_b32_e32 v66, v240
	v_mov_b32_e32 v67, v241
	v_mov_b32_e32 v68, v242
	v_mov_b32_e32 v69, v243
	v_lshlrev_b32_e32 v73, 1, v184
	v_or_b32_e32 v75, v73, v74
	v_and_b32_e32 v128, 12, v73
	v_lshl_add_u64 v[64:65], s[50:51], 0, v[128:129]
	v_lshl_add_u64 v[64:65], v[64:65], 0, s[0:1]
	s_mov_b64 s[0:1], 0x4000
	v_pk_mul_f32 v[70:71], v[66:67], s[20:21] op_sel_hi:[1,0]
	s_nop 0
	v_mul_f32_e32 v60, v60, v70
	v_mul_f32_e32 v56, v56, v71
	v_cvt_pk_fp8_f32 v78, v60, v56
	v_pk_mul_f32 v[68:69], v[68:69], s[20:21] op_sel_hi:[1,0]
	v_mov_b32_e32 v56, v131
	v_mul_f32_e32 v52, v52, v68
	v_mul_f32_e32 v48, v48, v69
	v_cvt_pk_fp8_f32 v78, v52, v48 op_sel:[0,0,1]
	v_lshlrev_b32_e32 v48, 4, v75
	v_bitop3_b32 v128, v186, 48, v48 bitop3:0x48
	v_mul_f32_e32 v48, v61, v70
	v_mul_f32_e32 v52, v57, v71
	v_cvt_pk_fp8_f32 v56, v48, v52
	v_mul_f32_e32 v53, v53, v68
	v_mul_f32_e32 v49, v49, v69
	v_mul_f32_e32 v48, v62, v70
	v_cvt_pk_fp8_f32 v56, v53, v49 op_sel:[0,0,1]
	v_mul_f32_e32 v49, v58, v71
	v_mov_b32_e32 v53, v131
	v_cvt_pk_fp8_f32 v53, v48, v49
	v_mul_f32_e32 v52, v54, v68
	v_mul_f32_e32 v50, v50, v69
	v_mul_f32_e32 v48, v63, v70
	v_cvt_pk_fp8_f32 v53, v52, v50 op_sel:[0,0,1]
	v_mul_f32_e32 v49, v59, v71
	v_mov_b32_e32 v52, v131
	v_cvt_pk_fp8_f32 v52, v48, v49
	v_mul_f32_e32 v44, v44, v70
	v_mul_f32_e32 v40, v40, v71
	v_mov_b32_e32 v54, v131
	v_cvt_pk_fp8_f32 v54, v44, v40
	v_mul_f32_e32 v50, v55, v68
	v_mul_f32_e32 v51, v51, v69
	v_cvt_pk_fp8_f32 v52, v50, v51 op_sel:[0,0,1]
	v_or_b32_e32 v50, 4, v130
	v_mul_f32_e32 v36, v36, v68
	v_mul_f32_e32 v32, v32, v69
	v_cvt_pk_fp8_f32 v54, v36, v32 op_sel:[0,0,1]
	v_lshrrev_b32_e32 v32, 2, v50
	v_bitop3_b32 v32, v32, v73, v74 bitop3:0x1e
	v_lshlrev_b32_e32 v32, 4, v32
	v_lshlrev_b32_e32 v48, 6, v50
	v_and_b32_e32 v50, 48, v32
	v_mul_f32_e32 v32, v45, v70
	v_mul_f32_e32 v40, v41, v71
	v_mov_b32_e32 v44, v131
	v_cvt_pk_fp8_f32 v44, v32, v40
; __device__ __forceinline__ unsigned cvt_pk4_fp8(float a, float b, float c, float d) { int w; asm("" : "=v"(w));     w = __builtin_amdgcn_cvt_pk_fp8_f32(a, b, w, false); w = __builtin_amdgcn_cvt_pk_fp8_f32(c, d, w, true); return (unsigned)w; }
; __device__ __forceinline__ int lane_id() { int l; asm volatile("v_mbcnt_lo_u32_b32 %0, -1, 0\n\tv_mbcnt_hi_u32_b32 %0, -1, %0" : "=v"(l)); return l; }
; #define PG8_BAR __builtin_amdgcn_s_barrier()
;     __device__ __forceinline__ void operator()(const f32x4 (&acc)[2][2][4][2], const Unit& u, int wr, int wc, int fr, int fq) const {
;     ...
;         for (int ai = 0; ai < 2; ++ai) { unsigned char* tb = V8T + ((size_t)((bb * NH + u.pn) * (SEQ / 64) + tile0 + 2 * ai)) * 8192 + 4 * ((fr >> 1) & 3);
;             const f32x4 c4 = *(const f32x4*)(rs + u.pm * BM + rl0 + ai * HALF) * (1.0f / W8_SCALE);
; #pragma unroll
;             for (int e = 0; e < 8; ++e) { const int D = dl0 + e, ch = 2 * (fr & 1) + (fr >> 3);
;                 const unsigned w = cvt_pk4_fp8(acc[ai][1][0][e >> 2][e & 3] * c4[0], acc[ai][1][1][e >> 2][e & 3] * c4[1], acc[ai][1][2][e >> 2][e & 3] * c4[2], acc[ai][1][3][e >> 2][e & 3] * c4[3]);
;                 *(unsigned*)(tb + D * 64 + (((ch ^ (D >> 2)) & 3) << 4)) = w; } }
;         asm volatile("s_waitcnt lgkmcnt(0)" ::: "memory"); __builtin_amdgcn_s_barrier(); asm volatile("" ::: "memory");
; template <bool FP8 = false, class Epi, class Sched>
; __device__ __forceinline__ void gemm_phase(LAS unsigned char* lds, const int K, const int lda, const int ldb, const Sched& S, const Epi& E, const int wid) {
;     ...
;         if (wr == 0) PG8_BAR;
;         { const int l2 = lane_id(); E(acc, cur, wr, wc, l2 & 15, l2 >> 4); }
;         if (!has_next) break;
; #pragma unroll
;         for (int a = 0; a < 2; ++a)
; #pragma unroll
;             for (int b = 0; b < 2; ++b)
; #pragma unroll
;                 for (int m = 0; m < 4; ++m)
; #pragma unroll
;                     for (int n = 0; n < 2; ++n) acc[a][b][m][n] = (f32x4){0.f, 0.f, 0.f, 0.f};
;         cur = nxt; cA = nA; cB = nB; ++ui;
;         if (wr == 1) PG8_BAR;
	v_or_b32_e32 v36, 5, v130
	v_mul_f32_e32 v37, v37, v68
	v_mul_f32_e32 v33, v33, v69
	v_lshlrev_b32_e32 v32, 6, v36
	v_lshrrev_b32_e32 v36, 2, v36
	v_cvt_pk_fp8_f32 v44, v37, v33 op_sel:[0,0,1]
	v_bitop3_b32 v36, v36, v73, v74 bitop3:0x1e
	v_ashrrev_i32_e32 v33, 31, v32
	v_lshlrev_b32_e32 v36, 4, v36
	v_lshl_add_u64 v[40:41], v[64:65], 0, v[32:33]
	v_and_b32_e32 v36, 48, v36
	v_mov_b32_e32 v37, v129
	v_lshl_add_u64 v[40:41], v[40:41], 0, v[36:37]
	global_store_dword v[40:41], v44, off
	v_mul_f32_e32 v40, v46, v70
	v_mul_f32_e32 v41, v42, v71
	v_mov_b32_e32 v42, v131
	v_cvt_pk_fp8_f32 v42, v40, v41
	v_lshlrev_b32_e32 v66, 6, v130
	v_ashrrev_i32_e32 v67, 31, v66
	v_lshl_add_u64 v[76:77], v[64:65], 0, v[66:67]
	v_or_b32_e32 v44, 6, v130
	v_mul_f32_e32 v38, v38, v68
	v_mul_f32_e32 v34, v34, v69
	v_lshl_add_u64 v[76:77], v[76:77], 0, v[128:129]
	v_ashrrev_i32_e32 v49, 31, v48
	v_cvt_pk_fp8_f32 v42, v38, v34 op_sel:[0,0,1]
	v_lshrrev_b32_e32 v34, 2, v44
	global_store_dword v[76:77], v53, off offset:128
	global_store_dword v[76:77], v52, off offset:192
	v_lshl_add_u64 v[52:53], v[64:65], 0, v[48:49]
	v_mov_b32_e32 v51, v129
	v_lshlrev_b32_e32 v40, 6, v44
	v_bitop3_b32 v34, v34, v73, v74 bitop3:0x1e
	v_lshl_add_u64 v[52:53], v[52:53], 0, v[50:51]
	v_ashrrev_i32_e32 v41, 31, v40
	v_lshlrev_b32_e32 v34, 4, v34
	global_store_dword v[52:53], v54, off
	v_lshl_add_u64 v[52:53], v[64:65], 0, v[40:41]
	v_and_b32_e32 v44, 48, v34
	v_mov_b32_e32 v45, v129
	v_lshl_add_u64 v[52:53], v[52:53], 0, v[44:45]
	global_store_dword v[52:53], v42, off
	v_mul_f32_e32 v38, v47, v70
	v_mul_f32_e32 v42, v43, v71
	v_mov_b32_e32 v46, v131
	v_cvt_pk_fp8_f32 v46, v38, v42
	v_or_b32_e32 v34, 7, v130
	v_mul_f32_e32 v39, v39, v68
	v_mul_f32_e32 v35, v35, v69
	v_lshlrev_b32_e32 v38, 6, v34
	v_lshrrev_b32_e32 v34, 2, v34
	v_cvt_pk_fp8_f32 v46, v39, v35 op_sel:[0,0,1]
	v_bitop3_b32 v34, v34, v73, v74 bitop3:0x1e
	v_ashrrev_i32_e32 v39, 31, v38
	v_lshlrev_b32_e32 v34, 4, v34
	v_lshl_add_u64 v[42:43], v[64:65], 0, v[38:39]
	v_and_b32_e32 v34, 48, v34
	v_mov_b32_e32 v35, v129
	v_lshl_add_u64 v[42:43], v[42:43], 0, v[34:35]
	global_store_dword v[76:77], v78, off
	global_store_dword v[76:77], v56, off offset:64
	global_store_dword v[42:43], v46, off
	v_mov_b32_e32 v52, v244
	v_mov_b32_e32 v53, v245
	v_mov_b32_e32 v54, v246
	v_mov_b32_e32 v55, v247
	v_mov_b32_e32 v56, v131
	v_lshl_add_u64 v[42:43], v[64:65], 0, s[0:1]
	s_mov_b64 s[4:5], -1
	v_pk_mul_f32 v[52:53], v[52:53], s[20:21] op_sel_hi:[1,0]
	s_nop 0
	v_mul_f32_e32 v28, v28, v52
	v_mul_f32_e32 v24, v24, v53
	v_cvt_pk_fp8_f32 v56, v28, v24
	v_pk_mul_f32 v[46:47], v[54:55], s[20:21] op_sel_hi:[1,0]
	v_mov_b32_e32 v24, v131
	v_mul_f32_e32 v20, v20, v46
	v_mul_f32_e32 v16, v16, v47
	v_cvt_pk_fp8_f32 v56, v20, v16 op_sel:[0,0,1]
	v_mul_f32_e32 v16, v29, v52
	v_mul_f32_e32 v20, v25, v53
	v_cvt_pk_fp8_f32 v24, v16, v20
	v_mul_f32_e32 v21, v21, v46
	v_mul_f32_e32 v17, v17, v47
	v_mul_f32_e32 v16, v30, v52
	v_cvt_pk_fp8_f32 v24, v21, v17 op_sel:[0,0,1]
	v_mul_f32_e32 v17, v26, v53
	v_mov_b32_e32 v21, v131
	v_cvt_pk_fp8_f32 v21, v16, v17
	v_mul_f32_e32 v20, v22, v46
	v_mul_f32_e32 v18, v18, v47
	v_mul_f32_e32 v16, v31, v52
	v_cvt_pk_fp8_f32 v21, v20, v18 op_sel:[0,0,1]
	v_mul_f32_e32 v17, v27, v53
	v_mov_b32_e32 v20, v131
	v_cvt_pk_fp8_f32 v20, v16, v17
	v_mul_f32_e32 v18, v23, v46
	v_mul_f32_e32 v19, v19, v47
	v_mul_f32_e32 v12, v12, v52
	v_cvt_pk_fp8_f32 v20, v18, v19 op_sel:[0,0,1]
	v_mul_f32_e32 v8, v8, v53
	v_mov_b32_e32 v18, v131
	v_cvt_pk_fp8_f32 v18, v12, v8
	v_mul_f32_e32 v4, v4, v46
	v_mul_f32_e32 v0, v0, v47
	v_mov_b32_e32 v8, v131
	v_cvt_pk_fp8_f32 v18, v4, v0 op_sel:[0,0,1]
	v_mul_f32_e32 v0, v13, v52
	v_mul_f32_e32 v4, v9, v53
	v_cvt_pk_fp8_f32 v8, v0, v4
	v_mul_f32_e32 v5, v5, v46
	v_mul_f32_e32 v1, v1, v47
	v_mul_f32_e32 v4, v6, v46
	v_cvt_pk_fp8_f32 v8, v5, v1 op_sel:[0,0,1]
	v_lshl_add_u64 v[0:1], v[42:43], 0, v[32:33]
	v_lshl_add_u64 v[0:1], v[0:1], 0, v[36:37]
	v_mov_b32_e32 v5, v131
	global_store_dword v[0:1], v8, off
	v_mul_f32_e32 v0, v14, v52
	v_mul_f32_e32 v1, v10, v53
	v_cvt_pk_fp8_f32 v5, v0, v1
	v_mul_f32_e32 v2, v2, v47
	v_lshl_add_u64 v[0:1], v[42:43], 0, v[40:41]
	v_lshl_add_u64 v[0:1], v[0:1], 0, v[44:45]
	v_cvt_pk_fp8_f32 v5, v4, v2 op_sel:[0,0,1]
	v_mul_f32_e32 v2, v7, v46
	v_mul_f32_e32 v3, v3, v47
	v_lshl_add_u64 v[54:55], v[42:43], 0, v[66:67]
	global_store_dword v[0:1], v5, off
	v_mul_f32_e32 v0, v15, v52
	v_mul_f32_e32 v1, v11, v53
	v_cvt_pk_fp8_f32 v131, v0, v1
	v_lshl_add_u64 v[16:17], v[42:43], 0, v[48:49]
	v_lshl_add_u64 v[0:1], v[42:43], 0, v[38:39]
	v_lshl_add_u64 v[54:55], v[54:55], 0, v[128:129]
	v_cvt_pk_fp8_f32 v131, v2, v3 op_sel:[0,0,1]
	v_lshl_add_u64 v[16:17], v[16:17], 0, v[50:51]
	v_lshl_add_u64 v[0:1], v[0:1], 0, v[34:35]
	global_store_dword v[54:55], v56, off
	global_store_dword v[54:55], v24, off offset:64
	global_store_dword v[54:55], v21, off offset:128
	global_store_dword v[54:55], v20, off offset:192
	global_store_dword v[16:17], v18, off
	global_store_dword v[0:1], v131, off
	s_waitcnt lgkmcnt(0)
	s_barrier
	s_cbranch_vccnz .LBB0_390
	s_andn2_b64 vcc, exec, s[6:7]
	s_cbranch_vccnz .LBB0_389
	s_barrier
	s_branch .LBB0_389

; __global__ void __launch_bounds__(512, 2) fwd_kernel(Params p) {
;     ...
;         const int grp = (bx >> 3) % 5;
;         constexpr int CNIT = NE * 16 * 128 + NE * 16 * 64;
;         const bool compact = (G == 256);
;         const int gcus = grp < 2 ? 56 : 48, grank = (bx & 7) * (gcus / 8) + (bx >> 3) / 5,     gstart = (grp < 2 ? grp * 56 : 112 + (grp - 2) * 48) * (CNIT / 256);
;         const int cfirst = compact ? gstart + grank * 8 + wave : gw, cstride = compact ? gcus * 8 : NGW, cend = compact ? gstart + gcus * (CNIT / 256) : CNIT;
.LBB0_475:
	s_or_b64 exec, exec, s[4:5]
	s_ashr_i32 s94, s2, 3
	s_mul_hi_i32 s0, s94, 0x66666667
	s_lshr_b32 s1, s0, 31
	s_ashr_i32 s0, s0, 1
	s_add_i32 s0, s0, s1
	s_mul_i32 s1, s0, 5
	s_sub_i32 s35, s94, s1
	s_cmp_lt_i32 s35, 2
	s_cselect_b64 s[4:5], -1, 0
	s_cmp_gt_i32 s35, 1
	s_waitcnt lgkmcnt(0)
	s_barrier
	s_nop 0
	s_nop 0
	s_nop 0
	s_nop 0
	s_nop 0
	s_nop 0
	s_nop 0
	s_nop 0
	s_nop 0
	s_nop 0
	s_nop 0
	s_nop 0
	s_cbranch_scc0 .LBB0_477
	s_mul_i32 s1, s35, 48
	s_add_i32 s1, s1, 16
	s_cbranch_execz .LBB0_478
	s_branch .LBB0_479

; template <bool FP8 = false, class Epi, class Sched>
; __device__ __forceinline__ void gemm_phase(LAS unsigned char* lds, const int K, const int lda, const int ldb, const Sched& S, const Epi& E, const int wid) {
;     ...
; #pragma unroll
;         for (int a = 0; a < 2; ++a)
; #pragma unroll
;             for (int b = 0; b < 2; ++b)
; #pragma unroll
;                 for (int m = 0; m < 4; ++m)
; #pragma unroll
;                     for (int n = 0; n < 2; ++n) acc[a][b][m][n] = (f32x4){0.f, 0.f, 0.f, 0.f};
.LBB0_839:
	v_mov_b32_e32 v0, 0
	s_mov_b64 s[56:57], 0
	s_mov_b64 s[50:51], -1
	s_mov_b64 s[54:55], 0
	v_mov_b32_e32 v1, v0
	v_mov_b64_e32 v[2:3], 0
	v_mov_b64_e32 v[4:5], 0
	v_mov_b64_e32 v[6:7], 0
	s_waitcnt vmcnt(14)
	v_mov_b64_e32 v[16:17], 0
	v_mov_b64_e32 v[18:19], 0
	v_mov_b64_e32 v[20:21], 0
	v_mov_b64_e32 v[22:23], 0
	s_waitcnt vmcnt(10)
	v_mov_b64_e32 v[32:33], 0
	v_mov_b64_e32 v[34:35], 0
	v_mov_b64_e32 v[36:37], 0
	v_mov_b64_e32 v[38:39], 0
	s_waitcnt vmcnt(4)
	v_mov_b64_e32 v[56:57], 0
	v_mov_b64_e32 v[58:59], 0
	v_mov_b64_e32 v[60:61], 0
	v_mov_b64_e32 v[62:63], 0
	v_mov_b64_e32 v[8:9], 0
	v_mov_b64_e32 v[10:11], 0
	v_mov_b64_e32 v[12:13], 0
	v_mov_b64_e32 v[14:15], 0
	v_mov_b64_e32 v[24:25], 0
	v_mov_b64_e32 v[26:27], 0
	v_mov_b64_e32 v[28:29], 0
	v_mov_b64_e32 v[30:31], 0
	v_mov_b64_e32 v[48:49], 0
	v_mov_b64_e32 v[50:51], 0
	v_mov_b64_e32 v[52:53], 0
	v_mov_b64_e32 v[54:55], 0
	v_mov_b64_e32 v[72:73], 0
	v_mov_b64_e32 v[74:75], 0
	v_mov_b64_e32 v[76:77], 0
	v_mov_b64_e32 v[78:79], 0
	v_mov_b64_e32 v[80:81], 0
	v_mov_b64_e32 v[82:83], 0
	v_mov_b64_e32 v[84:85], 0
	v_mov_b64_e32 v[86:87], 0
	v_mov_b64_e32 v[96:97], 0
	v_mov_b64_e32 v[98:99], 0
	v_mov_b64_e32 v[100:101], 0
	v_mov_b64_e32 v[102:103], 0
	v_mov_b64_e32 v[112:113], 0
	v_mov_b64_e32 v[114:115], 0
	v_mov_b64_e32 v[116:117], 0
	v_mov_b64_e32 v[118:119], 0
	v_mov_b64_e32 v[128:129], 0
	v_mov_b64_e32 v[130:131], 0
	v_mov_b64_e32 v[132:133], 0
	v_mov_b64_e32 v[134:135], 0
	v_mov_b64_e32 v[88:89], 0
	v_mov_b32_e32 v90, v0
	v_mov_b32_e32 v91, v0
	v_mov_b32_e32 v92, v0
	v_mov_b32_e32 v93, v0
	v_mov_b32_e32 v94, v0
	v_mov_b32_e32 v95, v0
	v_mov_b32_e32 v104, v0
	v_mov_b32_e32 v105, v0
	v_mov_b32_e32 v106, v0
	v_mov_b32_e32 v107, v0
	v_mov_b32_e32 v108, v0
	v_mov_b32_e32 v109, v0
	v_mov_b32_e32 v110, v0
	v_mov_b32_e32 v111, v0
	v_mov_b32_e32 v120, v0
	v_mov_b32_e32 v121, v0
	v_mov_b32_e32 v122, v0
	v_mov_b32_e32 v123, v0
	v_mov_b32_e32 v124, v0
	v_mov_b32_e32 v125, v0
	v_mov_b32_e32 v126, v0
	v_mov_b32_e32 v127, v0
	v_mov_b32_e32 v136, v0
	v_mov_b32_e32 v137, v0
	v_mov_b32_e32 v138, v0
	v_mov_b32_e32 v139, v0
	v_mov_b32_e32 v140, v0
	v_mov_b32_e32 v141, v0
	v_mov_b32_e32 v142, v0
	v_mov_b32_e32 v143, v0

; __device__ __forceinline__ unsigned cvt_pk_bf16(float lo, float hi) { unsigned r; asm volatile("v_cvt_pk_bf16_f32 %0, %1, %2" : "=v"(r) : "v"(lo), "v"(hi)); return r; }
; __device__ __forceinline__ float bf_lo(unsigned w) { return __uint_as_float(w << 16); }
; __device__ __forceinline__ float bf_hi(unsigned w) { return __uint_as_float(w & 0xffff0000u); }
;     __device__ __forceinline__ void operator()(const f32x4 (&acc)[2][2][4][2], const Unit& u, int wr, int wc, int fr, int fq) const {
;         const int row0 = u.pm * BM + wr * 64 + fr, col0 = u.pn * BM + wc * 32 + 8 * fq;
;     ...
;         f32x4 sv[2][2];
; #pragma unroll
;         for (int bj = 0; bj < 2; ++bj)
; #pragma unroll
;             for (int n = 0; n < 2; ++n) sv[bj][n] = *(const f32x4*)(s_pool + col0 + bj * HALF + 4 * n);
; #pragma unroll
;         for (int ai = 0; ai < 2; ++ai)
; #pragma unroll
;             for (int m = 0; m < 4; ++m) { const size_t r = (size_t)(row0 + ai * HALF + m * 16); bf16_t* rowp = O + r * DM + col0; const unsigned char* gr = G8 + r * 4096 + col0; const bf16_t* yr = YA + r * DM + col0;
; #pragma unroll
;                 for (int bj = 0; bj < 2; ++bj) { const u32x2 g = *(const u32x2*)(gr + 2048 + bj * HALF), a = *(const u32x2*)(gr + bj * HALF); const u32x4 y = *(const u32x4*)(yr + bj * HALF);
;                     const f32x4 v0 = acc[ai][bj][m][0] * sv[bj][0], v1 = acc[ai][bj][m][1] * sv[bj][1];
;                     u32x4 w;
;                     w.x = cvt_pk_bf16(v0[0] * U8F(g.x, 0) + U8F(a.x, 0) * bf_lo(y.x), v0[1] * U8F(g.x, 1) + U8F(a.x, 1) * bf_hi(y.x));
;                     w.y = cvt_pk_bf16(v0[2] * U8F(g.x, 2) + U8F(a.x, 2) * bf_lo(y.y), v0[3] * U8F(g.x, 3) + U8F(a.x, 3) * bf_hi(y.y));
;                     w.z = cvt_pk_bf16(v1[0] * U8F(g.y, 0) + U8F(a.y, 0) * bf_lo(y.z), v1[1] * U8F(g.y, 1) + U8F(a.y, 1) * bf_hi(y.z));
;                     w.w = cvt_pk_bf16(v1[2] * U8F(g.y, 2) + U8F(a.y, 2) * bf_lo(y.w), v1[3] * U8F(g.y, 3) + U8F(a.y, 3) * bf_hi(y.w));
;                     *(u32x4*)(rowp + bj * HALF) = w; } }
.LBB0_843:
	s_lshl_b32 s19, s26, 8
	s_lshl_b32 s26, s27, 8
	v_mbcnt_lo_u32_b32 v40, -1, 0
	v_mbcnt_hi_u32_b32 v40, -1, v40
	s_or_b32 s35, s26, s84
	s_load_dwordx2 s[26:27], s[88:89], 0x68
	s_add_i32 s19, s19, s34
	v_ashrrev_i32_e32 v41, 1, v40
	v_and_b32_e32 v41, -8, v41
	v_and_or_b32 v150, v40, 15, s19
	v_add_u32_e32 v146, s35, v41
	v_ashrrev_i32_e32 v151, 31, v150
	v_ashrrev_i32_e32 v147, 31, v146
	v_lshlrev_b64 v[148:149], 12, v[150:151]
	s_waitcnt lgkmcnt(0)
	v_lshl_add_u64 v[44:45], v[146:147], 2, s[26:27]
	v_lshl_add_u64 v[40:41], s[42:43], 0, v[148:149]
	global_load_dwordx4 v[64:67], v[44:45], off offset:16
	global_load_dwordx4 v[68:71], v[44:45], off
	v_lshlrev_b64 v[144:145], 1, v[146:147]
	v_lshl_add_u64 v[166:167], v[40:41], 0, v[146:147]
	v_lshl_add_u64 v[40:41], s[52:53], 0, v[148:149]
	v_lshl_add_u64 v[168:169], v[40:41], 0, v[144:145]
	global_load_dwordx4 v[162:165], v[168:169], off
	global_load_dwordx2 v[170:171], v[166:167], off
	global_load_dwordx2 v[172:173], v[166:167], off offset:2048
	global_load_dwordx4 v[40:43], v[44:45], off offset:528
	s_nop 0
	global_load_dwordx4 v[44:47], v[44:45], off offset:512
	v_add_u32_e32 v250, v148, v144
	v_add_u32_e32 v251, v148, v146
	v_mov_b32_e32 v253, v250
	global_load_dwordx4 v[194:197], v253, s[52:53] offset:256
	v_mov_b32_e32 v253, v251
	global_load_dwordx2 v[198:199], v253, s[42:43] offset:128
	global_load_dwordx2 v[200:201], v253, s[42:43] offset:2176
	v_add_u32_e32 v253, 0x10000, v250
	global_load_dwordx4 v[202:205], v253, s[52:53]
	v_add_u32_e32 v253, 0x10000, v251
	global_load_dwordx2 v[206:207], v253, s[42:43]
	global_load_dwordx2 v[208:209], v253, s[42:43] offset:2048
	v_add_u32_e32 v253, 0x10000, v250
	global_load_dwordx4 v[210:213], v253, s[52:53] offset:256
	v_add_u32_e32 v253, 0x10000, v251
	global_load_dwordx2 v[214:215], v253, s[42:43] offset:128
	global_load_dwordx2 v[216:217], v253, s[42:43] offset:2176
	v_add_u32_e32 v253, 0x20000, v250
	global_load_dwordx4 v[218:221], v253, s[52:53]
	v_add_u32_e32 v253, 0x20000, v251
	global_load_dwordx2 v[222:223], v253, s[42:43]
	global_load_dwordx2 v[224:225], v253, s[42:43] offset:2048
	v_add_u32_e32 v253, 0x20000, v250
	global_load_dwordx4 v[226:229], v253, s[52:53] offset:256
	v_add_u32_e32 v253, 0x20000, v251
	global_load_dwordx2 v[230:231], v253, s[42:43] offset:128
	global_load_dwordx2 v[232:233], v253, s[42:43] offset:2176
	v_add_u32_e32 v253, 0x30000, v250
	global_load_dwordx4 v[234:237], v253, s[52:53]
	v_add_u32_e32 v253, 0x30000, v251
	global_load_dwordx2 v[238:239], v253, s[42:43]
	global_load_dwordx2 v[240:241], v253, s[42:43] offset:2048
	v_add_u32_e32 v253, 0x30000, v250
	global_load_dwordx4 v[242:245], v253, s[52:53] offset:256
	v_add_u32_e32 v253, 0x30000, v251
	global_load_dwordx2 v[246:247], v253, s[42:43] offset:128
	global_load_dwordx2 v[248:249], v253, s[42:43] offset:2176
	s_mov_b64 s[26:27], 0x80000
	s_andn2_b64 vcc, exec, s[24:25]
	s_mov_b64 s[24:25], -1
	s_waitcnt vmcnt(27)
	v_pk_mul_f32 v[138:139], v[138:139], v[66:67]
	s_waitcnt vmcnt(26)
	v_pk_mul_f32 v[142:143], v[142:143], v[70:71]
	v_pk_mul_f32 v[140:141], v[140:141], v[68:69]
	v_pk_mul_f32 v[136:137], v[136:137], v[64:65]
	s_waitcnt vmcnt(24)
	v_cvt_f32_ubyte0_e32 v177, v170
	s_waitcnt vmcnt(23)
	v_cvt_f32_ubyte0_e32 v176, v172
	v_cvt_f32_ubyte1_e32 v181, v170
	v_cvt_f32_ubyte1_e32 v180, v172
	v_cvt_f32_ubyte2_e32 v183, v170
	v_cvt_f32_ubyte2_e32 v182, v172
	v_cvt_f32_ubyte3_e32 v185, v170
	v_cvt_f32_ubyte3_e32 v184, v172
	v_lshlrev_b32_e32 v175, 16, v162
	v_mov_b32_e32 v174, v140
	v_and_b32_e32 v179, 0xffff0000, v162
	v_mov_b32_e32 v178, v141
	v_lshlrev_b32_e32 v141, 16, v163
	v_mov_b32_e32 v140, v142
	v_and_b32_e32 v163, 0xffff0000, v163
	v_mov_b32_e32 v162, v143
	v_lshlrev_b32_e32 v143, 16, v164
	v_cvt_f32_ubyte0_e32 v186, v173
	v_mov_b32_e32 v142, v136
	v_and_b32_e32 v189, 0xffff0000, v164
	v_cvt_f32_ubyte1_e32 v190, v173
	v_cvt_f32_ubyte2_e32 v192, v173
	v_mov_b32_e32 v136, v138
	v_cvt_f32_ubyte3_e32 v170, v173
	v_mov_b32_e32 v164, v139
	v_pk_mul_f32 v[138:139], v[176:177], s[16:17] op_sel_hi:[1,0]
	v_pk_mul_f32 v[172:173], v[180:181], s[16:17] op_sel_hi:[1,0]
	v_pk_mul_f32 v[176:177], v[182:183], s[16:17] op_sel_hi:[1,0]
	v_pk_mul_f32 v[180:181], v[184:185], s[16:17] op_sel_hi:[1,0]
	v_cvt_f32_ubyte0_e32 v187, v171
	v_cvt_f32_ubyte1_e32 v191, v171
	v_cvt_f32_ubyte2_e32 v193, v171
	v_cvt_f32_ubyte3_e32 v171, v171
	v_pk_mul_f32 v[140:141], v[140:141], v[176:177]
	v_pk_mul_f32 v[162:163], v[162:163], v[180:181]
	v_mov_b32_e32 v188, v137
	v_lshlrev_b32_e32 v137, 16, v165
	v_and_b32_e32 v165, 0xffff0000, v165
	v_pk_mul_f32 v[182:183], v[186:187], s[16:17] op_sel_hi:[1,0]
	v_pk_mul_f32 v[184:185], v[190:191], s[16:17] op_sel_hi:[1,0]
	v_pk_mul_f32 v[186:187], v[192:193], s[16:17] op_sel_hi:[1,0]
	v_pk_mul_f32 v[170:171], v[170:171], s[16:17] op_sel_hi:[1,0]
	v_pk_mul_f32 v[138:139], v[174:175], v[138:139]
	v_pk_mul_f32 v[172:173], v[178:179], v[172:173]
	v_add_f32_e32 v140, v140, v141
	v_add_f32_e32 v141, v162, v163
	v_lshl_add_u64 v[162:163], s[4:5], 0, v[148:149]
	v_pk_mul_f32 v[142:143], v[142:143], v[182:183]
	v_pk_mul_f32 v[174:175], v[188:189], v[184:185]
	v_pk_mul_f32 v[136:137], v[136:137], v[186:187]
	v_pk_mul_f32 v[164:165], v[164:165], v[170:171]
	v_add_f32_e32 v138, v138, v139
	v_add_f32_e32 v139, v172, v173
	v_lshl_add_u64 v[162:163], v[162:163], 0, v[144:145]
	v_add_f32_e32 v142, v142, v143
	v_add_f32_e32 v143, v174, v175
	v_add_f32_e32 v151, v136, v137
	v_add_f32_e32 v161, v164, v165
	v_cvt_pk_bf16_f32 v136, v138, v139
	v_cvt_pk_bf16_f32 v137, v140, v141
	v_cvt_pk_bf16_f32 v138, v142, v143
	v_cvt_pk_bf16_f32 v139, v151, v161
	global_store_dwordx4 v[162:163], v[136:139], off
	s_waitcnt vmcnt(19)
; __device__ __forceinline__ unsigned cvt_pk_bf16(float lo, float hi) { unsigned r; asm volatile("v_cvt_pk_bf16_f32 %0, %1, %2" : "=v"(r) : "v"(lo), "v"(hi)); return r; }
; __device__ __forceinline__ float bf_lo(unsigned w) { return __uint_as_float(w << 16); }
; __device__ __forceinline__ float bf_hi(unsigned w) { return __uint_as_float(w & 0xffff0000u); }
;     __device__ __forceinline__ void operator()(const f32x4 (&acc)[2][2][4][2], const Unit& u, int wr, int wc, int fr, int fq) const {
;     ...
; #pragma unroll
;         for (int ai = 0; ai < 2; ++ai)
; #pragma unroll
;             for (int m = 0; m < 4; ++m) { const size_t r = (size_t)(row0 + ai * HALF + m * 16); bf16_t* rowp = O + r * DM + col0; const unsigned char* gr = G8 + r * 4096 + col0; const bf16_t* yr = YA + r * DM + col0;
; #pragma unroll
;                 for (int bj = 0; bj < 2; ++bj) { const u32x2 g = *(const u32x2*)(gr + 2048 + bj * HALF), a = *(const u32x2*)(gr + bj * HALF); const u32x4 y = *(const u32x4*)(yr + bj * HALF);
;                     const f32x4 v0 = acc[ai][bj][m][0] * sv[bj][0], v1 = acc[ai][bj][m][1] * sv[bj][1];
;                     u32x4 w;
;                     w.x = cvt_pk_bf16(v0[0] * U8F(g.x, 0) + U8F(a.x, 0) * bf_lo(y.x), v0[1] * U8F(g.x, 1) + U8F(a.x, 1) * bf_hi(y.x));
;                     w.y = cvt_pk_bf16(v0[2] * U8F(g.x, 2) + U8F(a.x, 2) * bf_lo(y.y), v0[3] * U8F(g.x, 3) + U8F(a.x, 3) * bf_hi(y.y));
;                     w.z = cvt_pk_bf16(v1[0] * U8F(g.y, 0) + U8F(a.y, 0) * bf_lo(y.z), v1[1] * U8F(g.y, 1) + U8F(a.y, 1) * bf_hi(y.z));
;                     w.w = cvt_pk_bf16(v1[2] * U8F(g.y, 2) + U8F(a.y, 2) * bf_lo(y.w), v1[3] * U8F(g.y, 3) + U8F(a.y, 3) * bf_hi(y.w));
;                     *(u32x4*)(rowp + bj * HALF) = w; } }
	v_pk_mul_f32 v[134:135], v[134:135], v[46:47]
	v_pk_mul_f32 v[132:133], v[132:133], v[44:45]
	v_pk_mul_f32 v[130:131], v[130:131], v[42:43]
	v_pk_mul_f32 v[128:129], v[128:129], v[40:41]
	v_mov_b32_e32 v168, v133
	v_mov_b32_e32 v170, v135
	v_mov_b32_e32 v172, v129
	v_mov_b32_e32 v174, v131
	v_or_b32_e32 v164, 16, v150
	v_ashrrev_i32_e32 v165, 31, v164
	v_lshlrev_b64 v[164:165], 12, v[164:165]
	v_lshl_add_u64 v[166:167], s[52:53], 0, v[164:165]
	v_lshl_add_u64 v[166:167], v[166:167], 0, v[144:145]
	v_pk_mul_f32 v[126:127], v[126:127], v[70:71]
	v_pk_mul_f32 v[124:125], v[124:125], v[68:69]
	v_pk_mul_f32 v[122:123], v[122:123], v[66:67]
	v_pk_mul_f32 v[120:121], v[120:121], v[64:65]
	v_pk_mul_f32 v[118:119], v[118:119], v[46:47]
	v_pk_mul_f32 v[116:117], v[116:117], v[44:45]
	v_pk_mul_f32 v[114:115], v[114:115], v[42:43]
	v_pk_mul_f32 v[112:113], v[112:113], v[40:41]
	v_pk_mul_f32 v[110:111], v[110:111], v[70:71]
	v_pk_mul_f32 v[108:109], v[108:109], v[68:69]
	v_pk_mul_f32 v[106:107], v[106:107], v[66:67]
	v_pk_mul_f32 v[104:105], v[104:105], v[64:65]
	v_pk_mul_f32 v[102:103], v[102:103], v[46:47]
	v_pk_mul_f32 v[100:101], v[100:101], v[44:45]
	v_pk_mul_f32 v[98:99], v[98:99], v[42:43]
	v_pk_mul_f32 v[96:97], v[96:97], v[40:41]
	v_pk_mul_f32 v[94:95], v[94:95], v[70:71]
	v_pk_mul_f32 v[92:93], v[92:93], v[68:69]
	v_pk_mul_f32 v[90:91], v[90:91], v[66:67]
	v_pk_mul_f32 v[88:89], v[88:89], v[64:65]
	v_pk_mul_f32 v[86:87], v[86:87], v[46:47]
	v_pk_mul_f32 v[84:85], v[84:85], v[44:45]
	v_pk_mul_f32 v[82:83], v[82:83], v[42:43]
	v_pk_mul_f32 v[80:81], v[80:81], v[40:41]
	v_pk_mul_f32 v[78:79], v[78:79], v[70:71]
	v_pk_mul_f32 v[76:77], v[76:77], v[68:69]
	v_pk_mul_f32 v[74:75], v[74:75], v[66:67]
	v_pk_mul_f32 v[72:73], v[72:73], v[64:65]
	v_pk_mul_f32 v[62:63], v[62:63], v[46:47]
	v_pk_mul_f32 v[60:61], v[60:61], v[44:45]
	v_pk_mul_f32 v[58:59], v[58:59], v[42:43]
	v_pk_mul_f32 v[56:57], v[56:57], v[40:41]
	v_pk_mul_f32 v[54:55], v[54:55], v[70:71]
	v_pk_mul_f32 v[52:53], v[52:53], v[68:69]
	v_pk_mul_f32 v[50:51], v[50:51], v[66:67]
	v_pk_mul_f32 v[48:49], v[48:49], v[64:65]
	v_pk_mul_f32 v[38:39], v[38:39], v[46:47]
	v_pk_mul_f32 v[36:37], v[36:37], v[44:45]
	v_pk_mul_f32 v[34:35], v[34:35], v[42:43]
	v_pk_mul_f32 v[32:33], v[32:33], v[40:41]
	v_pk_mul_f32 v[30:31], v[30:31], v[70:71]
	v_pk_mul_f32 v[28:29], v[28:29], v[68:69]
	v_pk_mul_f32 v[26:27], v[26:27], v[66:67]
	v_pk_mul_f32 v[24:25], v[24:25], v[64:65]
	v_pk_mul_f32 v[22:23], v[22:23], v[46:47]
	v_pk_mul_f32 v[20:21], v[20:21], v[44:45]
	v_pk_mul_f32 v[18:19], v[18:19], v[42:43]
	v_pk_mul_f32 v[16:17], v[16:17], v[40:41]
	v_pk_mul_f32 v[14:15], v[14:15], v[70:71]
	v_pk_mul_f32 v[12:13], v[12:13], v[68:69]
	v_pk_mul_f32 v[10:11], v[10:11], v[66:67]
	v_pk_mul_f32 v[8:9], v[8:9], v[64:65]
	v_pk_mul_f32 v[6:7], v[6:7], v[46:47]
	v_pk_mul_f32 v[4:5], v[4:5], v[44:45]
	v_pk_mul_f32 v[2:3], v[2:3], v[42:43]
	v_pk_mul_f32 v[0:1], v[0:1], v[40:41]
	v_lshlrev_b32_e32 v133, 16, v194
	v_and_b32_e32 v169, 0xffff0000, v194
	v_lshlrev_b32_e32 v135, 16, v195
	v_and_b32_e32 v171, 0xffff0000, v195
	v_lshlrev_b32_e32 v129, 16, v196
	v_and_b32_e32 v173, 0xffff0000, v196
	v_lshlrev_b32_e32 v131, 16, v197
	v_and_b32_e32 v175, 0xffff0000, v197
	v_cvt_f32_ubyte0_e32 v141, v198
	v_cvt_f32_ubyte0_e32 v140, v200
	v_cvt_f32_ubyte1_e32 v143, v198
	v_cvt_f32_ubyte1_e32 v142, v200
	v_cvt_f32_ubyte2_e32 v177, v198
	v_cvt_f32_ubyte2_e32 v176, v200
	v_cvt_f32_ubyte3_e32 v179, v198
	v_cvt_f32_ubyte3_e32 v178, v200
	v_cvt_f32_ubyte0_e32 v181, v199
	v_cvt_f32_ubyte0_e32 v180, v201
	v_cvt_f32_ubyte1_e32 v183, v199
	v_cvt_f32_ubyte1_e32 v182, v201
	v_cvt_f32_ubyte2_e32 v185, v199
	v_cvt_f32_ubyte2_e32 v184, v201
	v_cvt_f32_ubyte3_e32 v137, v199
	v_cvt_f32_ubyte3_e32 v136, v201
	v_pk_mul_f32 v[138:139], v[140:141], s[16:17] op_sel_hi:[1,0]
	v_pk_mul_f32 v[140:141], v[142:143], s[16:17] op_sel_hi:[1,0]
	v_pk_mul_f32 v[142:143], v[176:177], s[16:17] op_sel_hi:[1,0]
	v_pk_mul_f32 v[176:177], v[178:179], s[16:17] op_sel_hi:[1,0]
	v_pk_mul_f32 v[178:179], v[180:181], s[16:17] op_sel_hi:[1,0]
	v_pk_mul_f32 v[180:181], v[182:183], s[16:17] op_sel_hi:[1,0]
	v_pk_mul_f32 v[182:183], v[184:185], s[16:17] op_sel_hi:[1,0]
	v_pk_mul_f32 v[136:137], v[136:137], s[16:17] op_sel_hi:[1,0]
	v_pk_mul_f32 v[130:131], v[130:131], v[182:183]
	v_pk_mul_f32 v[136:137], v[174:175], v[136:137]
	v_pk_mul_f32 v[132:133], v[132:133], v[138:139]
	v_pk_mul_f32 v[138:139], v[168:169], v[140:141]
	v_pk_mul_f32 v[134:135], v[134:135], v[142:143]
	v_pk_mul_f32 v[140:141], v[170:171], v[176:177]
	v_pk_mul_f32 v[128:129], v[128:129], v[178:179]
	v_pk_mul_f32 v[142:143], v[172:173], v[180:181]
	v_add_f32_e32 v131, v130, v131
	v_add_f32_e32 v136, v136, v137
	v_add_f32_e32 v132, v132, v133
	v_add_f32_e32 v133, v138, v139
	v_add_f32_e32 v134, v134, v135
	v_add_f32_e32 v135, v140, v141
	v_add_f32_e32 v138, v128, v129
	v_add_f32_e32 v139, v142, v143
	v_cvt_pk_bf16_f32 v128, v132, v133
	v_cvt_pk_bf16_f32 v129, v134, v135
	v_cvt_pk_bf16_f32 v130, v138, v139
	v_cvt_pk_bf16_f32 v131, v131, v136
	v_lshl_add_u64 v[136:137], s[42:43], 0, v[164:165]
	v_lshl_add_u64 v[136:137], v[136:137], 0, v[146:147]
	v_add_u32_e32 v253, 0x80000, v250
	global_load_dwordx4 v[194:197], v253, s[52:53]
	v_add_u32_e32 v253, 0x80000, v251
	global_load_dwordx2 v[198:199], v253, s[42:43]
	global_load_dwordx2 v[200:201], v253, s[42:43] offset:2048
	global_store_dwordx4 v[162:163], v[128:131], off offset:256
	v_mov_b32_e32 v138, v125
	v_mov_b32_e32 v140, v127
	v_mov_b32_e32 v142, v121
	v_mov_b32_e32 v162, v123
	s_waitcnt vmcnt(20)
; __device__ __forceinline__ unsigned cvt_pk_bf16(float lo, float hi) { unsigned r; asm volatile("v_cvt_pk_bf16_f32 %0, %1, %2" : "=v"(r) : "v"(lo), "v"(hi)); return r; }
; __device__ __forceinline__ float bf_lo(unsigned w) { return __uint_as_float(w << 16); }
; __device__ __forceinline__ float bf_hi(unsigned w) { return __uint_as_float(w & 0xffff0000u); }
;     __device__ __forceinline__ void operator()(const f32x4 (&acc)[2][2][4][2], const Unit& u, int wr, int wc, int fr, int fq) const {
;     ...
;             for (int m = 0; m < 4; ++m) { const size_t r = (size_t)(row0 + ai * HALF + m * 16); bf16_t* rowp = O + r * DM + col0; const unsigned char* gr = G8 + r * 4096 + col0; const bf16_t* yr = YA + r * DM + col0;
; #pragma unroll
;                 for (int bj = 0; bj < 2; ++bj) { const u32x2 g = *(const u32x2*)(gr + 2048 + bj * HALF), a = *(const u32x2*)(gr + bj * HALF); const u32x4 y = *(const u32x4*)(yr + bj * HALF);
;                     const f32x4 v0 = acc[ai][bj][m][0] * sv[bj][0], v1 = acc[ai][bj][m][1] * sv[bj][1];
;                     u32x4 w;
;                     w.x = cvt_pk_bf16(v0[0] * U8F(g.x, 0) + U8F(a.x, 0) * bf_lo(y.x), v0[1] * U8F(g.x, 1) + U8F(a.x, 1) * bf_hi(y.x));
;                     w.y = cvt_pk_bf16(v0[2] * U8F(g.x, 2) + U8F(a.x, 2) * bf_lo(y.y), v0[3] * U8F(g.x, 3) + U8F(a.x, 3) * bf_hi(y.y));
;                     w.z = cvt_pk_bf16(v1[0] * U8F(g.y, 0) + U8F(a.y, 0) * bf_lo(y.z), v1[1] * U8F(g.y, 1) + U8F(a.y, 1) * bf_hi(y.z));
;                     w.w = cvt_pk_bf16(v1[2] * U8F(g.y, 2) + U8F(a.y, 2) * bf_lo(y.w), v1[3] * U8F(g.y, 3) + U8F(a.y, 3) * bf_hi(y.w));
;                     *(u32x4*)(rowp + bj * HALF) = w; } }
	v_lshlrev_b32_e32 v125, 16, v202
	v_and_b32_e32 v139, 0xffff0000, v202
	v_lshlrev_b32_e32 v127, 16, v203
	v_and_b32_e32 v141, 0xffff0000, v203
	v_lshlrev_b32_e32 v121, 16, v204
	v_and_b32_e32 v143, 0xffff0000, v204
	v_lshlrev_b32_e32 v123, 16, v205
	v_and_b32_e32 v163, 0xffff0000, v205
	v_cvt_f32_ubyte0_e32 v133, v206
	v_cvt_f32_ubyte0_e32 v132, v208
	v_cvt_f32_ubyte1_e32 v135, v206
	v_cvt_f32_ubyte1_e32 v134, v208
	v_cvt_f32_ubyte2_e32 v169, v206
	v_cvt_f32_ubyte2_e32 v168, v208
	v_cvt_f32_ubyte3_e32 v171, v206
	v_cvt_f32_ubyte3_e32 v170, v208
	v_cvt_f32_ubyte0_e32 v173, v207
	v_cvt_f32_ubyte0_e32 v172, v209
	v_cvt_f32_ubyte1_e32 v175, v207
	v_cvt_f32_ubyte1_e32 v174, v209
	v_cvt_f32_ubyte2_e32 v177, v207
	v_cvt_f32_ubyte2_e32 v176, v209
	v_cvt_f32_ubyte3_e32 v129, v207
	v_cvt_f32_ubyte3_e32 v128, v209
	v_pk_mul_f32 v[130:131], v[132:133], s[16:17] op_sel_hi:[1,0]
	v_pk_mul_f32 v[132:133], v[134:135], s[16:17] op_sel_hi:[1,0]
	v_pk_mul_f32 v[134:135], v[168:169], s[16:17] op_sel_hi:[1,0]
	v_pk_mul_f32 v[168:169], v[170:171], s[16:17] op_sel_hi:[1,0]
	v_pk_mul_f32 v[170:171], v[172:173], s[16:17] op_sel_hi:[1,0]
	v_pk_mul_f32 v[172:173], v[174:175], s[16:17] op_sel_hi:[1,0]
	v_pk_mul_f32 v[174:175], v[176:177], s[16:17] op_sel_hi:[1,0]
	v_pk_mul_f32 v[128:129], v[128:129], s[16:17] op_sel_hi:[1,0]
	v_pk_mul_f32 v[122:123], v[122:123], v[174:175]
	v_pk_mul_f32 v[128:129], v[162:163], v[128:129]
	v_pk_mul_f32 v[124:125], v[124:125], v[130:131]
	v_pk_mul_f32 v[130:131], v[138:139], v[132:133]
	v_pk_mul_f32 v[126:127], v[126:127], v[134:135]
	v_pk_mul_f32 v[132:133], v[140:141], v[168:169]
	v_pk_mul_f32 v[120:121], v[120:121], v[170:171]
	v_pk_mul_f32 v[134:135], v[142:143], v[172:173]
	v_add_f32_e32 v123, v122, v123
	v_add_f32_e32 v128, v128, v129
	v_add_f32_e32 v124, v124, v125
	v_add_f32_e32 v125, v130, v131
	v_add_f32_e32 v126, v126, v127
	v_add_f32_e32 v127, v132, v133
	v_add_f32_e32 v130, v120, v121
	v_add_f32_e32 v131, v134, v135
	v_cvt_pk_bf16_f32 v120, v124, v125
	v_cvt_pk_bf16_f32 v121, v126, v127
	v_cvt_pk_bf16_f32 v122, v130, v131
	v_cvt_pk_bf16_f32 v123, v123, v128
	v_lshl_add_u64 v[128:129], s[4:5], 0, v[164:165]
	v_lshl_add_u64 v[128:129], v[128:129], 0, v[144:145]
	v_add_u32_e32 v253, 0x80000, v250
	global_load_dwordx4 v[202:205], v253, s[52:53] offset:256
	v_add_u32_e32 v253, 0x80000, v251
	global_load_dwordx2 v[206:207], v253, s[42:43] offset:128
	global_load_dwordx2 v[208:209], v253, s[42:43] offset:2176
	global_store_dwordx4 v[128:129], v[120:123], off
	v_mov_b32_e32 v134, v117
	v_mov_b32_e32 v136, v119
	v_mov_b32_e32 v138, v113
	v_mov_b32_e32 v140, v115
	v_or_b32_e32 v130, 32, v150
	v_ashrrev_i32_e32 v131, 31, v130
	v_lshlrev_b64 v[130:131], 12, v[130:131]
	v_lshl_add_u64 v[132:133], s[52:53], 0, v[130:131]
	v_lshl_add_u64 v[132:133], v[132:133], 0, v[144:145]
	s_waitcnt vmcnt(21)
	v_lshlrev_b32_e32 v117, 16, v210
	v_and_b32_e32 v135, 0xffff0000, v210
	v_lshlrev_b32_e32 v119, 16, v211
	v_and_b32_e32 v137, 0xffff0000, v211
	v_lshlrev_b32_e32 v113, 16, v212
	v_and_b32_e32 v139, 0xffff0000, v212
	v_lshlrev_b32_e32 v115, 16, v213
	v_and_b32_e32 v141, 0xffff0000, v213
	v_cvt_f32_ubyte0_e32 v125, v214
	v_cvt_f32_ubyte0_e32 v124, v216
	v_cvt_f32_ubyte1_e32 v127, v214
	v_cvt_f32_ubyte1_e32 v126, v216
	v_cvt_f32_ubyte2_e32 v143, v214
	v_cvt_f32_ubyte2_e32 v142, v216
	v_cvt_f32_ubyte3_e32 v163, v214
	v_cvt_f32_ubyte3_e32 v162, v216
	v_cvt_f32_ubyte0_e32 v165, v215
	v_cvt_f32_ubyte0_e32 v164, v217
	v_cvt_f32_ubyte1_e32 v167, v215
	v_cvt_f32_ubyte1_e32 v166, v217
	v_cvt_f32_ubyte2_e32 v169, v215
	v_cvt_f32_ubyte2_e32 v168, v217
	v_cvt_f32_ubyte3_e32 v121, v215
	v_cvt_f32_ubyte3_e32 v120, v217
	v_pk_mul_f32 v[122:123], v[124:125], s[16:17] op_sel_hi:[1,0]
	v_pk_mul_f32 v[124:125], v[126:127], s[16:17] op_sel_hi:[1,0]
	v_pk_mul_f32 v[126:127], v[142:143], s[16:17] op_sel_hi:[1,0]
	v_pk_mul_f32 v[142:143], v[162:163], s[16:17] op_sel_hi:[1,0]
	v_pk_mul_f32 v[162:163], v[164:165], s[16:17] op_sel_hi:[1,0]
	v_pk_mul_f32 v[164:165], v[166:167], s[16:17] op_sel_hi:[1,0]
	v_pk_mul_f32 v[166:167], v[168:169], s[16:17] op_sel_hi:[1,0]
	v_pk_mul_f32 v[120:121], v[120:121], s[16:17] op_sel_hi:[1,0]
	v_pk_mul_f32 v[114:115], v[114:115], v[166:167]
	v_pk_mul_f32 v[120:121], v[140:141], v[120:121]
	v_pk_mul_f32 v[116:117], v[116:117], v[122:123]
	v_pk_mul_f32 v[122:123], v[134:135], v[124:125]
	v_pk_mul_f32 v[118:119], v[118:119], v[126:127]
	v_pk_mul_f32 v[124:125], v[136:137], v[142:143]
	v_pk_mul_f32 v[112:113], v[112:113], v[162:163]
	v_pk_mul_f32 v[126:127], v[138:139], v[164:165]
	v_add_f32_e32 v115, v114, v115
	v_add_f32_e32 v120, v120, v121
	v_add_f32_e32 v116, v116, v117
	v_add_f32_e32 v117, v122, v123
	v_add_f32_e32 v118, v118, v119
	v_add_f32_e32 v119, v124, v125
	v_add_f32_e32 v122, v112, v113
	v_add_f32_e32 v123, v126, v127
	v_cvt_pk_bf16_f32 v112, v116, v117
	v_cvt_pk_bf16_f32 v113, v118, v119
	v_cvt_pk_bf16_f32 v114, v122, v123
	v_cvt_pk_bf16_f32 v115, v115, v120
	v_lshl_add_u64 v[120:121], s[42:43], 0, v[130:131]
	v_lshl_add_u64 v[120:121], v[120:121], 0, v[146:147]
	v_add_u32_e32 v253, 0x90000, v250
	global_load_dwordx4 v[210:213], v253, s[52:53]
	v_add_u32_e32 v253, 0x90000, v251
	global_load_dwordx2 v[214:215], v253, s[42:43]
	global_load_dwordx2 v[216:217], v253, s[42:43] offset:2048
	global_store_dwordx4 v[128:129], v[112:115], off offset:256
	v_mov_b32_e32 v122, v109
	v_mov_b32_e32 v124, v111
	v_mov_b32_e32 v126, v105
	v_mov_b32_e32 v128, v107
	s_waitcnt vmcnt(22)
; __device__ __forceinline__ unsigned cvt_pk_bf16(float lo, float hi) { unsigned r; asm volatile("v_cvt_pk_bf16_f32 %0, %1, %2" : "=v"(r) : "v"(lo), "v"(hi)); return r; }
; __device__ __forceinline__ float bf_lo(unsigned w) { return __uint_as_float(w << 16); }
; __device__ __forceinline__ float bf_hi(unsigned w) { return __uint_as_float(w & 0xffff0000u); }
;     __device__ __forceinline__ void operator()(const f32x4 (&acc)[2][2][4][2], const Unit& u, int wr, int wc, int fr, int fq) const {
;     ...
;             for (int m = 0; m < 4; ++m) { const size_t r = (size_t)(row0 + ai * HALF + m * 16); bf16_t* rowp = O + r * DM + col0; const unsigned char* gr = G8 + r * 4096 + col0; const bf16_t* yr = YA + r * DM + col0;
; #pragma unroll
;                 for (int bj = 0; bj < 2; ++bj) { const u32x2 g = *(const u32x2*)(gr + 2048 + bj * HALF), a = *(const u32x2*)(gr + bj * HALF); const u32x4 y = *(const u32x4*)(yr + bj * HALF);
;                     const f32x4 v0 = acc[ai][bj][m][0] * sv[bj][0], v1 = acc[ai][bj][m][1] * sv[bj][1];
;                     u32x4 w;
;                     w.x = cvt_pk_bf16(v0[0] * U8F(g.x, 0) + U8F(a.x, 0) * bf_lo(y.x), v0[1] * U8F(g.x, 1) + U8F(a.x, 1) * bf_hi(y.x));
;                     w.y = cvt_pk_bf16(v0[2] * U8F(g.x, 2) + U8F(a.x, 2) * bf_lo(y.y), v0[3] * U8F(g.x, 3) + U8F(a.x, 3) * bf_hi(y.y));
;                     w.z = cvt_pk_bf16(v1[0] * U8F(g.y, 0) + U8F(a.y, 0) * bf_lo(y.z), v1[1] * U8F(g.y, 1) + U8F(a.y, 1) * bf_hi(y.z));
;                     w.w = cvt_pk_bf16(v1[2] * U8F(g.y, 2) + U8F(a.y, 2) * bf_lo(y.w), v1[3] * U8F(g.y, 3) + U8F(a.y, 3) * bf_hi(y.w));
;                     *(u32x4*)(rowp + bj * HALF) = w; } }
	v_lshlrev_b32_e32 v109, 16, v218
	v_and_b32_e32 v123, 0xffff0000, v218
	v_lshlrev_b32_e32 v111, 16, v219
	v_and_b32_e32 v125, 0xffff0000, v219
	v_lshlrev_b32_e32 v105, 16, v220
	v_and_b32_e32 v127, 0xffff0000, v220
	v_lshlrev_b32_e32 v107, 16, v221
	v_and_b32_e32 v129, 0xffff0000, v221
	v_cvt_f32_ubyte0_e32 v117, v222
	v_cvt_f32_ubyte0_e32 v116, v224
	v_cvt_f32_ubyte1_e32 v119, v222
	v_cvt_f32_ubyte1_e32 v118, v224
	v_cvt_f32_ubyte2_e32 v135, v222
	v_cvt_f32_ubyte2_e32 v134, v224
	v_cvt_f32_ubyte3_e32 v137, v222
	v_cvt_f32_ubyte3_e32 v136, v224
	v_cvt_f32_ubyte0_e32 v139, v223
	v_cvt_f32_ubyte0_e32 v138, v225
	v_cvt_f32_ubyte1_e32 v141, v223
	v_cvt_f32_ubyte1_e32 v140, v225
	v_cvt_f32_ubyte2_e32 v143, v223
	v_cvt_f32_ubyte2_e32 v142, v225
	v_cvt_f32_ubyte3_e32 v113, v223
	v_cvt_f32_ubyte3_e32 v112, v225
	v_pk_mul_f32 v[114:115], v[116:117], s[16:17] op_sel_hi:[1,0]
	v_pk_mul_f32 v[116:117], v[118:119], s[16:17] op_sel_hi:[1,0]
	v_pk_mul_f32 v[118:119], v[134:135], s[16:17] op_sel_hi:[1,0]
	v_pk_mul_f32 v[134:135], v[136:137], s[16:17] op_sel_hi:[1,0]
	v_pk_mul_f32 v[136:137], v[138:139], s[16:17] op_sel_hi:[1,0]
	v_pk_mul_f32 v[138:139], v[140:141], s[16:17] op_sel_hi:[1,0]
	v_pk_mul_f32 v[140:141], v[142:143], s[16:17] op_sel_hi:[1,0]
	v_pk_mul_f32 v[112:113], v[112:113], s[16:17] op_sel_hi:[1,0]
	v_pk_mul_f32 v[106:107], v[106:107], v[140:141]
	v_pk_mul_f32 v[112:113], v[128:129], v[112:113]
	v_pk_mul_f32 v[108:109], v[108:109], v[114:115]
	v_pk_mul_f32 v[114:115], v[122:123], v[116:117]
	v_pk_mul_f32 v[110:111], v[110:111], v[118:119]
	v_pk_mul_f32 v[116:117], v[124:125], v[134:135]
	v_pk_mul_f32 v[104:105], v[104:105], v[136:137]
	v_pk_mul_f32 v[118:119], v[126:127], v[138:139]
	v_add_f32_e32 v107, v106, v107
	v_add_f32_e32 v112, v112, v113
	v_add_f32_e32 v108, v108, v109
	v_add_f32_e32 v109, v114, v115
	v_add_f32_e32 v110, v110, v111
	v_add_f32_e32 v111, v116, v117
	v_add_f32_e32 v114, v104, v105
	v_add_f32_e32 v115, v118, v119
	v_cvt_pk_bf16_f32 v104, v108, v109
	v_cvt_pk_bf16_f32 v105, v110, v111
	v_cvt_pk_bf16_f32 v106, v114, v115
	v_cvt_pk_bf16_f32 v107, v107, v112
	v_lshl_add_u64 v[112:113], s[4:5], 0, v[130:131]
	v_lshl_add_u64 v[112:113], v[112:113], 0, v[144:145]
	v_add_u32_e32 v253, 0x90000, v250
	global_load_dwordx4 v[218:221], v253, s[52:53] offset:256
	v_add_u32_e32 v253, 0x90000, v251
	global_load_dwordx2 v[222:223], v253, s[42:43] offset:128
	global_load_dwordx2 v[224:225], v253, s[42:43] offset:2176
	global_store_dwordx4 v[112:113], v[104:107], off
	v_mov_b32_e32 v118, v101
	v_mov_b32_e32 v120, v103
	v_mov_b32_e32 v122, v97
	v_mov_b32_e32 v124, v99
	v_or_b32_e32 v114, 48, v150
	v_ashrrev_i32_e32 v115, 31, v114
	v_lshlrev_b64 v[114:115], 12, v[114:115]
	v_lshl_add_u64 v[116:117], s[52:53], 0, v[114:115]
	v_lshl_add_u64 v[116:117], v[116:117], 0, v[144:145]
	s_waitcnt vmcnt(23)
	v_lshlrev_b32_e32 v101, 16, v226
	v_and_b32_e32 v119, 0xffff0000, v226
	v_lshlrev_b32_e32 v103, 16, v227
	v_and_b32_e32 v121, 0xffff0000, v227
	v_lshlrev_b32_e32 v97, 16, v228
	v_and_b32_e32 v123, 0xffff0000, v228
	v_lshlrev_b32_e32 v99, 16, v229
	v_and_b32_e32 v125, 0xffff0000, v229
	v_cvt_f32_ubyte0_e32 v109, v230
	v_cvt_f32_ubyte0_e32 v108, v232
	v_cvt_f32_ubyte1_e32 v111, v230
	v_cvt_f32_ubyte1_e32 v110, v232
	v_cvt_f32_ubyte2_e32 v127, v230
	v_cvt_f32_ubyte2_e32 v126, v232
	v_cvt_f32_ubyte3_e32 v129, v230
	v_cvt_f32_ubyte3_e32 v128, v232
	v_cvt_f32_ubyte0_e32 v131, v231
	v_cvt_f32_ubyte0_e32 v130, v233
	v_cvt_f32_ubyte1_e32 v133, v231
	v_cvt_f32_ubyte1_e32 v132, v233
	v_cvt_f32_ubyte2_e32 v135, v231
	v_cvt_f32_ubyte2_e32 v134, v233
	v_cvt_f32_ubyte3_e32 v105, v231
	v_cvt_f32_ubyte3_e32 v104, v233
	v_pk_mul_f32 v[106:107], v[108:109], s[16:17] op_sel_hi:[1,0]
	v_pk_mul_f32 v[108:109], v[110:111], s[16:17] op_sel_hi:[1,0]
	v_pk_mul_f32 v[110:111], v[126:127], s[16:17] op_sel_hi:[1,0]
	v_pk_mul_f32 v[126:127], v[128:129], s[16:17] op_sel_hi:[1,0]
	v_pk_mul_f32 v[128:129], v[130:131], s[16:17] op_sel_hi:[1,0]
	v_pk_mul_f32 v[130:131], v[132:133], s[16:17] op_sel_hi:[1,0]
	v_pk_mul_f32 v[132:133], v[134:135], s[16:17] op_sel_hi:[1,0]
	v_pk_mul_f32 v[104:105], v[104:105], s[16:17] op_sel_hi:[1,0]
	v_pk_mul_f32 v[98:99], v[98:99], v[132:133]
	v_pk_mul_f32 v[104:105], v[124:125], v[104:105]
	v_pk_mul_f32 v[100:101], v[100:101], v[106:107]
	v_pk_mul_f32 v[106:107], v[118:119], v[108:109]
	v_pk_mul_f32 v[102:103], v[102:103], v[110:111]
	v_pk_mul_f32 v[108:109], v[120:121], v[126:127]
	v_pk_mul_f32 v[96:97], v[96:97], v[128:129]
	v_pk_mul_f32 v[110:111], v[122:123], v[130:131]
	v_add_f32_e32 v99, v98, v99
	v_add_f32_e32 v104, v104, v105
	v_add_f32_e32 v100, v100, v101
	v_add_f32_e32 v101, v106, v107
	v_add_f32_e32 v102, v102, v103
	v_add_f32_e32 v103, v108, v109
	v_add_f32_e32 v106, v96, v97
	v_add_f32_e32 v107, v110, v111
	v_cvt_pk_bf16_f32 v96, v100, v101
	v_cvt_pk_bf16_f32 v97, v102, v103
	v_cvt_pk_bf16_f32 v98, v106, v107
	v_cvt_pk_bf16_f32 v99, v99, v104
	v_lshl_add_u64 v[104:105], s[42:43], 0, v[114:115]
	v_lshl_add_u64 v[104:105], v[104:105], 0, v[146:147]
	v_add_u32_e32 v253, 0xa0000, v250
	global_load_dwordx4 v[226:229], v253, s[52:53]
	v_add_u32_e32 v253, 0xa0000, v251
	global_load_dwordx2 v[230:231], v253, s[42:43]
	global_load_dwordx2 v[232:233], v253, s[42:43] offset:2048
	global_store_dwordx4 v[112:113], v[96:99], off offset:256
	v_mov_b32_e32 v106, v93
	v_mov_b32_e32 v108, v95
	v_mov_b32_e32 v110, v89
	v_mov_b32_e32 v112, v91
	s_waitcnt vmcnt(24)
; __device__ __forceinline__ unsigned cvt_pk_bf16(float lo, float hi) { unsigned r; asm volatile("v_cvt_pk_bf16_f32 %0, %1, %2" : "=v"(r) : "v"(lo), "v"(hi)); return r; }
; __device__ __forceinline__ float bf_lo(unsigned w) { return __uint_as_float(w << 16); }
; __device__ __forceinline__ float bf_hi(unsigned w) { return __uint_as_float(w & 0xffff0000u); }
;     __device__ __forceinline__ void operator()(const f32x4 (&acc)[2][2][4][2], const Unit& u, int wr, int wc, int fr, int fq) const {
;     ...
;             for (int m = 0; m < 4; ++m) { const size_t r = (size_t)(row0 + ai * HALF + m * 16); bf16_t* rowp = O + r * DM + col0; const unsigned char* gr = G8 + r * 4096 + col0; const bf16_t* yr = YA + r * DM + col0;
; #pragma unroll
;                 for (int bj = 0; bj < 2; ++bj) { const u32x2 g = *(const u32x2*)(gr + 2048 + bj * HALF), a = *(const u32x2*)(gr + bj * HALF); const u32x4 y = *(const u32x4*)(yr + bj * HALF);
;                     const f32x4 v0 = acc[ai][bj][m][0] * sv[bj][0], v1 = acc[ai][bj][m][1] * sv[bj][1];
;                     u32x4 w;
;                     w.x = cvt_pk_bf16(v0[0] * U8F(g.x, 0) + U8F(a.x, 0) * bf_lo(y.x), v0[1] * U8F(g.x, 1) + U8F(a.x, 1) * bf_hi(y.x));
;                     w.y = cvt_pk_bf16(v0[2] * U8F(g.x, 2) + U8F(a.x, 2) * bf_lo(y.y), v0[3] * U8F(g.x, 3) + U8F(a.x, 3) * bf_hi(y.y));
;                     w.z = cvt_pk_bf16(v1[0] * U8F(g.y, 0) + U8F(a.y, 0) * bf_lo(y.z), v1[1] * U8F(g.y, 1) + U8F(a.y, 1) * bf_hi(y.z));
;                     w.w = cvt_pk_bf16(v1[2] * U8F(g.y, 2) + U8F(a.y, 2) * bf_lo(y.w), v1[3] * U8F(g.y, 3) + U8F(a.y, 3) * bf_hi(y.w));
;                     *(u32x4*)(rowp + bj * HALF) = w; } }
	v_lshlrev_b32_e32 v93, 16, v234
	v_and_b32_e32 v107, 0xffff0000, v234
	v_lshlrev_b32_e32 v95, 16, v235
	v_and_b32_e32 v109, 0xffff0000, v235
	v_lshlrev_b32_e32 v89, 16, v236
	v_and_b32_e32 v111, 0xffff0000, v236
	v_lshlrev_b32_e32 v91, 16, v237
	v_and_b32_e32 v113, 0xffff0000, v237
	v_cvt_f32_ubyte0_e32 v101, v238
	v_cvt_f32_ubyte0_e32 v100, v240
	v_cvt_f32_ubyte1_e32 v103, v238
	v_cvt_f32_ubyte1_e32 v102, v240
	v_cvt_f32_ubyte2_e32 v119, v238
	v_cvt_f32_ubyte2_e32 v118, v240
	v_cvt_f32_ubyte3_e32 v121, v238
	v_cvt_f32_ubyte3_e32 v120, v240
	v_cvt_f32_ubyte0_e32 v123, v239
	v_cvt_f32_ubyte0_e32 v122, v241
	v_cvt_f32_ubyte1_e32 v125, v239
	v_cvt_f32_ubyte1_e32 v124, v241
	v_cvt_f32_ubyte2_e32 v127, v239
	v_cvt_f32_ubyte2_e32 v126, v241
	v_cvt_f32_ubyte3_e32 v97, v239
	v_cvt_f32_ubyte3_e32 v96, v241
	v_pk_mul_f32 v[98:99], v[100:101], s[16:17] op_sel_hi:[1,0]
	v_pk_mul_f32 v[100:101], v[102:103], s[16:17] op_sel_hi:[1,0]
	v_pk_mul_f32 v[102:103], v[118:119], s[16:17] op_sel_hi:[1,0]
	v_pk_mul_f32 v[118:119], v[120:121], s[16:17] op_sel_hi:[1,0]
	v_pk_mul_f32 v[120:121], v[122:123], s[16:17] op_sel_hi:[1,0]
	v_pk_mul_f32 v[122:123], v[124:125], s[16:17] op_sel_hi:[1,0]
	v_pk_mul_f32 v[124:125], v[126:127], s[16:17] op_sel_hi:[1,0]
	v_pk_mul_f32 v[96:97], v[96:97], s[16:17] op_sel_hi:[1,0]
	v_pk_mul_f32 v[90:91], v[90:91], v[124:125]
	v_pk_mul_f32 v[96:97], v[112:113], v[96:97]
	v_pk_mul_f32 v[92:93], v[92:93], v[98:99]
	v_pk_mul_f32 v[98:99], v[106:107], v[100:101]
	v_pk_mul_f32 v[94:95], v[94:95], v[102:103]
	v_pk_mul_f32 v[100:101], v[108:109], v[118:119]
	v_pk_mul_f32 v[88:89], v[88:89], v[120:121]
	v_pk_mul_f32 v[102:103], v[110:111], v[122:123]
	v_add_f32_e32 v91, v90, v91
	v_add_f32_e32 v96, v96, v97
	v_add_f32_e32 v92, v92, v93
	v_add_f32_e32 v93, v98, v99
	v_add_f32_e32 v94, v94, v95
	v_add_f32_e32 v95, v100, v101
	v_add_f32_e32 v98, v88, v89
	v_add_f32_e32 v99, v102, v103
	v_cvt_pk_bf16_f32 v88, v92, v93
	v_cvt_pk_bf16_f32 v89, v94, v95
	v_cvt_pk_bf16_f32 v90, v98, v99
	v_cvt_pk_bf16_f32 v91, v91, v96
	v_lshl_add_u64 v[96:97], s[4:5], 0, v[114:115]
	v_lshl_add_u64 v[96:97], v[96:97], 0, v[144:145]
	v_add_u32_e32 v253, 0xa0000, v250
	global_load_dwordx4 v[234:237], v253, s[52:53] offset:256
	v_add_u32_e32 v253, 0xa0000, v251
	global_load_dwordx2 v[238:239], v253, s[42:43] offset:128
	global_load_dwordx2 v[240:241], v253, s[42:43] offset:2176
	global_store_dwordx4 v[96:97], v[88:91], off
	v_mov_b32_e32 v102, v85
	v_mov_b32_e32 v104, v87
	v_mov_b32_e32 v106, v81
	v_mov_b32_e32 v108, v83
	v_lshl_add_u64 v[98:99], v[148:149], 0, s[26:27]
	v_lshl_add_u64 v[100:101], s[52:53], 0, v[98:99]
	v_lshl_add_u64 v[100:101], v[100:101], 0, v[144:145]
	s_mov_b64 s[26:27], 0x90000
	s_waitcnt vmcnt(25)
	v_lshlrev_b32_e32 v85, 16, v242
	v_and_b32_e32 v103, 0xffff0000, v242
	v_lshlrev_b32_e32 v87, 16, v243
	v_and_b32_e32 v105, 0xffff0000, v243
	v_lshlrev_b32_e32 v81, 16, v244
	v_and_b32_e32 v107, 0xffff0000, v244
	v_lshlrev_b32_e32 v83, 16, v245
	v_and_b32_e32 v109, 0xffff0000, v245
	v_cvt_f32_ubyte0_e32 v93, v246
	v_cvt_f32_ubyte0_e32 v92, v248
	v_cvt_f32_ubyte1_e32 v95, v246
	v_cvt_f32_ubyte1_e32 v94, v248
	v_cvt_f32_ubyte2_e32 v111, v246
	v_cvt_f32_ubyte2_e32 v110, v248
	v_cvt_f32_ubyte3_e32 v113, v246
	v_cvt_f32_ubyte3_e32 v112, v248
	v_cvt_f32_ubyte0_e32 v115, v247
	v_cvt_f32_ubyte0_e32 v114, v249
	v_cvt_f32_ubyte1_e32 v117, v247
	v_cvt_f32_ubyte1_e32 v116, v249
	v_cvt_f32_ubyte2_e32 v119, v247
	v_cvt_f32_ubyte2_e32 v118, v249
	v_cvt_f32_ubyte3_e32 v89, v247
	v_cvt_f32_ubyte3_e32 v88, v249
	v_pk_mul_f32 v[90:91], v[92:93], s[16:17] op_sel_hi:[1,0]
	v_pk_mul_f32 v[92:93], v[94:95], s[16:17] op_sel_hi:[1,0]
	v_pk_mul_f32 v[94:95], v[110:111], s[16:17] op_sel_hi:[1,0]
	v_pk_mul_f32 v[110:111], v[112:113], s[16:17] op_sel_hi:[1,0]
	v_pk_mul_f32 v[112:113], v[114:115], s[16:17] op_sel_hi:[1,0]
	v_pk_mul_f32 v[114:115], v[116:117], s[16:17] op_sel_hi:[1,0]
	v_pk_mul_f32 v[116:117], v[118:119], s[16:17] op_sel_hi:[1,0]
	v_pk_mul_f32 v[88:89], v[88:89], s[16:17] op_sel_hi:[1,0]
	v_pk_mul_f32 v[82:83], v[82:83], v[116:117]
	v_pk_mul_f32 v[88:89], v[108:109], v[88:89]
	v_pk_mul_f32 v[84:85], v[84:85], v[90:91]
	v_pk_mul_f32 v[90:91], v[102:103], v[92:93]
	v_pk_mul_f32 v[86:87], v[86:87], v[94:95]
	v_pk_mul_f32 v[92:93], v[104:105], v[110:111]
	v_pk_mul_f32 v[80:81], v[80:81], v[112:113]
	v_pk_mul_f32 v[94:95], v[106:107], v[114:115]
	v_add_f32_e32 v83, v82, v83
	v_add_f32_e32 v88, v88, v89
	v_add_f32_e32 v84, v84, v85
	v_add_f32_e32 v85, v90, v91
	v_add_f32_e32 v86, v86, v87
	v_add_f32_e32 v87, v92, v93
	v_add_f32_e32 v90, v80, v81
	v_add_f32_e32 v91, v94, v95
	v_cvt_pk_bf16_f32 v80, v84, v85
	v_cvt_pk_bf16_f32 v81, v86, v87
	v_cvt_pk_bf16_f32 v82, v90, v91
	v_cvt_pk_bf16_f32 v83, v83, v88
	v_lshl_add_u64 v[88:89], s[42:43], 0, v[98:99]
	v_lshl_add_u64 v[88:89], v[88:89], 0, v[146:147]
	v_add_u32_e32 v253, 0xb0000, v250
	global_load_dwordx4 v[242:245], v253, s[52:53]
	v_add_u32_e32 v253, 0xb0000, v251
	global_load_dwordx2 v[246:247], v253, s[42:43]
	global_load_dwordx2 v[248:249], v253, s[42:43] offset:2048
	global_store_dwordx4 v[96:97], v[80:83], off offset:256
	v_mov_b32_e32 v90, v77
	v_mov_b32_e32 v92, v79
	v_mov_b32_e32 v94, v73
	v_mov_b32_e32 v96, v75
	s_waitcnt vmcnt(25)
; __device__ __forceinline__ unsigned cvt_pk_bf16(float lo, float hi) { unsigned r; asm volatile("v_cvt_pk_bf16_f32 %0, %1, %2" : "=v"(r) : "v"(lo), "v"(hi)); return r; }
; __device__ __forceinline__ float bf_lo(unsigned w) { return __uint_as_float(w << 16); }
; __device__ __forceinline__ float bf_hi(unsigned w) { return __uint_as_float(w & 0xffff0000u); }
;     __device__ __forceinline__ void operator()(const f32x4 (&acc)[2][2][4][2], const Unit& u, int wr, int wc, int fr, int fq) const {
;     ...
;             for (int m = 0; m < 4; ++m) { const size_t r = (size_t)(row0 + ai * HALF + m * 16); bf16_t* rowp = O + r * DM + col0; const unsigned char* gr = G8 + r * 4096 + col0; const bf16_t* yr = YA + r * DM + col0;
; #pragma unroll
;                 for (int bj = 0; bj < 2; ++bj) { const u32x2 g = *(const u32x2*)(gr + 2048 + bj * HALF), a = *(const u32x2*)(gr + bj * HALF); const u32x4 y = *(const u32x4*)(yr + bj * HALF);
;                     const f32x4 v0 = acc[ai][bj][m][0] * sv[bj][0], v1 = acc[ai][bj][m][1] * sv[bj][1];
;                     u32x4 w;
;                     w.x = cvt_pk_bf16(v0[0] * U8F(g.x, 0) + U8F(a.x, 0) * bf_lo(y.x), v0[1] * U8F(g.x, 1) + U8F(a.x, 1) * bf_hi(y.x));
;                     w.y = cvt_pk_bf16(v0[2] * U8F(g.x, 2) + U8F(a.x, 2) * bf_lo(y.y), v0[3] * U8F(g.x, 3) + U8F(a.x, 3) * bf_hi(y.y));
;                     w.z = cvt_pk_bf16(v1[0] * U8F(g.y, 0) + U8F(a.y, 0) * bf_lo(y.z), v1[1] * U8F(g.y, 1) + U8F(a.y, 1) * bf_hi(y.z));
;                     w.w = cvt_pk_bf16(v1[2] * U8F(g.y, 2) + U8F(a.y, 2) * bf_lo(y.w), v1[3] * U8F(g.y, 3) + U8F(a.y, 3) * bf_hi(y.w));
;                     *(u32x4*)(rowp + bj * HALF) = w; } }
	v_lshlrev_b32_e32 v77, 16, v194
	v_and_b32_e32 v91, 0xffff0000, v194
	v_lshlrev_b32_e32 v79, 16, v195
	v_and_b32_e32 v93, 0xffff0000, v195
	v_lshlrev_b32_e32 v73, 16, v196
	v_and_b32_e32 v95, 0xffff0000, v196
	v_lshlrev_b32_e32 v75, 16, v197
	v_and_b32_e32 v97, 0xffff0000, v197
	v_cvt_f32_ubyte0_e32 v85, v198
	v_cvt_f32_ubyte0_e32 v84, v200
	v_cvt_f32_ubyte1_e32 v87, v198
	v_cvt_f32_ubyte1_e32 v86, v200
	v_cvt_f32_ubyte2_e32 v103, v198
	v_cvt_f32_ubyte2_e32 v102, v200
	v_cvt_f32_ubyte3_e32 v105, v198
	v_cvt_f32_ubyte3_e32 v104, v200
	v_cvt_f32_ubyte0_e32 v107, v199
	v_cvt_f32_ubyte0_e32 v106, v201
	v_cvt_f32_ubyte1_e32 v109, v199
	v_cvt_f32_ubyte1_e32 v108, v201
	v_cvt_f32_ubyte2_e32 v111, v199
	v_cvt_f32_ubyte2_e32 v110, v201
	v_cvt_f32_ubyte3_e32 v81, v199
	v_cvt_f32_ubyte3_e32 v80, v201
	v_pk_mul_f32 v[82:83], v[84:85], s[16:17] op_sel_hi:[1,0]
	v_pk_mul_f32 v[84:85], v[86:87], s[16:17] op_sel_hi:[1,0]
	v_pk_mul_f32 v[86:87], v[102:103], s[16:17] op_sel_hi:[1,0]
	v_pk_mul_f32 v[102:103], v[104:105], s[16:17] op_sel_hi:[1,0]
	v_pk_mul_f32 v[104:105], v[106:107], s[16:17] op_sel_hi:[1,0]
	v_pk_mul_f32 v[106:107], v[108:109], s[16:17] op_sel_hi:[1,0]
	v_pk_mul_f32 v[108:109], v[110:111], s[16:17] op_sel_hi:[1,0]
	v_pk_mul_f32 v[80:81], v[80:81], s[16:17] op_sel_hi:[1,0]
	v_pk_mul_f32 v[74:75], v[74:75], v[108:109]
	v_pk_mul_f32 v[80:81], v[96:97], v[80:81]
	v_pk_mul_f32 v[76:77], v[76:77], v[82:83]
	v_pk_mul_f32 v[82:83], v[90:91], v[84:85]
	v_pk_mul_f32 v[78:79], v[78:79], v[86:87]
	v_pk_mul_f32 v[84:85], v[92:93], v[102:103]
	v_pk_mul_f32 v[72:73], v[72:73], v[104:105]
	v_pk_mul_f32 v[86:87], v[94:95], v[106:107]
	v_add_f32_e32 v75, v74, v75
	v_add_f32_e32 v80, v80, v81
	v_add_f32_e32 v76, v76, v77
	v_add_f32_e32 v77, v82, v83
	v_add_f32_e32 v78, v78, v79
	v_add_f32_e32 v79, v84, v85
	v_add_f32_e32 v82, v72, v73
	v_add_f32_e32 v83, v86, v87
	v_cvt_pk_bf16_f32 v72, v76, v77
	v_cvt_pk_bf16_f32 v73, v78, v79
	v_cvt_pk_bf16_f32 v74, v82, v83
	v_cvt_pk_bf16_f32 v75, v75, v80
	v_lshl_add_u64 v[80:81], s[4:5], 0, v[98:99]
	v_lshl_add_u64 v[80:81], v[80:81], 0, v[144:145]
	v_add_u32_e32 v253, 0xb0000, v250
	global_load_dwordx4 v[194:197], v253, s[52:53] offset:256
	v_add_u32_e32 v253, 0xb0000, v251
	global_load_dwordx2 v[198:199], v253, s[42:43] offset:128
	global_load_dwordx2 v[200:201], v253, s[42:43] offset:2176
	global_store_dwordx4 v[80:81], v[72:75], off
	v_mov_b32_e32 v86, v61
	v_mov_b32_e32 v88, v63
	v_mov_b32_e32 v90, v57
	v_mov_b32_e32 v92, v59
	v_lshl_add_u64 v[82:83], v[148:149], 0, s[26:27]
	v_lshl_add_u64 v[84:85], s[52:53], 0, v[82:83]
	v_lshl_add_u64 v[84:85], v[84:85], 0, v[144:145]
	s_mov_b64 s[26:27], 0xa0000
	s_waitcnt vmcnt(25)
	v_lshlrev_b32_e32 v61, 16, v202
	v_and_b32_e32 v87, 0xffff0000, v202
	v_lshlrev_b32_e32 v63, 16, v203
	v_and_b32_e32 v89, 0xffff0000, v203
	v_lshlrev_b32_e32 v57, 16, v204
	v_and_b32_e32 v91, 0xffff0000, v204
	v_lshlrev_b32_e32 v59, 16, v205
	v_and_b32_e32 v93, 0xffff0000, v205
	v_cvt_f32_ubyte0_e32 v77, v206
	v_cvt_f32_ubyte0_e32 v76, v208
	v_cvt_f32_ubyte1_e32 v79, v206
	v_cvt_f32_ubyte1_e32 v78, v208
	v_cvt_f32_ubyte2_e32 v95, v206
	v_cvt_f32_ubyte2_e32 v94, v208
	v_cvt_f32_ubyte3_e32 v97, v206
	v_cvt_f32_ubyte3_e32 v96, v208
	v_cvt_f32_ubyte0_e32 v99, v207
	v_cvt_f32_ubyte0_e32 v98, v209
	v_cvt_f32_ubyte1_e32 v101, v207
	v_cvt_f32_ubyte1_e32 v100, v209
	v_cvt_f32_ubyte2_e32 v103, v207
	v_cvt_f32_ubyte2_e32 v102, v209
	v_cvt_f32_ubyte3_e32 v73, v207
	v_cvt_f32_ubyte3_e32 v72, v209
	v_pk_mul_f32 v[74:75], v[76:77], s[16:17] op_sel_hi:[1,0]
	v_pk_mul_f32 v[76:77], v[78:79], s[16:17] op_sel_hi:[1,0]
	v_pk_mul_f32 v[78:79], v[94:95], s[16:17] op_sel_hi:[1,0]
	v_pk_mul_f32 v[94:95], v[96:97], s[16:17] op_sel_hi:[1,0]
	v_pk_mul_f32 v[96:97], v[98:99], s[16:17] op_sel_hi:[1,0]
	v_pk_mul_f32 v[98:99], v[100:101], s[16:17] op_sel_hi:[1,0]
	v_pk_mul_f32 v[100:101], v[102:103], s[16:17] op_sel_hi:[1,0]
	v_pk_mul_f32 v[72:73], v[72:73], s[16:17] op_sel_hi:[1,0]
	v_pk_mul_f32 v[58:59], v[58:59], v[100:101]
	v_pk_mul_f32 v[72:73], v[92:93], v[72:73]
	v_pk_mul_f32 v[60:61], v[60:61], v[74:75]
	v_pk_mul_f32 v[74:75], v[86:87], v[76:77]
	v_pk_mul_f32 v[62:63], v[62:63], v[78:79]
	v_pk_mul_f32 v[76:77], v[88:89], v[94:95]
	v_pk_mul_f32 v[56:57], v[56:57], v[96:97]
	v_pk_mul_f32 v[78:79], v[90:91], v[98:99]
	v_add_f32_e32 v59, v58, v59
	v_add_f32_e32 v72, v72, v73
	v_add_f32_e32 v60, v60, v61
	v_add_f32_e32 v61, v74, v75
	v_add_f32_e32 v62, v62, v63
	v_add_f32_e32 v63, v76, v77
	v_add_f32_e32 v74, v56, v57
	v_add_f32_e32 v75, v78, v79
	v_cvt_pk_bf16_f32 v56, v60, v61
	v_cvt_pk_bf16_f32 v57, v62, v63
	v_cvt_pk_bf16_f32 v58, v74, v75
	v_cvt_pk_bf16_f32 v59, v59, v72
	v_lshl_add_u64 v[72:73], s[42:43], 0, v[82:83]
	v_lshl_add_u64 v[72:73], v[72:73], 0, v[146:147]
	global_store_dwordx4 v[80:81], v[56:59], off offset:256
	v_mov_b32_e32 v74, v53
	v_mov_b32_e32 v76, v55
	v_mov_b32_e32 v78, v49
	v_mov_b32_e32 v80, v51
	s_waitcnt vmcnt(22)
; __device__ __forceinline__ unsigned cvt_pk_bf16(float lo, float hi) { unsigned r; asm volatile("v_cvt_pk_bf16_f32 %0, %1, %2" : "=v"(r) : "v"(lo), "v"(hi)); return r; }
; __device__ __forceinline__ float bf_lo(unsigned w) { return __uint_as_float(w << 16); }
; __device__ __forceinline__ float bf_hi(unsigned w) { return __uint_as_float(w & 0xffff0000u); }
;     __device__ __forceinline__ void operator()(const f32x4 (&acc)[2][2][4][2], const Unit& u, int wr, int wc, int fr, int fq) const {
;     ...
;             for (int m = 0; m < 4; ++m) { const size_t r = (size_t)(row0 + ai * HALF + m * 16); bf16_t* rowp = O + r * DM + col0; const unsigned char* gr = G8 + r * 4096 + col0; const bf16_t* yr = YA + r * DM + col0;
; #pragma unroll
;                 for (int bj = 0; bj < 2; ++bj) { const u32x2 g = *(const u32x2*)(gr + 2048 + bj * HALF), a = *(const u32x2*)(gr + bj * HALF); const u32x4 y = *(const u32x4*)(yr + bj * HALF);
;                     const f32x4 v0 = acc[ai][bj][m][0] * sv[bj][0], v1 = acc[ai][bj][m][1] * sv[bj][1];
;                     u32x4 w;
;                     w.x = cvt_pk_bf16(v0[0] * U8F(g.x, 0) + U8F(a.x, 0) * bf_lo(y.x), v0[1] * U8F(g.x, 1) + U8F(a.x, 1) * bf_hi(y.x));
;                     w.y = cvt_pk_bf16(v0[2] * U8F(g.x, 2) + U8F(a.x, 2) * bf_lo(y.y), v0[3] * U8F(g.x, 3) + U8F(a.x, 3) * bf_hi(y.y));
;                     w.z = cvt_pk_bf16(v1[0] * U8F(g.y, 0) + U8F(a.y, 0) * bf_lo(y.z), v1[1] * U8F(g.y, 1) + U8F(a.y, 1) * bf_hi(y.z));
;                     w.w = cvt_pk_bf16(v1[2] * U8F(g.y, 2) + U8F(a.y, 2) * bf_lo(y.w), v1[3] * U8F(g.y, 3) + U8F(a.y, 3) * bf_hi(y.w));
;                     *(u32x4*)(rowp + bj * HALF) = w; } }
	v_lshlrev_b32_e32 v53, 16, v210
	v_and_b32_e32 v75, 0xffff0000, v210
	v_lshlrev_b32_e32 v55, 16, v211
	v_and_b32_e32 v77, 0xffff0000, v211
	v_lshlrev_b32_e32 v49, 16, v212
	v_and_b32_e32 v79, 0xffff0000, v212
	v_lshlrev_b32_e32 v51, 16, v213
	v_and_b32_e32 v81, 0xffff0000, v213
	v_cvt_f32_ubyte0_e32 v61, v214
	v_cvt_f32_ubyte0_e32 v60, v216
	v_cvt_f32_ubyte1_e32 v63, v214
	v_cvt_f32_ubyte1_e32 v62, v216
	v_cvt_f32_ubyte2_e32 v87, v214
	v_cvt_f32_ubyte2_e32 v86, v216
	v_cvt_f32_ubyte3_e32 v89, v214
	v_cvt_f32_ubyte3_e32 v88, v216
	v_cvt_f32_ubyte0_e32 v91, v215
	v_cvt_f32_ubyte0_e32 v90, v217
	v_cvt_f32_ubyte1_e32 v93, v215
	v_cvt_f32_ubyte1_e32 v92, v217
	v_cvt_f32_ubyte2_e32 v95, v215
	v_cvt_f32_ubyte2_e32 v94, v217
	v_cvt_f32_ubyte3_e32 v57, v215
	v_cvt_f32_ubyte3_e32 v56, v217
	v_pk_mul_f32 v[58:59], v[60:61], s[16:17] op_sel_hi:[1,0]
	v_pk_mul_f32 v[60:61], v[62:63], s[16:17] op_sel_hi:[1,0]
	v_pk_mul_f32 v[62:63], v[86:87], s[16:17] op_sel_hi:[1,0]
	v_pk_mul_f32 v[86:87], v[88:89], s[16:17] op_sel_hi:[1,0]
	v_pk_mul_f32 v[88:89], v[90:91], s[16:17] op_sel_hi:[1,0]
	v_pk_mul_f32 v[90:91], v[92:93], s[16:17] op_sel_hi:[1,0]
	v_pk_mul_f32 v[92:93], v[94:95], s[16:17] op_sel_hi:[1,0]
	v_pk_mul_f32 v[56:57], v[56:57], s[16:17] op_sel_hi:[1,0]
	v_pk_mul_f32 v[50:51], v[50:51], v[92:93]
	v_pk_mul_f32 v[56:57], v[80:81], v[56:57]
	v_pk_mul_f32 v[52:53], v[52:53], v[58:59]
	v_pk_mul_f32 v[58:59], v[74:75], v[60:61]
	v_pk_mul_f32 v[54:55], v[54:55], v[62:63]
	v_pk_mul_f32 v[60:61], v[76:77], v[86:87]
	v_pk_mul_f32 v[48:49], v[48:49], v[88:89]
	v_pk_mul_f32 v[62:63], v[78:79], v[90:91]
	v_add_f32_e32 v51, v50, v51
	v_add_f32_e32 v56, v56, v57
	v_add_f32_e32 v52, v52, v53
	v_add_f32_e32 v53, v58, v59
	v_add_f32_e32 v54, v54, v55
	v_add_f32_e32 v55, v60, v61
	v_add_f32_e32 v58, v48, v49
	v_add_f32_e32 v59, v62, v63
	v_cvt_pk_bf16_f32 v48, v52, v53
	v_cvt_pk_bf16_f32 v49, v54, v55
	v_cvt_pk_bf16_f32 v50, v58, v59
	v_cvt_pk_bf16_f32 v51, v51, v56
	v_lshl_add_u64 v[56:57], s[4:5], 0, v[82:83]
	v_lshl_add_u64 v[56:57], v[56:57], 0, v[144:145]
	global_store_dwordx4 v[56:57], v[48:51], off
	v_mov_b32_e32 v62, v37
	v_mov_b32_e32 v72, v39
	v_mov_b32_e32 v74, v33
	v_mov_b32_e32 v76, v35
	v_lshl_add_u64 v[58:59], v[148:149], 0, s[26:27]
	v_lshl_add_u64 v[60:61], s[52:53], 0, v[58:59]
	v_lshl_add_u64 v[60:61], v[60:61], 0, v[144:145]
	s_mov_b64 s[26:27], 0xb0000
	s_waitcnt vmcnt(19)
	v_lshlrev_b32_e32 v37, 16, v218
	v_and_b32_e32 v63, 0xffff0000, v218
	v_lshlrev_b32_e32 v39, 16, v219
	v_and_b32_e32 v73, 0xffff0000, v219
	v_lshlrev_b32_e32 v33, 16, v220
	v_and_b32_e32 v75, 0xffff0000, v220
	v_lshlrev_b32_e32 v35, 16, v221
	v_and_b32_e32 v77, 0xffff0000, v221
	v_cvt_f32_ubyte0_e32 v53, v222
	v_cvt_f32_ubyte0_e32 v52, v224
	v_cvt_f32_ubyte1_e32 v55, v222
	v_cvt_f32_ubyte1_e32 v54, v224
	v_cvt_f32_ubyte2_e32 v79, v222
	v_cvt_f32_ubyte2_e32 v78, v224
	v_cvt_f32_ubyte3_e32 v81, v222
	v_cvt_f32_ubyte3_e32 v80, v224
	v_cvt_f32_ubyte0_e32 v83, v223
	v_cvt_f32_ubyte0_e32 v82, v225
	v_cvt_f32_ubyte1_e32 v85, v223
	v_cvt_f32_ubyte1_e32 v84, v225
	v_cvt_f32_ubyte2_e32 v87, v223
	v_cvt_f32_ubyte2_e32 v86, v225
	v_cvt_f32_ubyte3_e32 v49, v223
	v_cvt_f32_ubyte3_e32 v48, v225
	v_pk_mul_f32 v[50:51], v[52:53], s[16:17] op_sel_hi:[1,0]
	v_pk_mul_f32 v[52:53], v[54:55], s[16:17] op_sel_hi:[1,0]
	v_pk_mul_f32 v[54:55], v[78:79], s[16:17] op_sel_hi:[1,0]
	v_pk_mul_f32 v[78:79], v[80:81], s[16:17] op_sel_hi:[1,0]
	v_pk_mul_f32 v[80:81], v[82:83], s[16:17] op_sel_hi:[1,0]
	v_pk_mul_f32 v[82:83], v[84:85], s[16:17] op_sel_hi:[1,0]
	v_pk_mul_f32 v[84:85], v[86:87], s[16:17] op_sel_hi:[1,0]
	v_pk_mul_f32 v[48:49], v[48:49], s[16:17] op_sel_hi:[1,0]
	v_pk_mul_f32 v[34:35], v[34:35], v[84:85]
	v_pk_mul_f32 v[48:49], v[76:77], v[48:49]
	v_pk_mul_f32 v[36:37], v[36:37], v[50:51]
	v_pk_mul_f32 v[50:51], v[62:63], v[52:53]
	v_pk_mul_f32 v[38:39], v[38:39], v[54:55]
	v_pk_mul_f32 v[52:53], v[72:73], v[78:79]
	v_pk_mul_f32 v[32:33], v[32:33], v[80:81]
	v_pk_mul_f32 v[54:55], v[74:75], v[82:83]
	v_add_f32_e32 v35, v34, v35
	v_add_f32_e32 v48, v48, v49
	v_add_f32_e32 v36, v36, v37
	v_add_f32_e32 v37, v50, v51
	v_add_f32_e32 v38, v38, v39
	v_add_f32_e32 v39, v52, v53
	v_add_f32_e32 v50, v32, v33
	v_add_f32_e32 v51, v54, v55
	v_cvt_pk_bf16_f32 v32, v36, v37
	v_cvt_pk_bf16_f32 v33, v38, v39
	v_cvt_pk_bf16_f32 v34, v50, v51
	v_cvt_pk_bf16_f32 v35, v35, v48
	v_lshl_add_u64 v[48:49], s[42:43], 0, v[58:59]
	v_lshl_add_u64 v[48:49], v[48:49], 0, v[146:147]
	global_store_dwordx4 v[56:57], v[32:35], off offset:256
	v_mov_b32_e32 v50, v29
	v_mov_b32_e32 v52, v31
	v_mov_b32_e32 v54, v25
	v_mov_b32_e32 v56, v27
	s_waitcnt vmcnt(16)
; __device__ __forceinline__ unsigned cvt_pk_bf16(float lo, float hi) { unsigned r; asm volatile("v_cvt_pk_bf16_f32 %0, %1, %2" : "=v"(r) : "v"(lo), "v"(hi)); return r; }
; __device__ __forceinline__ float bf_lo(unsigned w) { return __uint_as_float(w << 16); }
; __device__ __forceinline__ float bf_hi(unsigned w) { return __uint_as_float(w & 0xffff0000u); }
;     __device__ __forceinline__ void operator()(const f32x4 (&acc)[2][2][4][2], const Unit& u, int wr, int wc, int fr, int fq) const {
;     ...
;             for (int m = 0; m < 4; ++m) { const size_t r = (size_t)(row0 + ai * HALF + m * 16); bf16_t* rowp = O + r * DM + col0; const unsigned char* gr = G8 + r * 4096 + col0; const bf16_t* yr = YA + r * DM + col0;
; #pragma unroll
;                 for (int bj = 0; bj < 2; ++bj) { const u32x2 g = *(const u32x2*)(gr + 2048 + bj * HALF), a = *(const u32x2*)(gr + bj * HALF); const u32x4 y = *(const u32x4*)(yr + bj * HALF);
;                     const f32x4 v0 = acc[ai][bj][m][0] * sv[bj][0], v1 = acc[ai][bj][m][1] * sv[bj][1];
;                     u32x4 w;
;                     w.x = cvt_pk_bf16(v0[0] * U8F(g.x, 0) + U8F(a.x, 0) * bf_lo(y.x), v0[1] * U8F(g.x, 1) + U8F(a.x, 1) * bf_hi(y.x));
;                     w.y = cvt_pk_bf16(v0[2] * U8F(g.x, 2) + U8F(a.x, 2) * bf_lo(y.y), v0[3] * U8F(g.x, 3) + U8F(a.x, 3) * bf_hi(y.y));
;                     w.z = cvt_pk_bf16(v1[0] * U8F(g.y, 0) + U8F(a.y, 0) * bf_lo(y.z), v1[1] * U8F(g.y, 1) + U8F(a.y, 1) * bf_hi(y.z));
;                     w.w = cvt_pk_bf16(v1[2] * U8F(g.y, 2) + U8F(a.y, 2) * bf_lo(y.w), v1[3] * U8F(g.y, 3) + U8F(a.y, 3) * bf_hi(y.w));
;                     *(u32x4*)(rowp + bj * HALF) = w; } }
	v_lshlrev_b32_e32 v29, 16, v226
	v_and_b32_e32 v51, 0xffff0000, v226
	v_lshlrev_b32_e32 v31, 16, v227
	v_and_b32_e32 v53, 0xffff0000, v227
	v_lshlrev_b32_e32 v25, 16, v228
	v_and_b32_e32 v55, 0xffff0000, v228
	v_lshlrev_b32_e32 v27, 16, v229
	v_and_b32_e32 v57, 0xffff0000, v229
	v_cvt_f32_ubyte0_e32 v37, v230
	v_cvt_f32_ubyte0_e32 v36, v232
	v_cvt_f32_ubyte1_e32 v39, v230
	v_cvt_f32_ubyte1_e32 v38, v232
	v_cvt_f32_ubyte2_e32 v63, v230
	v_cvt_f32_ubyte2_e32 v62, v232
	v_cvt_f32_ubyte3_e32 v73, v230
	v_cvt_f32_ubyte3_e32 v72, v232
	v_cvt_f32_ubyte0_e32 v75, v231
	v_cvt_f32_ubyte0_e32 v74, v233
	v_cvt_f32_ubyte1_e32 v77, v231
	v_cvt_f32_ubyte1_e32 v76, v233
	v_cvt_f32_ubyte2_e32 v79, v231
	v_cvt_f32_ubyte2_e32 v78, v233
	v_cvt_f32_ubyte3_e32 v33, v231
	v_cvt_f32_ubyte3_e32 v32, v233
	v_pk_mul_f32 v[34:35], v[36:37], s[16:17] op_sel_hi:[1,0]
	v_pk_mul_f32 v[36:37], v[38:39], s[16:17] op_sel_hi:[1,0]
	v_pk_mul_f32 v[38:39], v[62:63], s[16:17] op_sel_hi:[1,0]
	v_pk_mul_f32 v[62:63], v[72:73], s[16:17] op_sel_hi:[1,0]
	v_pk_mul_f32 v[72:73], v[74:75], s[16:17] op_sel_hi:[1,0]
	v_pk_mul_f32 v[74:75], v[76:77], s[16:17] op_sel_hi:[1,0]
	v_pk_mul_f32 v[76:77], v[78:79], s[16:17] op_sel_hi:[1,0]
	v_pk_mul_f32 v[32:33], v[32:33], s[16:17] op_sel_hi:[1,0]
	v_pk_mul_f32 v[26:27], v[26:27], v[76:77]
	v_pk_mul_f32 v[32:33], v[56:57], v[32:33]
	v_pk_mul_f32 v[28:29], v[28:29], v[34:35]
	v_pk_mul_f32 v[34:35], v[50:51], v[36:37]
	v_pk_mul_f32 v[30:31], v[30:31], v[38:39]
	v_pk_mul_f32 v[36:37], v[52:53], v[62:63]
	v_pk_mul_f32 v[24:25], v[24:25], v[72:73]
	v_pk_mul_f32 v[38:39], v[54:55], v[74:75]
	v_add_f32_e32 v27, v26, v27
	v_add_f32_e32 v32, v32, v33
	v_add_f32_e32 v28, v28, v29
	v_add_f32_e32 v29, v34, v35
	v_add_f32_e32 v30, v30, v31
	v_add_f32_e32 v31, v36, v37
	v_add_f32_e32 v34, v24, v25
	v_add_f32_e32 v35, v38, v39
	v_cvt_pk_bf16_f32 v24, v28, v29
	v_cvt_pk_bf16_f32 v25, v30, v31
	v_cvt_pk_bf16_f32 v26, v34, v35
	v_cvt_pk_bf16_f32 v27, v27, v32
	v_lshl_add_u64 v[32:33], s[4:5], 0, v[58:59]
	v_lshl_add_u64 v[32:33], v[32:33], 0, v[144:145]
	global_store_dwordx4 v[32:33], v[24:27], off
	v_mov_b32_e32 v38, v21
	v_mov_b32_e32 v48, v23
	v_mov_b32_e32 v50, v17
	v_mov_b32_e32 v52, v19
	v_lshl_add_u64 v[34:35], v[148:149], 0, s[26:27]
	v_lshl_add_u64 v[36:37], s[52:53], 0, v[34:35]
	v_lshl_add_u64 v[36:37], v[36:37], 0, v[144:145]
	s_waitcnt vmcnt(13)
	v_lshlrev_b32_e32 v21, 16, v234
	v_and_b32_e32 v39, 0xffff0000, v234
	v_lshlrev_b32_e32 v23, 16, v235
	v_and_b32_e32 v49, 0xffff0000, v235
	v_lshlrev_b32_e32 v17, 16, v236
	v_and_b32_e32 v51, 0xffff0000, v236
	v_lshlrev_b32_e32 v19, 16, v237
	v_and_b32_e32 v53, 0xffff0000, v237
	v_cvt_f32_ubyte0_e32 v29, v238
	v_cvt_f32_ubyte0_e32 v28, v240
	v_cvt_f32_ubyte1_e32 v31, v238
	v_cvt_f32_ubyte1_e32 v30, v240
	v_cvt_f32_ubyte2_e32 v55, v238
	v_cvt_f32_ubyte2_e32 v54, v240
	v_cvt_f32_ubyte3_e32 v57, v238
	v_cvt_f32_ubyte3_e32 v56, v240
	v_cvt_f32_ubyte0_e32 v59, v239
	v_cvt_f32_ubyte0_e32 v58, v241
	v_cvt_f32_ubyte1_e32 v61, v239
	v_cvt_f32_ubyte1_e32 v60, v241
	v_cvt_f32_ubyte2_e32 v63, v239
	v_cvt_f32_ubyte2_e32 v62, v241
	v_cvt_f32_ubyte3_e32 v25, v239
	v_cvt_f32_ubyte3_e32 v24, v241
	v_pk_mul_f32 v[26:27], v[28:29], s[16:17] op_sel_hi:[1,0]
	v_pk_mul_f32 v[28:29], v[30:31], s[16:17] op_sel_hi:[1,0]
	v_pk_mul_f32 v[30:31], v[54:55], s[16:17] op_sel_hi:[1,0]
	v_pk_mul_f32 v[54:55], v[56:57], s[16:17] op_sel_hi:[1,0]
	v_pk_mul_f32 v[56:57], v[58:59], s[16:17] op_sel_hi:[1,0]
	v_pk_mul_f32 v[58:59], v[60:61], s[16:17] op_sel_hi:[1,0]
	v_pk_mul_f32 v[60:61], v[62:63], s[16:17] op_sel_hi:[1,0]
	v_pk_mul_f32 v[24:25], v[24:25], s[16:17] op_sel_hi:[1,0]
	v_pk_mul_f32 v[18:19], v[18:19], v[60:61]
	v_pk_mul_f32 v[24:25], v[52:53], v[24:25]
	v_pk_mul_f32 v[20:21], v[20:21], v[26:27]
	v_pk_mul_f32 v[26:27], v[38:39], v[28:29]
	v_pk_mul_f32 v[22:23], v[22:23], v[30:31]
	v_pk_mul_f32 v[28:29], v[48:49], v[54:55]
	v_pk_mul_f32 v[16:17], v[16:17], v[56:57]
	v_pk_mul_f32 v[30:31], v[50:51], v[58:59]
	v_add_f32_e32 v19, v18, v19
	v_add_f32_e32 v24, v24, v25
	v_add_f32_e32 v20, v20, v21
	v_add_f32_e32 v21, v26, v27
	v_add_f32_e32 v22, v22, v23
	v_add_f32_e32 v23, v28, v29
	v_add_f32_e32 v26, v16, v17
	v_add_f32_e32 v27, v30, v31
	v_cvt_pk_bf16_f32 v16, v20, v21
	v_cvt_pk_bf16_f32 v17, v22, v23
	v_cvt_pk_bf16_f32 v18, v26, v27
	v_cvt_pk_bf16_f32 v19, v19, v24
	v_lshl_add_u64 v[24:25], s[42:43], 0, v[34:35]
	v_lshl_add_u64 v[24:25], v[24:25], 0, v[146:147]
	global_store_dwordx4 v[32:33], v[16:19], off offset:256
	v_mov_b32_e32 v26, v13
	v_mov_b32_e32 v28, v15
	v_mov_b32_e32 v30, v9
	v_mov_b32_e32 v32, v11
	s_waitcnt vmcnt(10)
; __device__ __forceinline__ unsigned cvt_pk_bf16(float lo, float hi) { unsigned r; asm volatile("v_cvt_pk_bf16_f32 %0, %1, %2" : "=v"(r) : "v"(lo), "v"(hi)); return r; }
; __device__ __forceinline__ float bf_lo(unsigned w) { return __uint_as_float(w << 16); }
; __device__ __forceinline__ float bf_hi(unsigned w) { return __uint_as_float(w & 0xffff0000u); }
;     __device__ __forceinline__ void operator()(const f32x4 (&acc)[2][2][4][2], const Unit& u, int wr, int wc, int fr, int fq) const {
;     ...
;             for (int m = 0; m < 4; ++m) { const size_t r = (size_t)(row0 + ai * HALF + m * 16); bf16_t* rowp = O + r * DM + col0; const unsigned char* gr = G8 + r * 4096 + col0; const bf16_t* yr = YA + r * DM + col0;
; #pragma unroll
;                 for (int bj = 0; bj < 2; ++bj) { const u32x2 g = *(const u32x2*)(gr + 2048 + bj * HALF), a = *(const u32x2*)(gr + bj * HALF); const u32x4 y = *(const u32x4*)(yr + bj * HALF);
;                     const f32x4 v0 = acc[ai][bj][m][0] * sv[bj][0], v1 = acc[ai][bj][m][1] * sv[bj][1];
;                     u32x4 w;
;                     w.x = cvt_pk_bf16(v0[0] * U8F(g.x, 0) + U8F(a.x, 0) * bf_lo(y.x), v0[1] * U8F(g.x, 1) + U8F(a.x, 1) * bf_hi(y.x));
;                     w.y = cvt_pk_bf16(v0[2] * U8F(g.x, 2) + U8F(a.x, 2) * bf_lo(y.y), v0[3] * U8F(g.x, 3) + U8F(a.x, 3) * bf_hi(y.y));
;                     w.z = cvt_pk_bf16(v1[0] * U8F(g.y, 0) + U8F(a.y, 0) * bf_lo(y.z), v1[1] * U8F(g.y, 1) + U8F(a.y, 1) * bf_hi(y.z));
;                     w.w = cvt_pk_bf16(v1[2] * U8F(g.y, 2) + U8F(a.y, 2) * bf_lo(y.w), v1[3] * U8F(g.y, 3) + U8F(a.y, 3) * bf_hi(y.w));
;                     *(u32x4*)(rowp + bj * HALF) = w; } }
; template <bool FP8 = false, class Epi, class Sched>
; __device__ __forceinline__ void gemm_phase(LAS unsigned char* lds, const int K, const int lda, const int ldb, const Sched& S, const Epi& E, const int wid) {
;     ...
;         if (wr == 0) PG8_BAR;
;         { const int l2 = lane_id(); E(acc, cur, wr, wc, l2 & 15, l2 >> 4); }
;         if (!has_next) break;
; #pragma unroll
;         for (int a = 0; a < 2; ++a)
; #pragma unroll
;             for (int b = 0; b < 2; ++b)
; #pragma unroll
;                 for (int m = 0; m < 4; ++m)
; #pragma unroll
;                     for (int n = 0; n < 2; ++n) acc[a][b][m][n] = (f32x4){0.f, 0.f, 0.f, 0.f};
;         cur = nxt; cA = nA; cB = nB; ++ui;
;         if (wr == 1) PG8_BAR;
	v_lshlrev_b32_e32 v13, 16, v242
	v_and_b32_e32 v27, 0xffff0000, v242
	v_lshlrev_b32_e32 v15, 16, v243
	v_and_b32_e32 v29, 0xffff0000, v243
	v_lshlrev_b32_e32 v9, 16, v244
	v_and_b32_e32 v31, 0xffff0000, v244
	v_lshlrev_b32_e32 v11, 16, v245
	v_and_b32_e32 v33, 0xffff0000, v245
	v_cvt_f32_ubyte0_e32 v21, v246
	v_cvt_f32_ubyte0_e32 v20, v248
	v_cvt_f32_ubyte1_e32 v23, v246
	v_cvt_f32_ubyte1_e32 v22, v248
	v_cvt_f32_ubyte2_e32 v39, v246
	v_cvt_f32_ubyte2_e32 v38, v248
	v_cvt_f32_ubyte3_e32 v49, v246
	v_cvt_f32_ubyte3_e32 v48, v248
	v_cvt_f32_ubyte0_e32 v51, v247
	v_cvt_f32_ubyte0_e32 v50, v249
	v_cvt_f32_ubyte1_e32 v53, v247
	v_cvt_f32_ubyte1_e32 v52, v249
	v_cvt_f32_ubyte2_e32 v55, v247
	v_cvt_f32_ubyte2_e32 v54, v249
	v_cvt_f32_ubyte3_e32 v17, v247
	v_cvt_f32_ubyte3_e32 v16, v249
	v_pk_mul_f32 v[18:19], v[20:21], s[16:17] op_sel_hi:[1,0]
	v_pk_mul_f32 v[20:21], v[22:23], s[16:17] op_sel_hi:[1,0]
	v_pk_mul_f32 v[22:23], v[38:39], s[16:17] op_sel_hi:[1,0]
	v_pk_mul_f32 v[38:39], v[48:49], s[16:17] op_sel_hi:[1,0]
	v_pk_mul_f32 v[48:49], v[50:51], s[16:17] op_sel_hi:[1,0]
	v_pk_mul_f32 v[50:51], v[52:53], s[16:17] op_sel_hi:[1,0]
	v_pk_mul_f32 v[52:53], v[54:55], s[16:17] op_sel_hi:[1,0]
	v_pk_mul_f32 v[16:17], v[16:17], s[16:17] op_sel_hi:[1,0]
	v_pk_mul_f32 v[10:11], v[10:11], v[52:53]
	v_pk_mul_f32 v[16:17], v[32:33], v[16:17]
	v_pk_mul_f32 v[12:13], v[12:13], v[18:19]
	v_pk_mul_f32 v[18:19], v[26:27], v[20:21]
	v_pk_mul_f32 v[14:15], v[14:15], v[22:23]
	v_pk_mul_f32 v[20:21], v[28:29], v[38:39]
	v_pk_mul_f32 v[8:9], v[8:9], v[48:49]
	v_pk_mul_f32 v[22:23], v[30:31], v[50:51]
	v_add_f32_e32 v11, v10, v11
	v_add_f32_e32 v16, v16, v17
	v_add_f32_e32 v12, v12, v13
	v_add_f32_e32 v13, v18, v19
	v_add_f32_e32 v14, v14, v15
	v_add_f32_e32 v15, v20, v21
	v_add_f32_e32 v18, v8, v9
	v_add_f32_e32 v19, v22, v23
	v_cvt_pk_bf16_f32 v8, v12, v13
	v_cvt_pk_bf16_f32 v9, v14, v15
	v_cvt_pk_bf16_f32 v10, v18, v19
	v_cvt_pk_bf16_f32 v11, v11, v16
	v_lshl_add_u64 v[16:17], s[4:5], 0, v[34:35]
	v_lshl_add_u64 v[16:17], v[16:17], 0, v[144:145]
	global_store_dwordx4 v[16:17], v[8:11], off
	v_mov_b32_e32 v18, v5
	v_mov_b32_e32 v20, v7
	v_mov_b32_e32 v22, v1
	v_mov_b32_e32 v24, v3
	s_waitcnt vmcnt(7)
	v_lshlrev_b32_e32 v5, 16, v194
	v_and_b32_e32 v19, 0xffff0000, v194
	v_lshlrev_b32_e32 v7, 16, v195
	v_and_b32_e32 v21, 0xffff0000, v195
	v_lshlrev_b32_e32 v1, 16, v196
	v_and_b32_e32 v23, 0xffff0000, v196
	v_lshlrev_b32_e32 v3, 16, v197
	v_and_b32_e32 v25, 0xffff0000, v197
	v_cvt_f32_ubyte0_e32 v13, v198
	v_cvt_f32_ubyte0_e32 v12, v200
	v_cvt_f32_ubyte1_e32 v15, v198
	v_cvt_f32_ubyte1_e32 v14, v200
	v_cvt_f32_ubyte2_e32 v27, v198
	v_cvt_f32_ubyte2_e32 v26, v200
	v_cvt_f32_ubyte3_e32 v29, v198
	v_cvt_f32_ubyte3_e32 v28, v200
	v_cvt_f32_ubyte0_e32 v31, v199
	v_cvt_f32_ubyte0_e32 v30, v201
	v_cvt_f32_ubyte1_e32 v33, v199
	v_cvt_f32_ubyte1_e32 v32, v201
	v_cvt_f32_ubyte2_e32 v35, v199
	v_cvt_f32_ubyte2_e32 v34, v201
	v_cvt_f32_ubyte3_e32 v9, v199
	v_cvt_f32_ubyte3_e32 v8, v201
	v_pk_mul_f32 v[10:11], v[12:13], s[16:17] op_sel_hi:[1,0]
	v_pk_mul_f32 v[12:13], v[14:15], s[16:17] op_sel_hi:[1,0]
	v_pk_mul_f32 v[14:15], v[26:27], s[16:17] op_sel_hi:[1,0]
	v_pk_mul_f32 v[26:27], v[28:29], s[16:17] op_sel_hi:[1,0]
	v_pk_mul_f32 v[28:29], v[30:31], s[16:17] op_sel_hi:[1,0]
	v_pk_mul_f32 v[30:31], v[32:33], s[16:17] op_sel_hi:[1,0]
	v_pk_mul_f32 v[32:33], v[34:35], s[16:17] op_sel_hi:[1,0]
	v_pk_mul_f32 v[8:9], v[8:9], s[16:17] op_sel_hi:[1,0]
	v_pk_mul_f32 v[2:3], v[2:3], v[32:33]
	v_pk_mul_f32 v[4:5], v[4:5], v[10:11]
	v_pk_mul_f32 v[10:11], v[18:19], v[12:13]
	v_pk_mul_f32 v[6:7], v[6:7], v[14:15]
	v_pk_mul_f32 v[12:13], v[20:21], v[26:27]
	v_pk_mul_f32 v[0:1], v[0:1], v[28:29]
	v_pk_mul_f32 v[14:15], v[22:23], v[30:31]
	v_pk_mul_f32 v[8:9], v[24:25], v[8:9]
	v_add_f32_e32 v3, v2, v3
	v_add_f32_e32 v4, v4, v5
	v_add_f32_e32 v5, v10, v11
	v_add_f32_e32 v6, v6, v7
	v_add_f32_e32 v7, v12, v13
	v_add_f32_e32 v10, v0, v1
	v_add_f32_e32 v11, v14, v15
	v_add_f32_e32 v8, v8, v9
	v_cvt_pk_bf16_f32 v0, v4, v5
	v_cvt_pk_bf16_f32 v1, v6, v7
	v_cvt_pk_bf16_f32 v2, v10, v11
	v_cvt_pk_bf16_f32 v3, v3, v8
	global_store_dwordx4 v[16:17], v[0:3], off offset:256
	s_cbranch_vccnz .LBB0_832
	s_andn2_b64 vcc, exec, s[12:13]
	s_cbranch_vccnz .LBB0_831
	s_barrier
	s_branch .LBB0_831

;     __device__ __forceinline__ void init(const void* A_, int slabA_, const void* Bt_, size_t estride_bytes, int rowbytes, const LAS int* ts_, int nN_, int G_, int c_) { slabA = slabA_; A = (const char*)A_; Bt = (const char*)Bt_; estride = estride_bytes; rowb = rowbytes; ts = ts_; nN = nN_; nwg = __builtin_amdgcn_readfirstlane(ts_[NE]) * nN_; G = G_; c = c_; }
; #define GRID_BAR() do { if (N_LAUNCHES == 1) xcd_barrier(bar, wave == 0 && lane_id() == 0); } while (0)
; #define BOTH(k) (IN(k) && IN((k) + 1))
; __global__ void __launch_bounds__(512, 2) fwd_kernel(Params p) {
;     ...
;         if (BOTH(5)) GRID_BAR();
;     }
;     if (IN(6)) {
;         { pg8::PoolOrder S; S.init(POOLED, 1024, WpoolT, 256, T, 2048, G, bx); pg8::EpiPool E{MERGED, G8, YA, p.in[I_SPOOL]}; pg8::gemm_phase(lds, 256, 1024, 256, S, E, wave); }
;         if (BOTH(6)) GRID_BAR();
;     }
;     if (IN(7)) {
;         pg8::DenseOrder S; S.init(MERGED, DM, WoutT, DM, T, DM, G, bx);
;         pg8::EpiOut E{p.in[I_X], X1, H2, p.in[I_GFFN]};
;         pg8::gemm_phase(lds, DM, DM, DM, S, E, wave);
.LBB0_901:
	s_or_b64 exec, exec, s[10:11]
	s_add_u32 s10, s28, 0x17800000
	s_addc_u32 s11, s29, 0
	s_add_u32 s14, s28, 0x9c000000
	s_addc_u32 s15, s29, 0
	s_andn2_b64 vcc, exec, s[6:7]
	s_waitcnt lgkmcnt(0)
	s_barrier
	s_nop 0
	s_nop 0
	v_mbcnt_lo_u32_b32 v0, -1, 0
	v_mbcnt_hi_u32_b32 v0, -1, v0
	s_cbranch_vccnz .LBB0_925
	s_ashr_i32 s0, s2, 31
	s_lshr_b32 s0, s0, 29
	s_add_i32 s3, s2, s0
	s_and_b32 s0, s3, -8
	s_sub_i32 s0, s2, s0
	s_cmp_gt_i32 s0, -1
	s_cbranch_scc0 .LBB0_904
	s_lshl_b32 s8, s0, 6
	s_cbranch_execz .LBB0_905
	s_branch .LBB0_906

; template <bool FP8 = false, class Epi, class Sched>
; __device__ __forceinline__ void gemm_phase(LAS unsigned char* lds, const int K, const int lda, const int ldb, const Sched& S, const Epi& E, const int wid) {
;     ...
; #pragma unroll
;         for (int a = 0; a < 2; ++a)
; #pragma unroll
;             for (int b = 0; b < 2; ++b)
; #pragma unroll
;                 for (int m = 0; m < 4; ++m)
; #pragma unroll
;                     for (int n = 0; n < 2; ++n) acc[a][b][m][n] = (f32x4){0.f, 0.f, 0.f, 0.f};
.LBB0_917:
	s_add_u32 s43, s56, 0x100
	v_mov_b32_e32 v0, 0
	s_addc_u32 s69, s57, 0
	s_mov_b32 s70, -2
	v_mov_b32_e32 v1, v0
	v_mov_b64_e32 v[2:3], 0
	v_mov_b64_e32 v[4:5], 0
	v_mov_b64_e32 v[6:7], 0
	s_waitcnt vmcnt(14)
	v_mov_b64_e32 v[16:17], 0
	v_mov_b64_e32 v[18:19], 0
	v_mov_b64_e32 v[20:21], 0
	v_mov_b64_e32 v[22:23], 0
	s_waitcnt vmcnt(10)
	v_mov_b64_e32 v[32:33], 0
	v_mov_b64_e32 v[34:35], 0
	v_mov_b64_e32 v[36:37], 0
	v_mov_b64_e32 v[38:39], 0
	s_waitcnt vmcnt(6)
	v_mov_b64_e32 v[48:49], 0
	v_mov_b64_e32 v[50:51], 0
	v_mov_b64_e32 v[52:53], 0
	v_mov_b64_e32 v[54:55], 0
	v_mov_b64_e32 v[8:9], 0
	v_mov_b64_e32 v[10:11], 0
	v_mov_b64_e32 v[12:13], 0
	v_mov_b64_e32 v[14:15], 0
	v_mov_b64_e32 v[24:25], 0
	v_mov_b64_e32 v[26:27], 0
	v_mov_b64_e32 v[28:29], 0
	v_mov_b64_e32 v[30:31], 0
	v_mov_b64_e32 v[40:41], 0
	v_mov_b64_e32 v[42:43], 0
	v_mov_b64_e32 v[44:45], 0
	v_mov_b64_e32 v[46:47], 0
	s_waitcnt vmcnt(4)
	v_mov_b64_e32 v[56:57], 0
	v_mov_b64_e32 v[58:59], 0
	v_mov_b64_e32 v[60:61], 0
	v_mov_b64_e32 v[62:63], 0
	v_mov_b64_e32 v[64:65], 0
	v_mov_b64_e32 v[66:67], 0
	v_mov_b64_e32 v[68:69], 0
	v_mov_b64_e32 v[70:71], 0
	v_mov_b64_e32 v[80:81], 0
	v_mov_b64_e32 v[82:83], 0
	v_mov_b64_e32 v[84:85], 0
	v_mov_b64_e32 v[86:87], 0
	v_mov_b64_e32 v[104:105], 0
	v_mov_b64_e32 v[106:107], 0
	v_mov_b64_e32 v[108:109], 0
	v_mov_b64_e32 v[110:111], 0
	v_mov_b64_e32 v[128:129], 0
	v_mov_b64_e32 v[130:131], 0
	v_mov_b64_e32 v[132:133], 0
	v_mov_b64_e32 v[134:135], 0
	v_mov_b64_e32 v[72:73], 0
	v_mov_b32_e32 v74, v0
	v_mov_b32_e32 v75, v0
	v_mov_b32_e32 v76, v0
	v_mov_b32_e32 v77, v0
	v_mov_b32_e32 v78, v0
	v_mov_b32_e32 v79, v0
	v_mov_b32_e32 v88, v0
	v_mov_b32_e32 v89, v0
	v_mov_b32_e32 v90, v0
	v_mov_b32_e32 v91, v0
	v_mov_b32_e32 v92, v0
	v_mov_b32_e32 v93, v0
	v_mov_b32_e32 v94, v0
	v_mov_b32_e32 v95, v0
	v_mov_b32_e32 v120, v0
	v_mov_b32_e32 v121, v0
	v_mov_b32_e32 v122, v0
	v_mov_b32_e32 v123, v0
	v_mov_b32_e32 v124, v0
	v_mov_b32_e32 v125, v0
	v_mov_b32_e32 v126, v0
	v_mov_b32_e32 v127, v0
	v_mov_b32_e32 v136, v0
	v_mov_b32_e32 v137, v0
	v_mov_b32_e32 v138, v0
	v_mov_b32_e32 v139, v0
	v_mov_b32_e32 v140, v0
	v_mov_b32_e32 v141, v0
	v_mov_b32_e32 v142, v0
	v_mov_b32_e32 v143, v0

; template <bool FP8 = false, class Epi, class Sched>
; __device__ __forceinline__ void gemm_phase(LAS unsigned char* lds, const int K, const int lda, const int ldb, const Sched& S, const Epi& E, const int wid) {
;     ...
; #pragma unroll
;         for (int a = 0; a < 2; ++a)
; #pragma unroll
;             for (int b = 0; b < 2; ++b)
; #pragma unroll
;                 for (int m = 0; m < 4; ++m)
; #pragma unroll
;                     for (int n = 0; n < 2; ++n) acc[a][b][m][n] = (f32x4){0.f, 0.f, 0.f, 0.f};
.LBB0_1058:
	s_add_u32 s39, s56, 0x100
	v_mov_b32_e32 v0, 0
	s_addc_u32 s43, s57, 0
	s_mov_b32 s49, -2
	v_mov_b32_e32 v1, v0
	v_mov_b64_e32 v[2:3], 0
	v_mov_b64_e32 v[4:5], 0
	v_mov_b64_e32 v[6:7], 0
	s_waitcnt vmcnt(14)
	v_mov_b64_e32 v[16:17], 0
	v_mov_b64_e32 v[18:19], 0
	v_mov_b64_e32 v[20:21], 0
	v_mov_b64_e32 v[22:23], 0
	s_waitcnt vmcnt(10)
	v_mov_b64_e32 v[32:33], 0
	v_mov_b64_e32 v[34:35], 0
	v_mov_b64_e32 v[36:37], 0
	v_mov_b64_e32 v[38:39], 0
	s_waitcnt vmcnt(6)
	v_mov_b64_e32 v[48:49], 0
	v_mov_b64_e32 v[50:51], 0
	v_mov_b64_e32 v[52:53], 0
	v_mov_b64_e32 v[54:55], 0
	v_mov_b64_e32 v[8:9], 0
	v_mov_b64_e32 v[10:11], 0
	v_mov_b64_e32 v[12:13], 0
	v_mov_b64_e32 v[14:15], 0
	v_mov_b64_e32 v[24:25], 0
	v_mov_b64_e32 v[26:27], 0
	v_mov_b64_e32 v[28:29], 0
	v_mov_b64_e32 v[30:31], 0
	v_mov_b64_e32 v[40:41], 0
	v_mov_b64_e32 v[42:43], 0
	v_mov_b64_e32 v[44:45], 0
	v_mov_b64_e32 v[46:47], 0
	s_waitcnt vmcnt(4)
	v_mov_b64_e32 v[56:57], 0
	v_mov_b64_e32 v[58:59], 0
	v_mov_b64_e32 v[60:61], 0
	v_mov_b64_e32 v[62:63], 0
	v_mov_b64_e32 v[64:65], 0
	v_mov_b64_e32 v[66:67], 0
	v_mov_b64_e32 v[68:69], 0
	v_mov_b64_e32 v[70:71], 0
	v_mov_b64_e32 v[96:97], 0
	v_mov_b64_e32 v[98:99], 0
	v_mov_b64_e32 v[100:101], 0
	v_mov_b64_e32 v[102:103], 0
	v_mov_b64_e32 v[112:113], 0
	v_mov_b64_e32 v[114:115], 0
	v_mov_b64_e32 v[116:117], 0
	v_mov_b64_e32 v[118:119], 0
	v_mov_b64_e32 v[128:129], 0
	v_mov_b64_e32 v[130:131], 0
	v_mov_b64_e32 v[132:133], 0
	v_mov_b64_e32 v[134:135], 0
	v_mov_b64_e32 v[72:73], 0
	v_mov_b32_e32 v74, v0
	v_mov_b32_e32 v75, v0
	v_mov_b32_e32 v76, v0
	v_mov_b32_e32 v77, v0
	v_mov_b32_e32 v78, v0
	v_mov_b32_e32 v79, v0
	v_mov_b32_e32 v104, v0
	v_mov_b32_e32 v105, v0
	v_mov_b32_e32 v106, v0
	v_mov_b32_e32 v107, v0
	v_mov_b32_e32 v108, v0
	v_mov_b32_e32 v109, v0
	v_mov_b32_e32 v110, v0
	v_mov_b32_e32 v111, v0
	v_mov_b32_e32 v120, v0
	v_mov_b32_e32 v121, v0
	v_mov_b32_e32 v122, v0
	v_mov_b32_e32 v123, v0
	v_mov_b32_e32 v124, v0
	v_mov_b32_e32 v125, v0
	v_mov_b32_e32 v126, v0
	v_mov_b32_e32 v127, v0
	v_mov_b32_e32 v136, v0
	v_mov_b32_e32 v137, v0
	v_mov_b32_e32 v138, v0
	v_mov_b32_e32 v139, v0
	v_mov_b32_e32 v140, v0
	v_mov_b32_e32 v141, v0
	v_mov_b32_e32 v142, v0
	v_mov_b32_e32 v143, v0

; template <bool FP8 = false, class Epi, class Sched>
; __device__ __forceinline__ void gemm_phase(LAS unsigned char* lds, const int K, const int lda, const int ldb, const Sched& S, const Epi& E, const int wid) {
;     ...
; #pragma unroll
;         for (int a = 0; a < 2; ++a)
; #pragma unroll
;             for (int b = 0; b < 2; ++b)
; #pragma unroll
;                 for (int m = 0; m < 4; ++m)
; #pragma unroll
;                     for (int n = 0; n < 2; ++n) acc[a][b][m][n] = (f32x4){0.f, 0.f, 0.f, 0.f};
.LBB0_1132:
	s_add_u32 s45, s66, 0x100
	v_mov_b32_e32 v0, 0
	s_addc_u32 s49, s67, 0
	s_mov_b32 s51, -2
	v_mov_b32_e32 v1, v0
	v_mov_b64_e32 v[2:3], 0
	v_mov_b64_e32 v[4:5], 0
	v_mov_b64_e32 v[6:7], 0
	s_waitcnt vmcnt(14)
	v_mov_b64_e32 v[16:17], 0
	v_mov_b64_e32 v[18:19], 0
	v_mov_b64_e32 v[20:21], 0
	v_mov_b64_e32 v[22:23], 0
	s_waitcnt vmcnt(10)
	v_mov_b64_e32 v[32:33], 0
	v_mov_b64_e32 v[34:35], 0
	v_mov_b64_e32 v[36:37], 0
	v_mov_b64_e32 v[38:39], 0
	s_waitcnt vmcnt(6)
	v_mov_b64_e32 v[48:49], 0
	v_mov_b64_e32 v[50:51], 0
	v_mov_b64_e32 v[52:53], 0
	v_mov_b64_e32 v[54:55], 0
	v_mov_b64_e32 v[8:9], 0
	v_mov_b64_e32 v[10:11], 0
	v_mov_b64_e32 v[12:13], 0
	v_mov_b64_e32 v[14:15], 0
	v_mov_b64_e32 v[24:25], 0
	v_mov_b64_e32 v[26:27], 0
	v_mov_b64_e32 v[28:29], 0
	v_mov_b64_e32 v[30:31], 0
	v_mov_b64_e32 v[40:41], 0
	v_mov_b64_e32 v[42:43], 0
	v_mov_b64_e32 v[44:45], 0
	v_mov_b64_e32 v[46:47], 0
	s_waitcnt vmcnt(4)
	v_mov_b64_e32 v[56:57], 0
	v_mov_b64_e32 v[58:59], 0
	v_mov_b64_e32 v[60:61], 0
	v_mov_b64_e32 v[62:63], 0
	v_mov_b64_e32 v[64:65], 0
	v_mov_b64_e32 v[66:67], 0
	v_mov_b64_e32 v[68:69], 0
	v_mov_b64_e32 v[70:71], 0
	v_mov_b64_e32 v[80:81], 0
	v_mov_b64_e32 v[82:83], 0
	v_mov_b64_e32 v[84:85], 0
	v_mov_b64_e32 v[86:87], 0
	v_mov_b64_e32 v[96:97], 0
	v_mov_b64_e32 v[98:99], 0
	v_mov_b64_e32 v[100:101], 0
	v_mov_b64_e32 v[102:103], 0
	v_mov_b64_e32 v[112:113], 0
	v_mov_b64_e32 v[114:115], 0
	v_mov_b64_e32 v[116:117], 0
	v_mov_b64_e32 v[118:119], 0
	v_mov_b64_e32 v[72:73], 0
	v_mov_b32_e32 v74, v0
	v_mov_b32_e32 v75, v0
	v_mov_b32_e32 v76, v0
	v_mov_b32_e32 v77, v0
	v_mov_b32_e32 v78, v0
	v_mov_b32_e32 v79, v0
	v_mov_b32_e32 v88, v0
	v_mov_b32_e32 v89, v0
	v_mov_b32_e32 v90, v0
	v_mov_b32_e32 v91, v0
	v_mov_b32_e32 v92, v0
	v_mov_b32_e32 v93, v0
	v_mov_b32_e32 v94, v0
	v_mov_b32_e32 v95, v0
	v_mov_b32_e32 v104, v0
	v_mov_b32_e32 v105, v0
	v_mov_b32_e32 v106, v0
	v_mov_b32_e32 v107, v0
	v_mov_b32_e32 v108, v0
	v_mov_b32_e32 v109, v0
	v_mov_b32_e32 v110, v0
	v_mov_b32_e32 v111, v0
	v_mov_b32_e32 v120, v0
	v_mov_b32_e32 v121, v0
	v_mov_b32_e32 v122, v0
	v_mov_b32_e32 v123, v0
	v_mov_b32_e32 v124, v0
	v_mov_b32_e32 v125, v0
	v_mov_b32_e32 v126, v0
	v_mov_b32_e32 v127, v0

; __global__ void __launch_bounds__(512, 2) fwd_kernel(Params p) {
;     extern __shared__ __attribute__((aligned(16))) unsigned char lds_raw[];
	.amdhsa_kernel _Z10fwd_kernel6Params
		.amdhsa_group_segment_fixed_size 0
		.amdhsa_private_segment_fixed_size 0
		.amdhsa_kernarg_size 456
		.amdhsa_user_sgpr_count 2
		.amdhsa_user_sgpr_dispatch_ptr 0
		.amdhsa_user_sgpr_queue_ptr 0
		.amdhsa_user_sgpr_kernarg_segment_ptr 1
		.amdhsa_user_sgpr_dispatch_id 0
		.amdhsa_user_sgpr_kernarg_preload_length 0
		.amdhsa_user_sgpr_kernarg_preload_offset 0
		.amdhsa_user_sgpr_private_segment_size 0
		.amdhsa_uses_dynamic_stack 0
		.amdhsa_enable_private_segment 0
		.amdhsa_system_sgpr_workgroup_id_x 1
		.amdhsa_system_sgpr_workgroup_id_y 0
		.amdhsa_system_sgpr_workgroup_id_z 0
		.amdhsa_system_sgpr_workgroup_info 0
		.amdhsa_system_vgpr_workitem_id 0
		.amdhsa_next_free_vgpr 256
		.amdhsa_next_free_sgpr 98
		.amdhsa_accum_offset 256
		.amdhsa_reserve_vcc 1
		.amdhsa_float_round_mode_32 0
		.amdhsa_float_round_mode_16_64 0
		.amdhsa_float_denorm_mode_32 3
		.amdhsa_float_denorm_mode_16_64 3
		.amdhsa_dx10_clamp 1
		.amdhsa_ieee_mode 1
		.amdhsa_fp16_overflow 0
		.amdhsa_tg_split 0
		.amdhsa_exception_fp_ieee_invalid_op 0
		.amdhsa_exception_fp_denorm_src 0
		.amdhsa_exception_fp_ieee_div_zero 0
		.amdhsa_exception_fp_ieee_overflow 0
		.amdhsa_exception_fp_ieee_underflow 0
		.amdhsa_exception_fp_ieee_inexact 0
		.amdhsa_exception_int_div_zero 0
	.end_amdhsa_kernel

; __global__ void __launch_bounds__(512, 2) fwd_kernel(Params p) {
;     extern __shared__ __attribute__((aligned(16))) unsigned char lds_raw[];
amdhsa.kernels:
  - .agpr_count:     0
    .args:
      - .offset:         0
        .size:           200
        .value_kind:     by_value
      - .offset:         200
        .size:           4
        .value_kind:     hidden_block_count_x
      - .offset:         204
        .size:           4
        .value_kind:     hidden_block_count_y
      - .offset:         208
        .size:           4
        .value_kind:     hidden_block_count_z
      - .offset:         212
        .size:           2
        .value_kind:     hidden_group_size_x
      - .offset:         214
        .size:           2
        .value_kind:     hidden_group_size_y
      - .offset:         216
        .size:           2
        .value_kind:     hidden_group_size_z
      - .offset:         218
        .size:           2
        .value_kind:     hidden_remainder_x
      - .offset:         220
        .size:           2
        .value_kind:     hidden_remainder_y
      - .offset:         222
        .size:           2
        .value_kind:     hidden_remainder_z
      - .offset:         240
        .size:           8
        .value_kind:     hidden_global_offset_x
      - .offset:         248
        .size:           8
        .value_kind:     hidden_global_offset_y
      - .offset:         256
        .size:           8
        .value_kind:     hidden_global_offset_z
      - .offset:         264
        .size:           2
        .value_kind:     hidden_grid_dims
      - .offset:         320
        .size:           4
        .value_kind:     hidden_dynamic_lds_size
    .group_segment_fixed_size: 0
    .kernarg_segment_align: 8
    .kernarg_segment_size: 456
    .language:       OpenCL C
    .language_version:
      - 2
      - 0
    .max_flat_workgroup_size: 512
    .name:           _Z10fwd_kernel6Params
    .private_segment_fixed_size: 0
    .sgpr_count:     104
    .sgpr_spill_count: 46
    .symbol:         _Z10fwd_kernel6Params.kd
    .uniform_work_group_size: 1
    .uses_dynamic_stack: false
    .vgpr_count:     256
    .vgpr_spill_count: 0
    .wavefront_size: 64
